# GEMM K-loops: the two waits before each barrier merged into one s_waitcnt and the redundant lgkmcnt(0) after the barrier removed (60+60 sites)
# baseline (speedup 1.0000x reference)
.Lnobar_e1o:
.LBB0_417:
	s_add_u32 s28, s6, 0xfffc0080
	s_addc_u32 s29, s7, -1
	s_add_i32 s43, 0, 0x10000
	s_cmp_eq_u32 s42, 12
	s_cselect_b32 s31, s5, s29
	s_cselect_b32 s30, s8, s28
	s_cselect_b32 s29, s9, s33
	s_cselect_b32 s28, s21, s23
	s_add_i32 s63, 0, 0x14000
	v_add_u32_e32 v142, s43, v186
	v_add_u32_e32 v168, s63, v186
	ds_read_b128 v[130:133], v142
	ds_read_b128 v[134:137], v142 offset:1024
	ds_read_b128 v[138:141], v142 offset:2048
	ds_read_b128 v[142:145], v142 offset:3072
	ds_read_b128 v[146:149], v168
	ds_read_b128 v[150:153], v168 offset:1024
	ds_read_b128 v[154:157], v168 offset:2048
	ds_read_b128 v[168:171], v168 offset:3072
	v_lshl_add_u64 v[216:217], s[6:7], 0, v[166:167]
	s_add_i32 m0, s45, 0xc000
	ds_read_b128 v[172:175], v188
	ds_read_b128 v[176:179], v188 offset:1024
	ds_read_b128 v[180:183], v188 offset:2048
	ds_read_b128 v[190:193], v188 offset:3072
	ds_read_b128 v[194:197], v188 offset:4096
	ds_read_b128 v[198:201], v188 offset:5120
	ds_read_b128 v[202:205], v188 offset:6144
	ds_read_b128 v[206:209], v188 offset:7168
	global_load_lds_dwordx4 v[216:217], off
	s_add_i32 m0, s45, 0xe000
	v_lshl_add_u64 v[216:217], s[6:7], 0, v[164:165]
	global_load_lds_dwordx4 v[216:217], off
	s_waitcnt vmcnt(8) lgkmcnt(0)
	s_barrier
	s_setprio 1
	v_mfma_f32_16x16x32_bf16 v[126:129], v[130:133], v[172:175], v[126:129]
	v_mfma_f32_16x16x32_bf16 v[122:125], v[138:141], v[172:175], v[122:125]
	v_mfma_f32_16x16x32_bf16 v[114:117], v[130:133], v[180:183], v[114:117]
	v_mfma_f32_16x16x32_bf16 v[106:109], v[138:141], v[180:183], v[106:109]
	v_mfma_f32_16x16x32_bf16 v[98:101], v[130:133], v[194:197], v[98:101]
	v_mfma_f32_16x16x32_bf16 v[90:93], v[138:141], v[194:197], v[90:93]
	v_mfma_f32_16x16x32_bf16 v[82:85], v[130:133], v[202:205], v[82:85]
	v_mfma_f32_16x16x32_bf16 v[74:77], v[138:141], v[202:205], v[74:77]
	v_mfma_f32_16x16x32_bf16 v[126:129], v[134:137], v[176:179], v[126:129]
	v_mfma_f32_16x16x32_bf16 v[122:125], v[142:145], v[176:179], v[122:125]
	v_mfma_f32_16x16x32_bf16 v[114:117], v[134:137], v[190:193], v[114:117]
	v_mfma_f32_16x16x32_bf16 v[106:109], v[142:145], v[190:193], v[106:109]
	v_mfma_f32_16x16x32_bf16 v[98:101], v[134:137], v[198:201], v[98:101]
	v_mfma_f32_16x16x32_bf16 v[90:93], v[142:145], v[198:201], v[90:93]
	v_mfma_f32_16x16x32_bf16 v[82:85], v[134:137], v[206:209], v[82:85]
	v_mfma_f32_16x16x32_bf16 v[74:77], v[142:145], v[206:209], v[74:77]
	s_setprio 0
	s_setprio 1
	v_mfma_f32_16x16x32_bf16 v[118:121], v[146:149], v[172:175], v[118:121]
	v_mfma_f32_16x16x32_bf16 v[110:113], v[154:157], v[172:175], v[110:113]
	v_mfma_f32_16x16x32_bf16 v[102:105], v[146:149], v[180:183], v[102:105]
	v_mfma_f32_16x16x32_bf16 v[94:97], v[154:157], v[180:183], v[94:97]
	v_mfma_f32_16x16x32_bf16 v[86:89], v[146:149], v[194:197], v[86:89]
	v_mfma_f32_16x16x32_bf16 v[78:81], v[154:157], v[194:197], v[78:81]
	v_mfma_f32_16x16x32_bf16 v[70:73], v[146:149], v[202:205], v[70:73]
	v_mfma_f32_16x16x32_bf16 v[66:69], v[154:157], v[202:205], v[66:69]
	v_mfma_f32_16x16x32_bf16 v[118:121], v[150:153], v[176:179], v[118:121]
	v_mfma_f32_16x16x32_bf16 v[110:113], v[168:171], v[176:179], v[110:113]
	v_mfma_f32_16x16x32_bf16 v[102:105], v[150:153], v[190:193], v[102:105]
	v_mfma_f32_16x16x32_bf16 v[94:97], v[168:171], v[190:193], v[94:97]
	v_mfma_f32_16x16x32_bf16 v[86:89], v[150:153], v[198:201], v[86:89]
	v_mfma_f32_16x16x32_bf16 v[78:81], v[168:171], v[198:201], v[78:81]
	v_mfma_f32_16x16x32_bf16 v[70:73], v[150:153], v[206:209], v[70:73]
	v_mfma_f32_16x16x32_bf16 v[66:69], v[168:171], v[206:209], v[66:69]
	s_setprio 0
	s_barrier
	s_add_i32 s43, s43, s44
	v_lshl_add_u64 v[216:217], s[28:29], 0, v[0:1]
	s_mov_b32 m0, s43
	ds_read_b128 v[172:175], v188 offset:16384
	ds_read_b128 v[176:179], v188 offset:17408
	ds_read_b128 v[180:183], v188 offset:18432
	ds_read_b128 v[190:193], v188 offset:19456
	ds_read_b128 v[194:197], v188 offset:20480
	ds_read_b128 v[198:201], v188 offset:21504
	ds_read_b128 v[202:205], v188 offset:22528
	ds_read_b128 v[206:209], v188 offset:23552
	global_load_lds_dwordx4 v[216:217], off
	s_add_i32 m0, s43, 0x2000
	s_add_u32 s58, s28, 0x40000
	v_lshl_add_u64 v[218:219], s[28:29], 0, v[158:159]
	s_addc_u32 s59, s29, 0
	s_add_i32 s43, s63, s44
	global_load_lds_dwordx4 v[218:219], off
	v_lshl_add_u64 v[220:221], s[58:59], 0, v[0:1]
	s_mov_b32 m0, s43
	v_lshl_add_u64 v[222:223], s[30:31], 0, v[160:161]
	global_load_lds_dwordx4 v[220:221], off
	s_add_i32 m0, s43, 0x2000
	v_lshl_add_u64 v[220:221], s[58:59], 0, v[158:159]
	global_load_lds_dwordx4 v[220:221], off
	s_mov_b32 m0, s45
	v_lshl_add_u64 v[220:221], s[30:31], 0, v[162:163]
	global_load_lds_dwordx4 v[220:221], off
	s_mov_b32 m0, s46
	s_nop 0
	global_load_lds_dwordx4 v[222:223], off
	s_waitcnt vmcnt(8) lgkmcnt(0)
	s_barrier
	s_setprio 1
	v_mfma_f32_16x16x32_bf16 v[62:65], v[130:133], v[172:175], v[62:65]
	v_mfma_f32_16x16x32_bf16 v[58:61], v[138:141], v[172:175], v[58:61]
	v_mfma_f32_16x16x32_bf16 v[50:53], v[130:133], v[180:183], v[50:53]
	v_mfma_f32_16x16x32_bf16 v[42:45], v[138:141], v[180:183], v[42:45]
	v_mfma_f32_16x16x32_bf16 v[34:37], v[130:133], v[194:197], v[34:37]
	v_mfma_f32_16x16x32_bf16 v[26:29], v[138:141], v[194:197], v[26:29]
	v_mfma_f32_16x16x32_bf16 v[18:21], v[130:133], v[202:205], v[18:21]
	v_mfma_f32_16x16x32_bf16 v[10:13], v[138:141], v[202:205], v[10:13]
	v_mfma_f32_16x16x32_bf16 v[62:65], v[134:137], v[176:179], v[62:65]
	v_mfma_f32_16x16x32_bf16 v[58:61], v[142:145], v[176:179], v[58:61]
	v_mfma_f32_16x16x32_bf16 v[50:53], v[134:137], v[190:193], v[50:53]
	v_mfma_f32_16x16x32_bf16 v[42:45], v[142:145], v[190:193], v[42:45]
	v_mfma_f32_16x16x32_bf16 v[34:37], v[134:137], v[198:201], v[34:37]
	v_mfma_f32_16x16x32_bf16 v[26:29], v[142:145], v[198:201], v[26:29]
	v_mfma_f32_16x16x32_bf16 v[18:21], v[134:137], v[206:209], v[18:21]
	v_mfma_f32_16x16x32_bf16 v[10:13], v[142:145], v[206:209], v[10:13]
	s_setprio 0
	s_setprio 1
	v_mfma_f32_16x16x32_bf16 v[54:57], v[146:149], v[172:175], v[54:57]
	v_mfma_f32_16x16x32_bf16 v[46:49], v[154:157], v[172:175], v[46:49]
	v_mfma_f32_16x16x32_bf16 v[38:41], v[146:149], v[180:183], v[38:41]
	v_mfma_f32_16x16x32_bf16 v[30:33], v[154:157], v[180:183], v[30:33]
	v_mfma_f32_16x16x32_bf16 v[22:25], v[146:149], v[194:197], v[22:25]
	v_mfma_f32_16x16x32_bf16 v[14:17], v[154:157], v[194:197], v[14:17]
	v_mfma_f32_16x16x32_bf16 v[6:9], v[146:149], v[202:205], v[6:9]
	v_mfma_f32_16x16x32_bf16 v[2:5], v[154:157], v[202:205], v[2:5]
	v_mfma_f32_16x16x32_bf16 v[54:57], v[150:153], v[176:179], v[54:57]
	v_mfma_f32_16x16x32_bf16 v[46:49], v[168:171], v[176:179], v[46:49]
	v_mfma_f32_16x16x32_bf16 v[38:41], v[150:153], v[190:193], v[38:41]
	v_mfma_f32_16x16x32_bf16 v[30:33], v[168:171], v[190:193], v[30:33]
	v_mfma_f32_16x16x32_bf16 v[22:25], v[150:153], v[198:201], v[22:25]
	v_mfma_f32_16x16x32_bf16 v[14:17], v[168:171], v[198:201], v[14:17]
	v_mfma_f32_16x16x32_bf16 v[6:9], v[150:153], v[206:209], v[6:9]
	v_mfma_f32_16x16x32_bf16 v[2:5], v[168:171], v[206:209], v[2:5]
	s_setprio 0
	s_barrier
	s_add_i32 s43, 0, 0x18000
	s_add_i32 s58, 0, 0x1c000
	v_add_u32_e32 v142, s43, v186
	v_add_u32_e32 v168, s58, v186
	ds_read_b128 v[130:133], v142
	ds_read_b128 v[134:137], v142 offset:1024
	ds_read_b128 v[138:141], v142 offset:2048
	ds_read_b128 v[142:145], v142 offset:3072
	ds_read_b128 v[146:149], v168
	ds_read_b128 v[150:153], v168 offset:1024
	ds_read_b128 v[154:157], v168 offset:2048
	ds_read_b128 v[168:171], v168 offset:3072
	s_add_u32 s30, s30, 0x40000
	s_addc_u32 s31, s31, 0
	s_mov_b32 m0, s47
	v_lshl_add_u64 v[224:225], s[30:31], 0, v[162:163]
	ds_read_b128 v[172:175], v188 offset:32768
	ds_read_b128 v[176:179], v188 offset:33792
	ds_read_b128 v[180:183], v188 offset:34816
	ds_read_b128 v[190:193], v188 offset:35840
	ds_read_b128 v[194:197], v188 offset:36864
	ds_read_b128 v[198:201], v188 offset:37888
	ds_read_b128 v[202:205], v188 offset:38912
	ds_read_b128 v[206:209], v188 offset:39936
	global_load_lds_dwordx4 v[224:225], off
	s_mov_b32 m0, s48
	v_lshl_add_u64 v[224:225], s[30:31], 0, v[160:161]
	global_load_lds_dwordx4 v[224:225], off
	s_waitcnt vmcnt(8) lgkmcnt(0)
	s_barrier
	s_setprio 1
	v_mfma_f32_16x16x32_bf16 v[126:129], v[130:133], v[172:175], v[126:129]
	v_mfma_f32_16x16x32_bf16 v[122:125], v[138:141], v[172:175], v[122:125]
	v_mfma_f32_16x16x32_bf16 v[114:117], v[130:133], v[180:183], v[114:117]
	v_mfma_f32_16x16x32_bf16 v[106:109], v[138:141], v[180:183], v[106:109]
	v_mfma_f32_16x16x32_bf16 v[98:101], v[130:133], v[194:197], v[98:101]
	v_mfma_f32_16x16x32_bf16 v[90:93], v[138:141], v[194:197], v[90:93]
	v_mfma_f32_16x16x32_bf16 v[82:85], v[130:133], v[202:205], v[82:85]
	v_mfma_f32_16x16x32_bf16 v[74:77], v[138:141], v[202:205], v[74:77]
	v_mfma_f32_16x16x32_bf16 v[126:129], v[134:137], v[176:179], v[126:129]
	v_mfma_f32_16x16x32_bf16 v[122:125], v[142:145], v[176:179], v[122:125]
	v_mfma_f32_16x16x32_bf16 v[114:117], v[134:137], v[190:193], v[114:117]
	v_mfma_f32_16x16x32_bf16 v[106:109], v[142:145], v[190:193], v[106:109]
	v_mfma_f32_16x16x32_bf16 v[98:101], v[134:137], v[198:201], v[98:101]
	v_mfma_f32_16x16x32_bf16 v[90:93], v[142:145], v[198:201], v[90:93]
	v_mfma_f32_16x16x32_bf16 v[82:85], v[134:137], v[206:209], v[82:85]
	v_mfma_f32_16x16x32_bf16 v[74:77], v[142:145], v[206:209], v[74:77]
	s_setprio 0
	s_setprio 1
	v_mfma_f32_16x16x32_bf16 v[118:121], v[146:149], v[172:175], v[118:121]
	v_mfma_f32_16x16x32_bf16 v[110:113], v[154:157], v[172:175], v[110:113]
	v_mfma_f32_16x16x32_bf16 v[102:105], v[146:149], v[180:183], v[102:105]
	v_mfma_f32_16x16x32_bf16 v[94:97], v[154:157], v[180:183], v[94:97]
	v_mfma_f32_16x16x32_bf16 v[86:89], v[146:149], v[194:197], v[86:89]
	v_mfma_f32_16x16x32_bf16 v[78:81], v[154:157], v[194:197], v[78:81]
	v_mfma_f32_16x16x32_bf16 v[70:73], v[146:149], v[202:205], v[70:73]
	v_mfma_f32_16x16x32_bf16 v[66:69], v[154:157], v[202:205], v[66:69]
	v_mfma_f32_16x16x32_bf16 v[118:121], v[150:153], v[176:179], v[118:121]
	v_mfma_f32_16x16x32_bf16 v[110:113], v[168:171], v[176:179], v[110:113]
	v_mfma_f32_16x16x32_bf16 v[102:105], v[150:153], v[190:193], v[102:105]
	v_mfma_f32_16x16x32_bf16 v[94:97], v[168:171], v[190:193], v[94:97]
	v_mfma_f32_16x16x32_bf16 v[86:89], v[150:153], v[198:201], v[86:89]
	v_mfma_f32_16x16x32_bf16 v[78:81], v[168:171], v[198:201], v[78:81]
	v_mfma_f32_16x16x32_bf16 v[70:73], v[150:153], v[206:209], v[70:73]
	v_mfma_f32_16x16x32_bf16 v[66:69], v[168:171], v[206:209], v[66:69]
	s_setprio 0
	s_barrier
	s_add_i32 s30, s43, s44
	v_lshl_add_u64 v[216:217], v[216:217], 0, s[56:57]
	s_mov_b32 m0, s30
	ds_read_b128 v[172:175], v188 offset:49152
	ds_read_b128 v[176:179], v188 offset:50176
	ds_read_b128 v[180:183], v188 offset:51200
	ds_read_b128 v[190:193], v188 offset:52224
	ds_read_b128 v[194:197], v188 offset:53248
	ds_read_b128 v[198:201], v188 offset:54272
	ds_read_b128 v[202:205], v188 offset:55296
	ds_read_b128 v[206:209], v188 offset:56320
	global_load_lds_dwordx4 v[216:217], off
	s_add_i32 m0, s30, 0x2000
	s_add_u32 s28, s28, 0x40080
	v_lshl_add_u64 v[216:217], v[218:219], 0, s[56:57]
	s_addc_u32 s29, s29, 0
	s_add_i32 s30, s58, s44
	global_load_lds_dwordx4 v[216:217], off
	s_mov_b32 m0, s30
	v_lshl_add_u64 v[216:217], s[28:29], 0, v[0:1]
	global_load_lds_dwordx4 v[216:217], off
	s_add_i32 m0, s30, 0x2000
	v_lshl_add_u64 v[216:217], s[28:29], 0, v[158:159]
	global_load_lds_dwordx4 v[216:217], off
	s_mov_b32 m0, s49
	v_lshl_add_u64 v[216:217], v[220:221], 0, s[56:57]
	global_load_lds_dwordx4 v[216:217], off
	s_mov_b32 m0, s52
	v_lshl_add_u64 v[216:217], v[222:223], 0, s[56:57]
	global_load_lds_dwordx4 v[216:217], off
	s_waitcnt vmcnt(8) lgkmcnt(0)
	s_barrier
	s_setprio 1
	v_mfma_f32_16x16x32_bf16 v[62:65], v[130:133], v[172:175], v[62:65]
	v_mfma_f32_16x16x32_bf16 v[58:61], v[138:141], v[172:175], v[58:61]
	v_mfma_f32_16x16x32_bf16 v[50:53], v[130:133], v[180:183], v[50:53]
	v_mfma_f32_16x16x32_bf16 v[42:45], v[138:141], v[180:183], v[42:45]
	v_mfma_f32_16x16x32_bf16 v[34:37], v[130:133], v[194:197], v[34:37]
	v_mfma_f32_16x16x32_bf16 v[26:29], v[138:141], v[194:197], v[26:29]
	v_mfma_f32_16x16x32_bf16 v[18:21], v[130:133], v[202:205], v[18:21]
	v_mfma_f32_16x16x32_bf16 v[10:13], v[138:141], v[202:205], v[10:13]
	v_mfma_f32_16x16x32_bf16 v[62:65], v[134:137], v[176:179], v[62:65]
	v_mfma_f32_16x16x32_bf16 v[58:61], v[142:145], v[176:179], v[58:61]
	v_mfma_f32_16x16x32_bf16 v[50:53], v[134:137], v[190:193], v[50:53]
	v_mfma_f32_16x16x32_bf16 v[42:45], v[142:145], v[190:193], v[42:45]
	v_mfma_f32_16x16x32_bf16 v[34:37], v[134:137], v[198:201], v[34:37]
	v_mfma_f32_16x16x32_bf16 v[26:29], v[142:145], v[198:201], v[26:29]
	v_mfma_f32_16x16x32_bf16 v[18:21], v[134:137], v[206:209], v[18:21]
	v_mfma_f32_16x16x32_bf16 v[10:13], v[142:145], v[206:209], v[10:13]
	s_setprio 0
	s_setprio 1
	v_mfma_f32_16x16x32_bf16 v[54:57], v[146:149], v[172:175], v[54:57]
	v_mfma_f32_16x16x32_bf16 v[46:49], v[154:157], v[172:175], v[46:49]
	v_mfma_f32_16x16x32_bf16 v[38:41], v[146:149], v[180:183], v[38:41]
	v_mfma_f32_16x16x32_bf16 v[30:33], v[154:157], v[180:183], v[30:33]
	v_mfma_f32_16x16x32_bf16 v[22:25], v[146:149], v[194:197], v[22:25]
	v_mfma_f32_16x16x32_bf16 v[14:17], v[154:157], v[194:197], v[14:17]
	v_mfma_f32_16x16x32_bf16 v[6:9], v[146:149], v[202:205], v[6:9]
	v_mfma_f32_16x16x32_bf16 v[2:5], v[154:157], v[202:205], v[2:5]
	v_mfma_f32_16x16x32_bf16 v[54:57], v[150:153], v[176:179], v[54:57]
	v_mfma_f32_16x16x32_bf16 v[46:49], v[168:171], v[176:179], v[46:49]
	v_mfma_f32_16x16x32_bf16 v[38:41], v[150:153], v[190:193], v[38:41]
	v_mfma_f32_16x16x32_bf16 v[30:33], v[168:171], v[190:193], v[30:33]
	v_mfma_f32_16x16x32_bf16 v[22:25], v[150:153], v[198:201], v[22:25]
	v_mfma_f32_16x16x32_bf16 v[14:17], v[168:171], v[198:201], v[14:17]
	v_mfma_f32_16x16x32_bf16 v[6:9], v[150:153], v[206:209], v[6:9]
	v_mfma_f32_16x16x32_bf16 v[2:5], v[168:171], v[206:209], v[2:5]
	s_setprio 0
	s_barrier
	s_add_i32 s42, s42, 2
	s_add_u32 s23, s23, 0x100
	s_addc_u32 s33, s33, 0
	s_add_u32 s6, s6, 0x100
	s_addc_u32 s7, s7, 0
	s_cmp_gt_u32 s42, 13
	s_cbranch_scc0 .LBB0_417
	s_and_b64 vcc, exec, s[18:19]
	s_cbranch_vccz .LBB0_420
	s_barrier

.LBB0_587:
	s_add_u32 s18, s34, s62
	s_addc_u32 s19, s35, s63
	s_add_u32 s18, s18, 0x100
	s_addc_u32 s19, s19, 0
	s_add_u32 s70, s8, s62
	s_addc_u32 s71, s9, s63
	s_add_i32 s26, 0, 0x10000
	s_cmpk_eq_i32 s62, 0x700
	s_cselect_b32 s77, s47, s19
	s_cselect_b32 s76, s59, s18
	s_cselect_b32 s71, s37, s71
	s_cselect_b32 s70, vcc_lo, s70
	s_add_i32 s27, 0, 0x14000
	v_add_u32_e32 v158, s26, v144
	v_add_u32_e32 v176, s27, v144
	ds_read_b128 v[146:149], v158
	ds_read_b128 v[150:153], v158 offset:1024
	ds_read_b128 v[154:157], v158 offset:2048
	ds_read_b128 v[158:161], v158 offset:3072
	ds_read_b128 v[162:165], v176
	ds_read_b128 v[168:171], v176 offset:1024
	ds_read_b128 v[172:175], v176 offset:2048
	ds_read_b128 v[176:179], v176 offset:3072
	v_lshl_add_u64 v[208:209], v[142:143], 0, s[62:63]
	s_add_i32 m0, s4, 0xc000
	ds_read_b128 v[180:183], v145
	ds_read_b128 v[184:187], v145 offset:1024
	ds_read_b128 v[188:191], v145 offset:2048
	ds_read_b128 v[192:195], v145 offset:3072
	ds_read_b128 v[196:199], v145 offset:4096
	ds_read_b128 v[200:203], v145 offset:5120
	ds_read_b128 v[204:207], v145 offset:6144
	ds_read_b128 v[216:219], v145 offset:7168
	global_load_lds_dwordx4 v[208:209], off
	s_add_i32 m0, s4, 0xe000
	v_lshl_add_u64 v[208:209], v[140:141], 0, s[62:63]
	global_load_lds_dwordx4 v[208:209], off
	s_waitcnt vmcnt(8) lgkmcnt(0)
	s_barrier
	s_setprio 1
	v_mfma_f32_16x16x32_bf16 v[134:137], v[146:149], v[180:183], v[134:137]
	v_mfma_f32_16x16x32_bf16 v[130:133], v[154:157], v[180:183], v[130:133]
	v_mfma_f32_16x16x32_bf16 v[110:113], v[146:149], v[188:191], v[110:113]
	v_mfma_f32_16x16x32_bf16 v[106:109], v[154:157], v[188:191], v[106:109]
	v_mfma_f32_16x16x32_bf16 v[94:97], v[146:149], v[196:199], v[94:97]
	v_mfma_f32_16x16x32_bf16 v[90:93], v[154:157], v[196:199], v[90:93]
	v_mfma_f32_16x16x32_bf16 v[78:81], v[146:149], v[204:207], v[78:81]
	v_mfma_f32_16x16x32_bf16 v[74:77], v[154:157], v[204:207], v[74:77]
	v_mfma_f32_16x16x32_bf16 v[134:137], v[150:153], v[184:187], v[134:137]
	v_mfma_f32_16x16x32_bf16 v[130:133], v[158:161], v[184:187], v[130:133]
	v_mfma_f32_16x16x32_bf16 v[110:113], v[150:153], v[192:195], v[110:113]
	v_mfma_f32_16x16x32_bf16 v[106:109], v[158:161], v[192:195], v[106:109]
	v_mfma_f32_16x16x32_bf16 v[94:97], v[150:153], v[200:203], v[94:97]
	v_mfma_f32_16x16x32_bf16 v[90:93], v[158:161], v[200:203], v[90:93]
	v_mfma_f32_16x16x32_bf16 v[78:81], v[150:153], v[216:219], v[78:81]
	v_mfma_f32_16x16x32_bf16 v[74:77], v[158:161], v[216:219], v[74:77]
	s_setprio 0
	s_setprio 1
	v_mfma_f32_16x16x32_bf16 v[122:125], v[162:165], v[180:183], v[122:125]
	v_mfma_f32_16x16x32_bf16 v[114:117], v[172:175], v[180:183], v[114:117]
	v_mfma_f32_16x16x32_bf16 v[102:105], v[162:165], v[188:191], v[102:105]
	v_mfma_f32_16x16x32_bf16 v[98:101], v[172:175], v[188:191], v[98:101]
	v_mfma_f32_16x16x32_bf16 v[86:89], v[162:165], v[196:199], v[86:89]
	v_mfma_f32_16x16x32_bf16 v[82:85], v[172:175], v[196:199], v[82:85]
	v_mfma_f32_16x16x32_bf16 v[70:73], v[162:165], v[204:207], v[70:73]
	v_mfma_f32_16x16x32_bf16 v[66:69], v[172:175], v[204:207], v[66:69]
	v_mfma_f32_16x16x32_bf16 v[122:125], v[168:171], v[184:187], v[122:125]
	v_mfma_f32_16x16x32_bf16 v[114:117], v[176:179], v[184:187], v[114:117]
	v_mfma_f32_16x16x32_bf16 v[102:105], v[168:171], v[192:195], v[102:105]
	v_mfma_f32_16x16x32_bf16 v[98:101], v[176:179], v[192:195], v[98:101]
	v_mfma_f32_16x16x32_bf16 v[86:89], v[168:171], v[200:203], v[86:89]
	v_mfma_f32_16x16x32_bf16 v[82:85], v[176:179], v[200:203], v[82:85]
	v_mfma_f32_16x16x32_bf16 v[70:73], v[168:171], v[216:219], v[70:73]
	v_mfma_f32_16x16x32_bf16 v[66:69], v[176:179], v[216:219], v[66:69]
	s_setprio 0
	s_barrier
	s_add_i32 s18, s26, s84
	v_lshl_add_u64 v[208:209], s[70:71], 0, v[0:1]
	s_mov_b32 m0, s18
	ds_read_b128 v[180:183], v145 offset:16384
	ds_read_b128 v[184:187], v145 offset:17408
	ds_read_b128 v[188:191], v145 offset:18432
	ds_read_b128 v[192:195], v145 offset:19456
	ds_read_b128 v[196:199], v145 offset:20480
	ds_read_b128 v[200:203], v145 offset:21504
	ds_read_b128 v[204:207], v145 offset:22528
	ds_read_b128 v[216:219], v145 offset:23552
	global_load_lds_dwordx4 v[208:209], off
	s_add_i32 m0, s18, 0x2000
	s_add_u32 s18, s70, 0x40000
	v_lshl_add_u64 v[220:221], s[70:71], 0, v[118:119]
	s_addc_u32 s19, s71, 0
	s_add_i32 s26, s27, s84
	global_load_lds_dwordx4 v[220:221], off
	v_lshl_add_u64 v[222:223], s[18:19], 0, v[0:1]
	s_mov_b32 m0, s26
	v_lshl_add_u64 v[224:225], s[76:77], 0, v[120:121]
	global_load_lds_dwordx4 v[222:223], off
	s_add_i32 m0, s26, 0x2000
	v_lshl_add_u64 v[222:223], s[18:19], 0, v[118:119]
	global_load_lds_dwordx4 v[222:223], off
	s_mov_b32 m0, s4
	v_lshl_add_u64 v[222:223], s[76:77], 0, v[126:127]
	global_load_lds_dwordx4 v[222:223], off
	s_mov_b32 m0, s5
	s_nop 0
	global_load_lds_dwordx4 v[224:225], off
	s_waitcnt vmcnt(8) lgkmcnt(0)
	s_barrier
	s_setprio 1
	v_mfma_f32_16x16x32_bf16 v[62:65], v[146:149], v[180:183], v[62:65]
	v_mfma_f32_16x16x32_bf16 v[58:61], v[154:157], v[180:183], v[58:61]
	v_mfma_f32_16x16x32_bf16 v[46:49], v[146:149], v[188:191], v[46:49]
	v_mfma_f32_16x16x32_bf16 v[42:45], v[154:157], v[188:191], v[42:45]
	v_mfma_f32_16x16x32_bf16 v[30:33], v[146:149], v[196:199], v[30:33]
	v_mfma_f32_16x16x32_bf16 v[26:29], v[154:157], v[196:199], v[26:29]
	v_mfma_f32_16x16x32_bf16 v[14:17], v[146:149], v[204:207], v[14:17]
	v_mfma_f32_16x16x32_bf16 v[10:13], v[154:157], v[204:207], v[10:13]
	v_mfma_f32_16x16x32_bf16 v[62:65], v[150:153], v[184:187], v[62:65]
	v_mfma_f32_16x16x32_bf16 v[58:61], v[158:161], v[184:187], v[58:61]
	v_mfma_f32_16x16x32_bf16 v[46:49], v[150:153], v[192:195], v[46:49]
	v_mfma_f32_16x16x32_bf16 v[42:45], v[158:161], v[192:195], v[42:45]
	v_mfma_f32_16x16x32_bf16 v[30:33], v[150:153], v[200:203], v[30:33]
	v_mfma_f32_16x16x32_bf16 v[26:29], v[158:161], v[200:203], v[26:29]
	v_mfma_f32_16x16x32_bf16 v[14:17], v[150:153], v[216:219], v[14:17]
	v_mfma_f32_16x16x32_bf16 v[10:13], v[158:161], v[216:219], v[10:13]
	s_setprio 0
	s_setprio 1
	v_mfma_f32_16x16x32_bf16 v[54:57], v[162:165], v[180:183], v[54:57]
	v_mfma_f32_16x16x32_bf16 v[50:53], v[172:175], v[180:183], v[50:53]
	v_mfma_f32_16x16x32_bf16 v[38:41], v[162:165], v[188:191], v[38:41]
	v_mfma_f32_16x16x32_bf16 v[34:37], v[172:175], v[188:191], v[34:37]
	v_mfma_f32_16x16x32_bf16 v[22:25], v[162:165], v[196:199], v[22:25]
	v_mfma_f32_16x16x32_bf16 v[18:21], v[172:175], v[196:199], v[18:21]
	v_mfma_f32_16x16x32_bf16 v[6:9], v[162:165], v[204:207], v[6:9]
	v_mfma_f32_16x16x32_bf16 v[2:5], v[172:175], v[204:207], v[2:5]
	v_mfma_f32_16x16x32_bf16 v[54:57], v[168:171], v[184:187], v[54:57]
	v_mfma_f32_16x16x32_bf16 v[50:53], v[176:179], v[184:187], v[50:53]
	v_mfma_f32_16x16x32_bf16 v[38:41], v[168:171], v[192:195], v[38:41]
	v_mfma_f32_16x16x32_bf16 v[34:37], v[176:179], v[192:195], v[34:37]
	v_mfma_f32_16x16x32_bf16 v[22:25], v[168:171], v[200:203], v[22:25]
	v_mfma_f32_16x16x32_bf16 v[18:21], v[176:179], v[200:203], v[18:21]
	v_mfma_f32_16x16x32_bf16 v[6:9], v[168:171], v[216:219], v[6:9]
	v_mfma_f32_16x16x32_bf16 v[2:5], v[176:179], v[216:219], v[2:5]
	s_setprio 0
	s_barrier
	s_add_i32 s26, 0, 0x18000
	s_add_i32 s27, 0, 0x1c000
	v_add_u32_e32 v158, s26, v144
	v_add_u32_e32 v176, s27, v144
	ds_read_b128 v[146:149], v158
	ds_read_b128 v[150:153], v158 offset:1024
	ds_read_b128 v[154:157], v158 offset:2048
	ds_read_b128 v[158:161], v158 offset:3072
	ds_read_b128 v[162:165], v176
	ds_read_b128 v[168:171], v176 offset:1024
	ds_read_b128 v[172:175], v176 offset:2048
	ds_read_b128 v[176:179], v176 offset:3072
	s_add_u32 s18, s76, 0x40000
	s_addc_u32 s19, s77, 0
	s_mov_b32 m0, s33
	v_lshl_add_u64 v[242:243], s[18:19], 0, v[126:127]
	ds_read_b128 v[180:183], v145 offset:32768
	ds_read_b128 v[184:187], v145 offset:33792
	ds_read_b128 v[188:191], v145 offset:34816
	ds_read_b128 v[192:195], v145 offset:35840
	ds_read_b128 v[196:199], v145 offset:36864
	ds_read_b128 v[200:203], v145 offset:37888
	ds_read_b128 v[204:207], v145 offset:38912
	ds_read_b128 v[216:219], v145 offset:39936
	global_load_lds_dwordx4 v[242:243], off
	s_mov_b32 m0, s92
	v_lshl_add_u64 v[242:243], s[18:19], 0, v[120:121]
	global_load_lds_dwordx4 v[242:243], off
	s_waitcnt vmcnt(8) lgkmcnt(0)
	s_barrier
	s_setprio 1
	v_mfma_f32_16x16x32_bf16 v[134:137], v[146:149], v[180:183], v[134:137]
	v_mfma_f32_16x16x32_bf16 v[130:133], v[154:157], v[180:183], v[130:133]
	v_mfma_f32_16x16x32_bf16 v[110:113], v[146:149], v[188:191], v[110:113]
	v_mfma_f32_16x16x32_bf16 v[106:109], v[154:157], v[188:191], v[106:109]
	v_mfma_f32_16x16x32_bf16 v[94:97], v[146:149], v[196:199], v[94:97]
	v_mfma_f32_16x16x32_bf16 v[90:93], v[154:157], v[196:199], v[90:93]
	v_mfma_f32_16x16x32_bf16 v[78:81], v[146:149], v[204:207], v[78:81]
	v_mfma_f32_16x16x32_bf16 v[74:77], v[154:157], v[204:207], v[74:77]
	v_mfma_f32_16x16x32_bf16 v[134:137], v[150:153], v[184:187], v[134:137]
	v_mfma_f32_16x16x32_bf16 v[130:133], v[158:161], v[184:187], v[130:133]
	v_mfma_f32_16x16x32_bf16 v[110:113], v[150:153], v[192:195], v[110:113]
	v_mfma_f32_16x16x32_bf16 v[106:109], v[158:161], v[192:195], v[106:109]
	v_mfma_f32_16x16x32_bf16 v[94:97], v[150:153], v[200:203], v[94:97]
	v_mfma_f32_16x16x32_bf16 v[90:93], v[158:161], v[200:203], v[90:93]
	v_mfma_f32_16x16x32_bf16 v[78:81], v[150:153], v[216:219], v[78:81]
	v_mfma_f32_16x16x32_bf16 v[74:77], v[158:161], v[216:219], v[74:77]
	s_setprio 0
	s_setprio 1
	v_mfma_f32_16x16x32_bf16 v[122:125], v[162:165], v[180:183], v[122:125]
	v_mfma_f32_16x16x32_bf16 v[114:117], v[172:175], v[180:183], v[114:117]
	v_mfma_f32_16x16x32_bf16 v[102:105], v[162:165], v[188:191], v[102:105]
	v_mfma_f32_16x16x32_bf16 v[98:101], v[172:175], v[188:191], v[98:101]
	v_mfma_f32_16x16x32_bf16 v[86:89], v[162:165], v[196:199], v[86:89]
	v_mfma_f32_16x16x32_bf16 v[82:85], v[172:175], v[196:199], v[82:85]
	v_mfma_f32_16x16x32_bf16 v[70:73], v[162:165], v[204:207], v[70:73]
	v_mfma_f32_16x16x32_bf16 v[66:69], v[172:175], v[204:207], v[66:69]
	v_mfma_f32_16x16x32_bf16 v[122:125], v[168:171], v[184:187], v[122:125]
	v_mfma_f32_16x16x32_bf16 v[114:117], v[176:179], v[184:187], v[114:117]
	v_mfma_f32_16x16x32_bf16 v[102:105], v[168:171], v[192:195], v[102:105]
	v_mfma_f32_16x16x32_bf16 v[98:101], v[176:179], v[192:195], v[98:101]
	v_mfma_f32_16x16x32_bf16 v[86:89], v[168:171], v[200:203], v[86:89]
	v_mfma_f32_16x16x32_bf16 v[82:85], v[176:179], v[200:203], v[82:85]
	v_mfma_f32_16x16x32_bf16 v[70:73], v[168:171], v[216:219], v[70:73]
	v_mfma_f32_16x16x32_bf16 v[66:69], v[176:179], v[216:219], v[66:69]
	s_setprio 0
	s_barrier
	s_add_i32 s18, s26, s84
	v_lshl_add_u64 v[208:209], v[208:209], 0, s[56:57]
	s_mov_b32 m0, s18
	ds_read_b128 v[180:183], v145 offset:49152
	ds_read_b128 v[184:187], v145 offset:50176
	ds_read_b128 v[188:191], v145 offset:51200
	ds_read_b128 v[192:195], v145 offset:52224
	ds_read_b128 v[196:199], v145 offset:53248
	ds_read_b128 v[200:203], v145 offset:54272
	ds_read_b128 v[204:207], v145 offset:55296
	ds_read_b128 v[216:219], v145 offset:56320
	global_load_lds_dwordx4 v[208:209], off
	s_add_i32 m0, s18, 0x2000
	s_add_u32 s18, s70, 0x40080
	v_lshl_add_u64 v[208:209], v[220:221], 0, s[56:57]
	s_addc_u32 s19, s71, 0
	s_add_i32 s26, s27, s84
	global_load_lds_dwordx4 v[208:209], off
	s_mov_b32 m0, s26
	v_lshl_add_u64 v[208:209], s[18:19], 0, v[0:1]
	global_load_lds_dwordx4 v[208:209], off
	s_add_i32 m0, s26, 0x2000
	v_lshl_add_u64 v[208:209], s[18:19], 0, v[118:119]
	global_load_lds_dwordx4 v[208:209], off
	s_mov_b32 m0, s90
	v_lshl_add_u64 v[208:209], v[222:223], 0, s[56:57]
	global_load_lds_dwordx4 v[208:209], off
	s_mov_b32 m0, s96
	v_lshl_add_u64 v[208:209], v[224:225], 0, s[56:57]
	global_load_lds_dwordx4 v[208:209], off
	s_waitcnt vmcnt(8) lgkmcnt(0)
	s_barrier
	s_setprio 1
	v_mfma_f32_16x16x32_bf16 v[62:65], v[146:149], v[180:183], v[62:65]
	v_mfma_f32_16x16x32_bf16 v[58:61], v[154:157], v[180:183], v[58:61]
	v_mfma_f32_16x16x32_bf16 v[46:49], v[146:149], v[188:191], v[46:49]
	v_mfma_f32_16x16x32_bf16 v[42:45], v[154:157], v[188:191], v[42:45]
	v_mfma_f32_16x16x32_bf16 v[30:33], v[146:149], v[196:199], v[30:33]
	v_mfma_f32_16x16x32_bf16 v[26:29], v[154:157], v[196:199], v[26:29]
	v_mfma_f32_16x16x32_bf16 v[14:17], v[146:149], v[204:207], v[14:17]
	v_mfma_f32_16x16x32_bf16 v[10:13], v[154:157], v[204:207], v[10:13]
	v_mfma_f32_16x16x32_bf16 v[62:65], v[150:153], v[184:187], v[62:65]
	v_mfma_f32_16x16x32_bf16 v[58:61], v[158:161], v[184:187], v[58:61]
	v_mfma_f32_16x16x32_bf16 v[46:49], v[150:153], v[192:195], v[46:49]
	v_mfma_f32_16x16x32_bf16 v[42:45], v[158:161], v[192:195], v[42:45]
	v_mfma_f32_16x16x32_bf16 v[30:33], v[150:153], v[200:203], v[30:33]
	v_mfma_f32_16x16x32_bf16 v[26:29], v[158:161], v[200:203], v[26:29]
	v_mfma_f32_16x16x32_bf16 v[14:17], v[150:153], v[216:219], v[14:17]
	v_mfma_f32_16x16x32_bf16 v[10:13], v[158:161], v[216:219], v[10:13]
	s_setprio 0
	s_setprio 1
	v_mfma_f32_16x16x32_bf16 v[54:57], v[162:165], v[180:183], v[54:57]
	v_mfma_f32_16x16x32_bf16 v[50:53], v[172:175], v[180:183], v[50:53]
	v_mfma_f32_16x16x32_bf16 v[38:41], v[162:165], v[188:191], v[38:41]
	v_mfma_f32_16x16x32_bf16 v[34:37], v[172:175], v[188:191], v[34:37]
	v_mfma_f32_16x16x32_bf16 v[22:25], v[162:165], v[196:199], v[22:25]
	v_mfma_f32_16x16x32_bf16 v[18:21], v[172:175], v[196:199], v[18:21]
	v_mfma_f32_16x16x32_bf16 v[6:9], v[162:165], v[204:207], v[6:9]
	v_mfma_f32_16x16x32_bf16 v[2:5], v[172:175], v[204:207], v[2:5]
	v_mfma_f32_16x16x32_bf16 v[54:57], v[168:171], v[184:187], v[54:57]
	v_mfma_f32_16x16x32_bf16 v[50:53], v[176:179], v[184:187], v[50:53]
	v_mfma_f32_16x16x32_bf16 v[38:41], v[168:171], v[192:195], v[38:41]
	v_mfma_f32_16x16x32_bf16 v[34:37], v[176:179], v[192:195], v[34:37]
	v_mfma_f32_16x16x32_bf16 v[22:25], v[168:171], v[200:203], v[22:25]
	v_mfma_f32_16x16x32_bf16 v[18:21], v[176:179], v[200:203], v[18:21]
	v_mfma_f32_16x16x32_bf16 v[6:9], v[168:171], v[216:219], v[6:9]
	v_mfma_f32_16x16x32_bf16 v[2:5], v[176:179], v[216:219], v[2:5]
	s_setprio 0
	s_barrier
	s_add_i32 vcc_hi, vcc_hi, 2
	s_add_u32 s62, s62, 0x100
	s_addc_u32 s63, s63, 0
	s_cmp_gt_u32 vcc_hi, 13
	s_cbranch_scc0 .LBB0_587
	s_add_u32 s62, s8, 0xffffff00
	s_addc_u32 s63, s9, -1
	s_andn2_b64 vcc, exec, s[44:45]
	s_cbranch_vccnz .LBB0_590
	v_mov_b32_e32 v2, 0
	s_mov_b32 s20, s36
	s_mov_b32 s83, s46
	s_mov_b64 s[34:35], s[52:53]
	s_mov_b32 s68, s58
	v_mov_b32_e32 v3, v2
	v_mov_b32_e32 v4, v2
	v_mov_b32_e32 v5, v2
	v_mov_b32_e32 v6, v2
	v_mov_b32_e32 v7, v2
	v_mov_b32_e32 v8, v2
	v_mov_b32_e32 v9, v2
	v_mov_b32_e32 v18, v2
	v_mov_b32_e32 v19, v2
	v_mov_b32_e32 v20, v2
	v_mov_b32_e32 v21, v2
	v_mov_b32_e32 v22, v2
	v_mov_b32_e32 v23, v2
	v_mov_b32_e32 v24, v2
	v_mov_b32_e32 v25, v2
	v_mov_b32_e32 v34, v2
	v_mov_b32_e32 v35, v2
	v_mov_b32_e32 v36, v2
	v_mov_b32_e32 v37, v2
	v_mov_b32_e32 v38, v2
	v_mov_b32_e32 v39, v2
	v_mov_b32_e32 v40, v2
	v_mov_b32_e32 v41, v2
	v_mov_b32_e32 v50, v2
	v_mov_b32_e32 v51, v2
	v_mov_b32_e32 v52, v2
	v_mov_b32_e32 v53, v2
	v_mov_b32_e32 v54, v2
	v_mov_b32_e32 v55, v2
	v_mov_b32_e32 v56, v2
	v_mov_b32_e32 v57, v2
	v_mov_b32_e32 v10, v2
	v_mov_b32_e32 v11, v2
	v_mov_b32_e32 v12, v2
	v_mov_b32_e32 v13, v2
	v_mov_b32_e32 v14, v2
	v_mov_b32_e32 v15, v2
	v_mov_b32_e32 v16, v2
	v_mov_b32_e32 v17, v2
	v_mov_b32_e32 v26, v2
	v_mov_b32_e32 v27, v2
	v_mov_b32_e32 v28, v2
	v_mov_b32_e32 v29, v2
	v_mov_b32_e32 v30, v2
	v_mov_b32_e32 v31, v2
	v_mov_b32_e32 v32, v2
	v_mov_b32_e32 v33, v2
	v_mov_b32_e32 v42, v2
	v_mov_b32_e32 v43, v2
	v_mov_b32_e32 v44, v2
	v_mov_b32_e32 v45, v2
	v_mov_b32_e32 v46, v2
	v_mov_b32_e32 v47, v2
	v_mov_b32_e32 v48, v2
	v_mov_b32_e32 v49, v2
	v_mov_b32_e32 v58, v2
	v_mov_b32_e32 v59, v2
	v_mov_b32_e32 v60, v2
	v_mov_b32_e32 v61, v2
	v_mov_b32_e32 v62, v2
	v_mov_b32_e32 v63, v2
	v_mov_b32_e32 v64, v2
	v_mov_b32_e32 v65, v2
	v_mov_b32_e32 v66, v2
	v_mov_b32_e32 v67, v2
	v_mov_b32_e32 v68, v2
	v_mov_b32_e32 v69, v2
	v_mov_b32_e32 v70, v2
	v_mov_b32_e32 v71, v2
	v_mov_b32_e32 v72, v2
	v_mov_b32_e32 v73, v2
	v_mov_b32_e32 v82, v2
	v_mov_b32_e32 v83, v2
	v_mov_b32_e32 v84, v2
	v_mov_b32_e32 v85, v2
	v_mov_b32_e32 v86, v2
	v_mov_b32_e32 v87, v2
	v_mov_b32_e32 v88, v2
	v_mov_b32_e32 v89, v2
	v_mov_b32_e32 v98, v2
	v_mov_b32_e32 v99, v2
	v_mov_b32_e32 v100, v2
	v_mov_b32_e32 v101, v2
	v_mov_b32_e32 v102, v2
	v_mov_b32_e32 v103, v2
	v_mov_b32_e32 v104, v2
	v_mov_b32_e32 v105, v2
	v_mov_b32_e32 v114, v2
	v_mov_b32_e32 v115, v2
	v_mov_b32_e32 v116, v2
	v_mov_b32_e32 v117, v2
	v_mov_b32_e32 v122, v2
	v_mov_b32_e32 v123, v2
	v_mov_b32_e32 v124, v2
	v_mov_b32_e32 v125, v2
	v_mov_b32_e32 v74, v2
	v_mov_b32_e32 v75, v2
	v_mov_b32_e32 v76, v2
	v_mov_b32_e32 v77, v2
	v_mov_b32_e32 v78, v2
	v_mov_b32_e32 v79, v2
	v_mov_b32_e32 v80, v2
	v_mov_b32_e32 v81, v2
	v_mov_b32_e32 v90, v2
	v_mov_b32_e32 v91, v2
	v_mov_b32_e32 v92, v2
	v_mov_b32_e32 v93, v2
	v_mov_b32_e32 v94, v2
	v_mov_b32_e32 v95, v2
	v_mov_b32_e32 v96, v2
	v_mov_b32_e32 v97, v2
	v_mov_b32_e32 v106, v2
	v_mov_b32_e32 v107, v2
	v_mov_b32_e32 v108, v2
	v_mov_b32_e32 v109, v2
	v_mov_b32_e32 v110, v2
	v_mov_b32_e32 v111, v2
	v_mov_b32_e32 v112, v2
	v_mov_b32_e32 v113, v2
	v_mov_b32_e32 v130, v2
	v_mov_b32_e32 v131, v2
	v_mov_b32_e32 v132, v2
	v_mov_b32_e32 v133, v2
	v_mov_b32_e32 v134, v2
	v_mov_b32_e32 v135, v2
	v_mov_b32_e32 v136, v2
	v_mov_b32_e32 v137, v2
	s_andn2_b64 vcc, exec, s[42:43]
	s_cbranch_vccnz .LBB0_591
	s_branch .LBB0_592

.LBB0_684:
	s_add_u32 s52, s30, s48
	s_addc_u32 s53, s31, s49
	s_add_u32 s52, s52, 0x100
	s_addc_u32 s53, s53, 0
	s_add_u32 s95, s8, s48
	s_addc_u32 s96, s9, s49
	s_add_i32 vcc_lo, 0, 0x10000
	s_cmpk_eq_i32 s48, 0x700
	s_cselect_b32 s63, s37, s53
	s_cselect_b32 s62, s59, s52
	s_cselect_b32 s53, s35, s96
	s_cselect_b32 s52, s93, s95
	s_add_i32 s95, 0, 0x14000
	v_add_u32_e32 v158, vcc_lo, v144
	v_add_u32_e32 v167, s95, v144
	ds_read_b128 v[146:149], v158
	ds_read_b128 v[150:153], v158 offset:1024
	ds_read_b128 v[154:157], v158 offset:2048
	ds_read_b128 v[158:161], v158 offset:3072
	ds_read_b128 v[162:165], v167
	ds_read_b128 v[168:171], v167 offset:1024
	ds_read_b128 v[172:175], v167 offset:2048
	ds_read_b128 v[176:179], v167 offset:3072
	v_lshl_add_u64 v[208:209], v[142:143], 0, s[48:49]
	s_add_i32 m0, s4, 0xc000
	ds_read_b128 v[180:183], v145
	ds_read_b128 v[184:187], v145 offset:1024
	ds_read_b128 v[188:191], v145 offset:2048
	ds_read_b128 v[192:195], v145 offset:3072
	ds_read_b128 v[196:199], v145 offset:4096
	ds_read_b128 v[200:203], v145 offset:5120
	ds_read_b128 v[204:207], v145 offset:6144
	ds_read_b128 v[216:219], v145 offset:7168
	global_load_lds_dwordx4 v[208:209], off
	s_add_i32 m0, s4, 0xe000
	v_lshl_add_u64 v[208:209], v[140:141], 0, s[48:49]
	global_load_lds_dwordx4 v[208:209], off
	s_waitcnt vmcnt(8) lgkmcnt(0)
	s_barrier
	s_setprio 1
	v_mfma_f32_16x16x32_bf16 v[134:137], v[146:149], v[180:183], v[134:137]
	v_mfma_f32_16x16x32_bf16 v[130:133], v[154:157], v[180:183], v[130:133]
	v_mfma_f32_16x16x32_bf16 v[110:113], v[146:149], v[188:191], v[110:113]
	v_mfma_f32_16x16x32_bf16 v[106:109], v[154:157], v[188:191], v[106:109]
	v_mfma_f32_16x16x32_bf16 v[94:97], v[146:149], v[196:199], v[94:97]
	v_mfma_f32_16x16x32_bf16 v[90:93], v[154:157], v[196:199], v[90:93]
	v_mfma_f32_16x16x32_bf16 v[78:81], v[146:149], v[204:207], v[78:81]
	v_mfma_f32_16x16x32_bf16 v[74:77], v[154:157], v[204:207], v[74:77]
	v_mfma_f32_16x16x32_bf16 v[134:137], v[150:153], v[184:187], v[134:137]
	v_mfma_f32_16x16x32_bf16 v[130:133], v[158:161], v[184:187], v[130:133]
	v_mfma_f32_16x16x32_bf16 v[110:113], v[150:153], v[192:195], v[110:113]
	v_mfma_f32_16x16x32_bf16 v[106:109], v[158:161], v[192:195], v[106:109]
	v_mfma_f32_16x16x32_bf16 v[94:97], v[150:153], v[200:203], v[94:97]
	v_mfma_f32_16x16x32_bf16 v[90:93], v[158:161], v[200:203], v[90:93]
	v_mfma_f32_16x16x32_bf16 v[78:81], v[150:153], v[216:219], v[78:81]
	v_mfma_f32_16x16x32_bf16 v[74:77], v[158:161], v[216:219], v[74:77]
	s_setprio 0
	s_setprio 1
	v_mfma_f32_16x16x32_bf16 v[122:125], v[162:165], v[180:183], v[122:125]
	v_mfma_f32_16x16x32_bf16 v[114:117], v[172:175], v[180:183], v[114:117]
	v_mfma_f32_16x16x32_bf16 v[102:105], v[162:165], v[188:191], v[102:105]
	v_mfma_f32_16x16x32_bf16 v[98:101], v[172:175], v[188:191], v[98:101]
	v_mfma_f32_16x16x32_bf16 v[86:89], v[162:165], v[196:199], v[86:89]
	v_mfma_f32_16x16x32_bf16 v[82:85], v[172:175], v[196:199], v[82:85]
	v_mfma_f32_16x16x32_bf16 v[70:73], v[162:165], v[204:207], v[70:73]
	v_mfma_f32_16x16x32_bf16 v[66:69], v[172:175], v[204:207], v[66:69]
	v_mfma_f32_16x16x32_bf16 v[122:125], v[168:171], v[184:187], v[122:125]
	v_mfma_f32_16x16x32_bf16 v[114:117], v[176:179], v[184:187], v[114:117]
	v_mfma_f32_16x16x32_bf16 v[102:105], v[168:171], v[192:195], v[102:105]
	v_mfma_f32_16x16x32_bf16 v[98:101], v[176:179], v[192:195], v[98:101]
	v_mfma_f32_16x16x32_bf16 v[86:89], v[168:171], v[200:203], v[86:89]
	v_mfma_f32_16x16x32_bf16 v[82:85], v[176:179], v[200:203], v[82:85]
	v_mfma_f32_16x16x32_bf16 v[70:73], v[168:171], v[216:219], v[70:73]
	v_mfma_f32_16x16x32_bf16 v[66:69], v[176:179], v[216:219], v[66:69]
	s_setprio 0
	s_barrier
	s_add_i32 s96, vcc_lo, s77
	v_lshl_add_u64 v[208:209], s[52:53], 0, v[0:1]
	s_mov_b32 m0, s96
	ds_read_b128 v[180:183], v145 offset:16384
	ds_read_b128 v[184:187], v145 offset:17408
	ds_read_b128 v[188:191], v145 offset:18432
	ds_read_b128 v[192:195], v145 offset:19456
	ds_read_b128 v[196:199], v145 offset:20480
	ds_read_b128 v[200:203], v145 offset:21504
	ds_read_b128 v[204:207], v145 offset:22528
	ds_read_b128 v[216:219], v145 offset:23552
	global_load_lds_dwordx4 v[208:209], off
	s_add_i32 m0, s96, 0x2000
	s_add_u32 vcc_lo, s52, 0x40000
	v_lshl_add_u64 v[220:221], s[52:53], 0, v[118:119]
	s_addc_u32 vcc_hi, s53, 0
	s_add_i32 s95, s95, s77
	global_load_lds_dwordx4 v[220:221], off
	v_lshl_add_u64 v[222:223], vcc, 0, v[0:1]
	s_mov_b32 m0, s95
	v_lshl_add_u64 v[224:225], s[62:63], 0, v[120:121]
	global_load_lds_dwordx4 v[222:223], off
	s_add_i32 m0, s95, 0x2000
	v_lshl_add_u64 v[222:223], vcc, 0, v[118:119]
	global_load_lds_dwordx4 v[222:223], off
	s_mov_b32 m0, s4
	v_lshl_add_u64 v[222:223], s[62:63], 0, v[126:127]
	global_load_lds_dwordx4 v[222:223], off
	s_mov_b32 m0, s5
	s_nop 0
	global_load_lds_dwordx4 v[224:225], off
	s_waitcnt vmcnt(8) lgkmcnt(0)
	s_barrier
	s_setprio 1
	v_mfma_f32_16x16x32_bf16 v[62:65], v[146:149], v[180:183], v[62:65]
	v_mfma_f32_16x16x32_bf16 v[58:61], v[154:157], v[180:183], v[58:61]
	v_mfma_f32_16x16x32_bf16 v[46:49], v[146:149], v[188:191], v[46:49]
	v_mfma_f32_16x16x32_bf16 v[42:45], v[154:157], v[188:191], v[42:45]
	v_mfma_f32_16x16x32_bf16 v[30:33], v[146:149], v[196:199], v[30:33]
	v_mfma_f32_16x16x32_bf16 v[26:29], v[154:157], v[196:199], v[26:29]
	v_mfma_f32_16x16x32_bf16 v[14:17], v[146:149], v[204:207], v[14:17]
	v_mfma_f32_16x16x32_bf16 v[10:13], v[154:157], v[204:207], v[10:13]
	v_mfma_f32_16x16x32_bf16 v[62:65], v[150:153], v[184:187], v[62:65]
	v_mfma_f32_16x16x32_bf16 v[58:61], v[158:161], v[184:187], v[58:61]
	v_mfma_f32_16x16x32_bf16 v[46:49], v[150:153], v[192:195], v[46:49]
	v_mfma_f32_16x16x32_bf16 v[42:45], v[158:161], v[192:195], v[42:45]
	v_mfma_f32_16x16x32_bf16 v[30:33], v[150:153], v[200:203], v[30:33]
	v_mfma_f32_16x16x32_bf16 v[26:29], v[158:161], v[200:203], v[26:29]
	v_mfma_f32_16x16x32_bf16 v[14:17], v[150:153], v[216:219], v[14:17]
	v_mfma_f32_16x16x32_bf16 v[10:13], v[158:161], v[216:219], v[10:13]
	s_setprio 0
	s_setprio 1
	v_mfma_f32_16x16x32_bf16 v[54:57], v[162:165], v[180:183], v[54:57]
	v_mfma_f32_16x16x32_bf16 v[50:53], v[172:175], v[180:183], v[50:53]
	v_mfma_f32_16x16x32_bf16 v[38:41], v[162:165], v[188:191], v[38:41]
	v_mfma_f32_16x16x32_bf16 v[34:37], v[172:175], v[188:191], v[34:37]
	v_mfma_f32_16x16x32_bf16 v[22:25], v[162:165], v[196:199], v[22:25]
	v_mfma_f32_16x16x32_bf16 v[18:21], v[172:175], v[196:199], v[18:21]
	v_mfma_f32_16x16x32_bf16 v[6:9], v[162:165], v[204:207], v[6:9]
	v_mfma_f32_16x16x32_bf16 v[2:5], v[172:175], v[204:207], v[2:5]
	v_mfma_f32_16x16x32_bf16 v[54:57], v[168:171], v[184:187], v[54:57]
	v_mfma_f32_16x16x32_bf16 v[50:53], v[176:179], v[184:187], v[50:53]
	v_mfma_f32_16x16x32_bf16 v[38:41], v[168:171], v[192:195], v[38:41]
	v_mfma_f32_16x16x32_bf16 v[34:37], v[176:179], v[192:195], v[34:37]
	v_mfma_f32_16x16x32_bf16 v[22:25], v[168:171], v[200:203], v[22:25]
	v_mfma_f32_16x16x32_bf16 v[18:21], v[176:179], v[200:203], v[18:21]
	v_mfma_f32_16x16x32_bf16 v[6:9], v[168:171], v[216:219], v[6:9]
	v_mfma_f32_16x16x32_bf16 v[2:5], v[176:179], v[216:219], v[2:5]
	s_setprio 0
	s_barrier
	s_add_i32 s95, 0, 0x18000
	s_add_i32 s96, 0, 0x1c000
	v_add_u32_e32 v158, s95, v144
	v_add_u32_e32 v167, s96, v144
	ds_read_b128 v[146:149], v158
	ds_read_b128 v[150:153], v158 offset:1024
	ds_read_b128 v[154:157], v158 offset:2048
	ds_read_b128 v[158:161], v158 offset:3072
	ds_read_b128 v[162:165], v167
	ds_read_b128 v[168:171], v167 offset:1024
	ds_read_b128 v[172:175], v167 offset:2048
	ds_read_b128 v[176:179], v167 offset:3072
	s_add_u32 s62, s62, 0x40000
	s_addc_u32 s63, s63, 0
	s_mov_b32 m0, s33
	v_lshl_add_u64 v[242:243], s[62:63], 0, v[126:127]
	ds_read_b128 v[180:183], v145 offset:32768
	ds_read_b128 v[184:187], v145 offset:33792
	ds_read_b128 v[188:191], v145 offset:34816
	ds_read_b128 v[192:195], v145 offset:35840
	ds_read_b128 v[196:199], v145 offset:36864
	ds_read_b128 v[200:203], v145 offset:37888
	ds_read_b128 v[204:207], v145 offset:38912
	ds_read_b128 v[216:219], v145 offset:39936
	global_load_lds_dwordx4 v[242:243], off
	s_mov_b32 m0, s84
	v_lshl_add_u64 v[242:243], s[62:63], 0, v[120:121]
	global_load_lds_dwordx4 v[242:243], off
	s_waitcnt vmcnt(8) lgkmcnt(0)
	s_barrier
	s_setprio 1
	v_mfma_f32_16x16x32_bf16 v[134:137], v[146:149], v[180:183], v[134:137]
	v_mfma_f32_16x16x32_bf16 v[130:133], v[154:157], v[180:183], v[130:133]
	v_mfma_f32_16x16x32_bf16 v[110:113], v[146:149], v[188:191], v[110:113]
	v_mfma_f32_16x16x32_bf16 v[106:109], v[154:157], v[188:191], v[106:109]
	v_mfma_f32_16x16x32_bf16 v[94:97], v[146:149], v[196:199], v[94:97]
	v_mfma_f32_16x16x32_bf16 v[90:93], v[154:157], v[196:199], v[90:93]
	v_mfma_f32_16x16x32_bf16 v[78:81], v[146:149], v[204:207], v[78:81]
	v_mfma_f32_16x16x32_bf16 v[74:77], v[154:157], v[204:207], v[74:77]
	v_mfma_f32_16x16x32_bf16 v[134:137], v[150:153], v[184:187], v[134:137]
	v_mfma_f32_16x16x32_bf16 v[130:133], v[158:161], v[184:187], v[130:133]
	v_mfma_f32_16x16x32_bf16 v[110:113], v[150:153], v[192:195], v[110:113]
	v_mfma_f32_16x16x32_bf16 v[106:109], v[158:161], v[192:195], v[106:109]
	v_mfma_f32_16x16x32_bf16 v[94:97], v[150:153], v[200:203], v[94:97]
	v_mfma_f32_16x16x32_bf16 v[90:93], v[158:161], v[200:203], v[90:93]
	v_mfma_f32_16x16x32_bf16 v[78:81], v[150:153], v[216:219], v[78:81]
	v_mfma_f32_16x16x32_bf16 v[74:77], v[158:161], v[216:219], v[74:77]
	s_setprio 0
	s_setprio 1
	v_mfma_f32_16x16x32_bf16 v[122:125], v[162:165], v[180:183], v[122:125]
	v_mfma_f32_16x16x32_bf16 v[114:117], v[172:175], v[180:183], v[114:117]
	v_mfma_f32_16x16x32_bf16 v[102:105], v[162:165], v[188:191], v[102:105]
	v_mfma_f32_16x16x32_bf16 v[98:101], v[172:175], v[188:191], v[98:101]
	v_mfma_f32_16x16x32_bf16 v[86:89], v[162:165], v[196:199], v[86:89]
	v_mfma_f32_16x16x32_bf16 v[82:85], v[172:175], v[196:199], v[82:85]
	v_mfma_f32_16x16x32_bf16 v[70:73], v[162:165], v[204:207], v[70:73]
	v_mfma_f32_16x16x32_bf16 v[66:69], v[172:175], v[204:207], v[66:69]
	v_mfma_f32_16x16x32_bf16 v[122:125], v[168:171], v[184:187], v[122:125]
	v_mfma_f32_16x16x32_bf16 v[114:117], v[176:179], v[184:187], v[114:117]
	v_mfma_f32_16x16x32_bf16 v[102:105], v[168:171], v[192:195], v[102:105]
	v_mfma_f32_16x16x32_bf16 v[98:101], v[176:179], v[192:195], v[98:101]
	v_mfma_f32_16x16x32_bf16 v[86:89], v[168:171], v[200:203], v[86:89]
	v_mfma_f32_16x16x32_bf16 v[82:85], v[176:179], v[200:203], v[82:85]
	v_mfma_f32_16x16x32_bf16 v[70:73], v[168:171], v[216:219], v[70:73]
	v_mfma_f32_16x16x32_bf16 v[66:69], v[176:179], v[216:219], v[66:69]
	s_setprio 0
	s_barrier
	s_add_i32 s62, s95, s77
	v_lshl_add_u64 v[208:209], v[208:209], 0, s[56:57]
	s_mov_b32 m0, s62
	ds_read_b128 v[180:183], v145 offset:49152
	ds_read_b128 v[184:187], v145 offset:50176
	ds_read_b128 v[188:191], v145 offset:51200
	ds_read_b128 v[192:195], v145 offset:52224
	ds_read_b128 v[196:199], v145 offset:53248
	ds_read_b128 v[200:203], v145 offset:54272
	ds_read_b128 v[204:207], v145 offset:55296
	ds_read_b128 v[216:219], v145 offset:56320
	global_load_lds_dwordx4 v[208:209], off
	s_add_i32 m0, s62, 0x2000
	s_add_u32 s52, s52, 0x40080
	v_lshl_add_u64 v[208:209], v[220:221], 0, s[56:57]
	s_addc_u32 s53, s53, 0
	s_add_i32 s62, s96, s77
	global_load_lds_dwordx4 v[208:209], off
	s_mov_b32 m0, s62
	v_lshl_add_u64 v[208:209], s[52:53], 0, v[0:1]
	global_load_lds_dwordx4 v[208:209], off
	s_add_i32 m0, s62, 0x2000
	v_lshl_add_u64 v[208:209], s[52:53], 0, v[118:119]
	global_load_lds_dwordx4 v[208:209], off
	s_mov_b32 m0, s85
	v_lshl_add_u64 v[208:209], v[222:223], 0, s[56:57]
	global_load_lds_dwordx4 v[208:209], off
	s_mov_b32 m0, s90
	v_lshl_add_u64 v[208:209], v[224:225], 0, s[56:57]
	global_load_lds_dwordx4 v[208:209], off
	s_waitcnt vmcnt(8) lgkmcnt(0)
	s_barrier
	s_setprio 1
	v_mfma_f32_16x16x32_bf16 v[62:65], v[146:149], v[180:183], v[62:65]
	v_mfma_f32_16x16x32_bf16 v[58:61], v[154:157], v[180:183], v[58:61]
	v_mfma_f32_16x16x32_bf16 v[46:49], v[146:149], v[188:191], v[46:49]
	v_mfma_f32_16x16x32_bf16 v[42:45], v[154:157], v[188:191], v[42:45]
	v_mfma_f32_16x16x32_bf16 v[30:33], v[146:149], v[196:199], v[30:33]
	v_mfma_f32_16x16x32_bf16 v[26:29], v[154:157], v[196:199], v[26:29]
	v_mfma_f32_16x16x32_bf16 v[14:17], v[146:149], v[204:207], v[14:17]
	v_mfma_f32_16x16x32_bf16 v[10:13], v[154:157], v[204:207], v[10:13]
	v_mfma_f32_16x16x32_bf16 v[62:65], v[150:153], v[184:187], v[62:65]
	v_mfma_f32_16x16x32_bf16 v[58:61], v[158:161], v[184:187], v[58:61]
	v_mfma_f32_16x16x32_bf16 v[46:49], v[150:153], v[192:195], v[46:49]
	v_mfma_f32_16x16x32_bf16 v[42:45], v[158:161], v[192:195], v[42:45]
	v_mfma_f32_16x16x32_bf16 v[30:33], v[150:153], v[200:203], v[30:33]
	v_mfma_f32_16x16x32_bf16 v[26:29], v[158:161], v[200:203], v[26:29]
	v_mfma_f32_16x16x32_bf16 v[14:17], v[150:153], v[216:219], v[14:17]
	v_mfma_f32_16x16x32_bf16 v[10:13], v[158:161], v[216:219], v[10:13]
	s_setprio 0
	s_setprio 1
	v_mfma_f32_16x16x32_bf16 v[54:57], v[162:165], v[180:183], v[54:57]
	v_mfma_f32_16x16x32_bf16 v[50:53], v[172:175], v[180:183], v[50:53]
	v_mfma_f32_16x16x32_bf16 v[38:41], v[162:165], v[188:191], v[38:41]
	v_mfma_f32_16x16x32_bf16 v[34:37], v[172:175], v[188:191], v[34:37]
	v_mfma_f32_16x16x32_bf16 v[22:25], v[162:165], v[196:199], v[22:25]
	v_mfma_f32_16x16x32_bf16 v[18:21], v[172:175], v[196:199], v[18:21]
	v_mfma_f32_16x16x32_bf16 v[6:9], v[162:165], v[204:207], v[6:9]
	v_mfma_f32_16x16x32_bf16 v[2:5], v[172:175], v[204:207], v[2:5]
	v_mfma_f32_16x16x32_bf16 v[54:57], v[168:171], v[184:187], v[54:57]
	v_mfma_f32_16x16x32_bf16 v[50:53], v[176:179], v[184:187], v[50:53]
	v_mfma_f32_16x16x32_bf16 v[38:41], v[168:171], v[192:195], v[38:41]
	v_mfma_f32_16x16x32_bf16 v[34:37], v[176:179], v[192:195], v[34:37]
	v_mfma_f32_16x16x32_bf16 v[22:25], v[168:171], v[200:203], v[22:25]
	v_mfma_f32_16x16x32_bf16 v[18:21], v[176:179], v[200:203], v[18:21]
	v_mfma_f32_16x16x32_bf16 v[6:9], v[168:171], v[216:219], v[6:9]
	v_mfma_f32_16x16x32_bf16 v[2:5], v[176:179], v[216:219], v[2:5]
	s_setprio 0
	s_barrier
	s_add_i32 s94, s94, 2
	s_add_u32 s48, s48, 0x100
	s_addc_u32 s49, s49, 0
	s_cmp_gt_u32 s94, 13
	s_cbranch_scc0 .LBB0_684
	s_add_u32 s48, s8, 0xffffff00
	s_addc_u32 s49, s9, -1
	s_andn2_b64 vcc, exec, s[42:43]
	s_cbranch_vccnz .LBB0_687
	v_mov_b32_e32 v2, 0
	s_mov_b32 s18, s34
	s_mov_b32 s92, s36
	s_mov_b64 s[30:31], s[46:47]
	s_mov_b32 s68, s58
	v_mov_b32_e32 v3, v2
	v_mov_b32_e32 v4, v2
	v_mov_b32_e32 v5, v2
	v_mov_b32_e32 v6, v2
	v_mov_b32_e32 v7, v2
	v_mov_b32_e32 v8, v2
	v_mov_b32_e32 v9, v2
	v_mov_b32_e32 v18, v2
	v_mov_b32_e32 v19, v2
	v_mov_b32_e32 v20, v2
	v_mov_b32_e32 v21, v2
	v_mov_b32_e32 v22, v2
	v_mov_b32_e32 v23, v2
	v_mov_b32_e32 v24, v2
	v_mov_b32_e32 v25, v2
	v_mov_b32_e32 v34, v2
	v_mov_b32_e32 v35, v2
	v_mov_b32_e32 v36, v2
	v_mov_b32_e32 v37, v2
	v_mov_b32_e32 v38, v2
	v_mov_b32_e32 v39, v2
	v_mov_b32_e32 v40, v2
	v_mov_b32_e32 v41, v2
	v_mov_b32_e32 v50, v2
	v_mov_b32_e32 v51, v2
	v_mov_b32_e32 v52, v2
	v_mov_b32_e32 v53, v2
	v_mov_b32_e32 v54, v2
	v_mov_b32_e32 v55, v2
	v_mov_b32_e32 v56, v2
	v_mov_b32_e32 v57, v2
	v_mov_b32_e32 v10, v2
	v_mov_b32_e32 v11, v2
	v_mov_b32_e32 v12, v2
	v_mov_b32_e32 v13, v2
	v_mov_b32_e32 v14, v2
	v_mov_b32_e32 v15, v2
	v_mov_b32_e32 v16, v2
	v_mov_b32_e32 v17, v2
	v_mov_b32_e32 v26, v2
	v_mov_b32_e32 v27, v2
	v_mov_b32_e32 v28, v2
	v_mov_b32_e32 v29, v2
	v_mov_b32_e32 v30, v2
	v_mov_b32_e32 v31, v2
	v_mov_b32_e32 v32, v2
	v_mov_b32_e32 v33, v2
	v_mov_b32_e32 v42, v2
	v_mov_b32_e32 v43, v2
	v_mov_b32_e32 v44, v2
	v_mov_b32_e32 v45, v2
	v_mov_b32_e32 v46, v2
	v_mov_b32_e32 v47, v2
	v_mov_b32_e32 v48, v2
	v_mov_b32_e32 v49, v2
	v_mov_b32_e32 v58, v2
	v_mov_b32_e32 v59, v2
	v_mov_b32_e32 v60, v2
	v_mov_b32_e32 v61, v2
	v_mov_b32_e32 v62, v2
	v_mov_b32_e32 v63, v2
	v_mov_b32_e32 v64, v2
	v_mov_b32_e32 v65, v2
	v_mov_b32_e32 v66, v2
	v_mov_b32_e32 v67, v2
	v_mov_b32_e32 v68, v2
	v_mov_b32_e32 v69, v2
	v_mov_b32_e32 v70, v2
	v_mov_b32_e32 v71, v2
	v_mov_b32_e32 v72, v2
	v_mov_b32_e32 v73, v2
	v_mov_b32_e32 v82, v2
	v_mov_b32_e32 v83, v2
	v_mov_b32_e32 v84, v2
	v_mov_b32_e32 v85, v2
	v_mov_b32_e32 v86, v2
	v_mov_b32_e32 v87, v2
	v_mov_b32_e32 v88, v2
	v_mov_b32_e32 v89, v2
	v_mov_b32_e32 v98, v2
	v_mov_b32_e32 v99, v2
	v_mov_b32_e32 v100, v2
	v_mov_b32_e32 v101, v2
	v_mov_b32_e32 v102, v2
	v_mov_b32_e32 v103, v2
	v_mov_b32_e32 v104, v2
	v_mov_b32_e32 v105, v2
	v_mov_b32_e32 v114, v2
	v_mov_b32_e32 v115, v2
	v_mov_b32_e32 v116, v2
	v_mov_b32_e32 v117, v2
	v_mov_b32_e32 v122, v2
	v_mov_b32_e32 v123, v2
	v_mov_b32_e32 v124, v2
	v_mov_b32_e32 v125, v2
	v_mov_b32_e32 v74, v2
	v_mov_b32_e32 v75, v2
	v_mov_b32_e32 v76, v2
	v_mov_b32_e32 v77, v2
	v_mov_b32_e32 v78, v2
	v_mov_b32_e32 v79, v2
	v_mov_b32_e32 v80, v2
	v_mov_b32_e32 v81, v2
	v_mov_b32_e32 v90, v2
	v_mov_b32_e32 v91, v2
	v_mov_b32_e32 v92, v2
	v_mov_b32_e32 v93, v2
	v_mov_b32_e32 v94, v2
	v_mov_b32_e32 v95, v2
	v_mov_b32_e32 v96, v2
	v_mov_b32_e32 v97, v2
	v_mov_b32_e32 v106, v2
	v_mov_b32_e32 v107, v2
	v_mov_b32_e32 v108, v2
	v_mov_b32_e32 v109, v2
	v_mov_b32_e32 v110, v2
	v_mov_b32_e32 v111, v2
	v_mov_b32_e32 v112, v2
	v_mov_b32_e32 v113, v2
	v_mov_b32_e32 v130, v2
	v_mov_b32_e32 v131, v2
	v_mov_b32_e32 v132, v2
	v_mov_b32_e32 v133, v2
	v_mov_b32_e32 v134, v2
	v_mov_b32_e32 v135, v2
	v_mov_b32_e32 v136, v2
	v_mov_b32_e32 v137, v2
	s_branch .LBB0_688

.Lnobar_e1e:
.LBB0_836:
	s_add_u32 s28, s6, 0xfffc0080
	s_addc_u32 s29, s7, -1
	s_add_i32 s41, 0, 0x10000
	s_cmp_eq_u32 s40, 12
	s_cselect_b32 s31, s5, s29
	s_cselect_b32 s30, s8, s28
	s_cselect_b32 s29, s9, s33
	s_cselect_b32 s28, s21, s23
	s_add_i32 s53, 0, 0x14000
	v_add_u32_e32 v142, s41, v186
	v_add_u32_e32 v168, s53, v186
	ds_read_b128 v[130:133], v142
	ds_read_b128 v[134:137], v142 offset:1024
	ds_read_b128 v[138:141], v142 offset:2048
	ds_read_b128 v[142:145], v142 offset:3072
	ds_read_b128 v[146:149], v168
	ds_read_b128 v[150:153], v168 offset:1024
	ds_read_b128 v[154:157], v168 offset:2048
	ds_read_b128 v[168:171], v168 offset:3072
	v_lshl_add_u64 v[216:217], s[6:7], 0, v[166:167]
	s_add_i32 m0, s43, 0xc000
	ds_read_b128 v[172:175], v188
	ds_read_b128 v[176:179], v188 offset:1024
	ds_read_b128 v[180:183], v188 offset:2048
	ds_read_b128 v[190:193], v188 offset:3072
	ds_read_b128 v[194:197], v188 offset:4096
	ds_read_b128 v[198:201], v188 offset:5120
	ds_read_b128 v[202:205], v188 offset:6144
	ds_read_b128 v[206:209], v188 offset:7168
	global_load_lds_dwordx4 v[216:217], off
	s_add_i32 m0, s43, 0xe000
	v_lshl_add_u64 v[216:217], s[6:7], 0, v[164:165]
	global_load_lds_dwordx4 v[216:217], off
	s_waitcnt vmcnt(8) lgkmcnt(0)
	s_barrier
	s_setprio 1
	v_mfma_f32_16x16x32_bf16 v[126:129], v[130:133], v[172:175], v[126:129]
	v_mfma_f32_16x16x32_bf16 v[122:125], v[138:141], v[172:175], v[122:125]
	v_mfma_f32_16x16x32_bf16 v[114:117], v[130:133], v[180:183], v[114:117]
	v_mfma_f32_16x16x32_bf16 v[106:109], v[138:141], v[180:183], v[106:109]
	v_mfma_f32_16x16x32_bf16 v[98:101], v[130:133], v[194:197], v[98:101]
	v_mfma_f32_16x16x32_bf16 v[90:93], v[138:141], v[194:197], v[90:93]
	v_mfma_f32_16x16x32_bf16 v[82:85], v[130:133], v[202:205], v[82:85]
	v_mfma_f32_16x16x32_bf16 v[74:77], v[138:141], v[202:205], v[74:77]
	v_mfma_f32_16x16x32_bf16 v[126:129], v[134:137], v[176:179], v[126:129]
	v_mfma_f32_16x16x32_bf16 v[122:125], v[142:145], v[176:179], v[122:125]
	v_mfma_f32_16x16x32_bf16 v[114:117], v[134:137], v[190:193], v[114:117]
	v_mfma_f32_16x16x32_bf16 v[106:109], v[142:145], v[190:193], v[106:109]
	v_mfma_f32_16x16x32_bf16 v[98:101], v[134:137], v[198:201], v[98:101]
	v_mfma_f32_16x16x32_bf16 v[90:93], v[142:145], v[198:201], v[90:93]
	v_mfma_f32_16x16x32_bf16 v[82:85], v[134:137], v[206:209], v[82:85]
	v_mfma_f32_16x16x32_bf16 v[74:77], v[142:145], v[206:209], v[74:77]
	s_setprio 0
	s_setprio 1
	v_mfma_f32_16x16x32_bf16 v[118:121], v[146:149], v[172:175], v[118:121]
	v_mfma_f32_16x16x32_bf16 v[110:113], v[154:157], v[172:175], v[110:113]
	v_mfma_f32_16x16x32_bf16 v[102:105], v[146:149], v[180:183], v[102:105]
	v_mfma_f32_16x16x32_bf16 v[94:97], v[154:157], v[180:183], v[94:97]
	v_mfma_f32_16x16x32_bf16 v[86:89], v[146:149], v[194:197], v[86:89]
	v_mfma_f32_16x16x32_bf16 v[78:81], v[154:157], v[194:197], v[78:81]
	v_mfma_f32_16x16x32_bf16 v[70:73], v[146:149], v[202:205], v[70:73]
	v_mfma_f32_16x16x32_bf16 v[66:69], v[154:157], v[202:205], v[66:69]
	v_mfma_f32_16x16x32_bf16 v[118:121], v[150:153], v[176:179], v[118:121]
	v_mfma_f32_16x16x32_bf16 v[110:113], v[168:171], v[176:179], v[110:113]
	v_mfma_f32_16x16x32_bf16 v[102:105], v[150:153], v[190:193], v[102:105]
	v_mfma_f32_16x16x32_bf16 v[94:97], v[168:171], v[190:193], v[94:97]
	v_mfma_f32_16x16x32_bf16 v[86:89], v[150:153], v[198:201], v[86:89]
	v_mfma_f32_16x16x32_bf16 v[78:81], v[168:171], v[198:201], v[78:81]
	v_mfma_f32_16x16x32_bf16 v[70:73], v[150:153], v[206:209], v[70:73]
	v_mfma_f32_16x16x32_bf16 v[66:69], v[168:171], v[206:209], v[66:69]
	s_setprio 0
	s_barrier
	s_add_i32 s41, s41, s42
	v_lshl_add_u64 v[216:217], s[28:29], 0, v[0:1]
	s_mov_b32 m0, s41
	ds_read_b128 v[172:175], v188 offset:16384
	ds_read_b128 v[176:179], v188 offset:17408
	ds_read_b128 v[180:183], v188 offset:18432
	ds_read_b128 v[190:193], v188 offset:19456
	ds_read_b128 v[194:197], v188 offset:20480
	ds_read_b128 v[198:201], v188 offset:21504
	ds_read_b128 v[202:205], v188 offset:22528
	ds_read_b128 v[206:209], v188 offset:23552
	global_load_lds_dwordx4 v[216:217], off
	s_add_i32 m0, s41, 0x2000
	s_add_u32 s58, s28, 0x40000
	v_lshl_add_u64 v[218:219], s[28:29], 0, v[158:159]
	s_addc_u32 s59, s29, 0
	s_add_i32 s41, s53, s42
	global_load_lds_dwordx4 v[218:219], off
	v_lshl_add_u64 v[220:221], s[58:59], 0, v[0:1]
	s_mov_b32 m0, s41
	v_lshl_add_u64 v[222:223], s[30:31], 0, v[160:161]
	global_load_lds_dwordx4 v[220:221], off
	s_add_i32 m0, s41, 0x2000
	v_lshl_add_u64 v[220:221], s[58:59], 0, v[158:159]
	global_load_lds_dwordx4 v[220:221], off
	s_mov_b32 m0, s43
	v_lshl_add_u64 v[220:221], s[30:31], 0, v[162:163]
	global_load_lds_dwordx4 v[220:221], off
	s_mov_b32 m0, s44
	s_nop 0
	global_load_lds_dwordx4 v[222:223], off
	s_waitcnt vmcnt(8) lgkmcnt(0)
	s_barrier
	s_setprio 1
	v_mfma_f32_16x16x32_bf16 v[62:65], v[130:133], v[172:175], v[62:65]
	v_mfma_f32_16x16x32_bf16 v[58:61], v[138:141], v[172:175], v[58:61]
	v_mfma_f32_16x16x32_bf16 v[50:53], v[130:133], v[180:183], v[50:53]
	v_mfma_f32_16x16x32_bf16 v[42:45], v[138:141], v[180:183], v[42:45]
	v_mfma_f32_16x16x32_bf16 v[34:37], v[130:133], v[194:197], v[34:37]
	v_mfma_f32_16x16x32_bf16 v[26:29], v[138:141], v[194:197], v[26:29]
	v_mfma_f32_16x16x32_bf16 v[18:21], v[130:133], v[202:205], v[18:21]
	v_mfma_f32_16x16x32_bf16 v[10:13], v[138:141], v[202:205], v[10:13]
	v_mfma_f32_16x16x32_bf16 v[62:65], v[134:137], v[176:179], v[62:65]
	v_mfma_f32_16x16x32_bf16 v[58:61], v[142:145], v[176:179], v[58:61]
	v_mfma_f32_16x16x32_bf16 v[50:53], v[134:137], v[190:193], v[50:53]
	v_mfma_f32_16x16x32_bf16 v[42:45], v[142:145], v[190:193], v[42:45]
	v_mfma_f32_16x16x32_bf16 v[34:37], v[134:137], v[198:201], v[34:37]
	v_mfma_f32_16x16x32_bf16 v[26:29], v[142:145], v[198:201], v[26:29]
	v_mfma_f32_16x16x32_bf16 v[18:21], v[134:137], v[206:209], v[18:21]
	v_mfma_f32_16x16x32_bf16 v[10:13], v[142:145], v[206:209], v[10:13]
	s_setprio 0
	s_setprio 1
	v_mfma_f32_16x16x32_bf16 v[54:57], v[146:149], v[172:175], v[54:57]
	v_mfma_f32_16x16x32_bf16 v[46:49], v[154:157], v[172:175], v[46:49]
	v_mfma_f32_16x16x32_bf16 v[38:41], v[146:149], v[180:183], v[38:41]
	v_mfma_f32_16x16x32_bf16 v[30:33], v[154:157], v[180:183], v[30:33]
	v_mfma_f32_16x16x32_bf16 v[22:25], v[146:149], v[194:197], v[22:25]
	v_mfma_f32_16x16x32_bf16 v[14:17], v[154:157], v[194:197], v[14:17]
	v_mfma_f32_16x16x32_bf16 v[6:9], v[146:149], v[202:205], v[6:9]
	v_mfma_f32_16x16x32_bf16 v[2:5], v[154:157], v[202:205], v[2:5]
	v_mfma_f32_16x16x32_bf16 v[54:57], v[150:153], v[176:179], v[54:57]
	v_mfma_f32_16x16x32_bf16 v[46:49], v[168:171], v[176:179], v[46:49]
	v_mfma_f32_16x16x32_bf16 v[38:41], v[150:153], v[190:193], v[38:41]
	v_mfma_f32_16x16x32_bf16 v[30:33], v[168:171], v[190:193], v[30:33]
	v_mfma_f32_16x16x32_bf16 v[22:25], v[150:153], v[198:201], v[22:25]
	v_mfma_f32_16x16x32_bf16 v[14:17], v[168:171], v[198:201], v[14:17]
	v_mfma_f32_16x16x32_bf16 v[6:9], v[150:153], v[206:209], v[6:9]
	v_mfma_f32_16x16x32_bf16 v[2:5], v[168:171], v[206:209], v[2:5]
	s_setprio 0
	s_barrier
	s_add_i32 s41, 0, 0x18000
	s_add_i32 s53, 0, 0x1c000
	v_add_u32_e32 v142, s41, v186
	v_add_u32_e32 v168, s53, v186
	ds_read_b128 v[130:133], v142
	ds_read_b128 v[134:137], v142 offset:1024
	ds_read_b128 v[138:141], v142 offset:2048
	ds_read_b128 v[142:145], v142 offset:3072
	ds_read_b128 v[146:149], v168
	ds_read_b128 v[150:153], v168 offset:1024
	ds_read_b128 v[154:157], v168 offset:2048
	ds_read_b128 v[168:171], v168 offset:3072
	s_add_u32 s30, s30, 0x40000
	s_addc_u32 s31, s31, 0
	s_mov_b32 m0, s45
	v_lshl_add_u64 v[224:225], s[30:31], 0, v[162:163]
	ds_read_b128 v[172:175], v188 offset:32768
	ds_read_b128 v[176:179], v188 offset:33792
	ds_read_b128 v[180:183], v188 offset:34816
	ds_read_b128 v[190:193], v188 offset:35840
	ds_read_b128 v[194:197], v188 offset:36864
	ds_read_b128 v[198:201], v188 offset:37888
	ds_read_b128 v[202:205], v188 offset:38912
	ds_read_b128 v[206:209], v188 offset:39936
	global_load_lds_dwordx4 v[224:225], off
	s_mov_b32 m0, s46
	v_lshl_add_u64 v[224:225], s[30:31], 0, v[160:161]
	global_load_lds_dwordx4 v[224:225], off
	s_waitcnt vmcnt(8) lgkmcnt(0)
	s_barrier
	s_setprio 1
	v_mfma_f32_16x16x32_bf16 v[126:129], v[130:133], v[172:175], v[126:129]
	v_mfma_f32_16x16x32_bf16 v[122:125], v[138:141], v[172:175], v[122:125]
	v_mfma_f32_16x16x32_bf16 v[114:117], v[130:133], v[180:183], v[114:117]
	v_mfma_f32_16x16x32_bf16 v[106:109], v[138:141], v[180:183], v[106:109]
	v_mfma_f32_16x16x32_bf16 v[98:101], v[130:133], v[194:197], v[98:101]
	v_mfma_f32_16x16x32_bf16 v[90:93], v[138:141], v[194:197], v[90:93]
	v_mfma_f32_16x16x32_bf16 v[82:85], v[130:133], v[202:205], v[82:85]
	v_mfma_f32_16x16x32_bf16 v[74:77], v[138:141], v[202:205], v[74:77]
	v_mfma_f32_16x16x32_bf16 v[126:129], v[134:137], v[176:179], v[126:129]
	v_mfma_f32_16x16x32_bf16 v[122:125], v[142:145], v[176:179], v[122:125]
	v_mfma_f32_16x16x32_bf16 v[114:117], v[134:137], v[190:193], v[114:117]
	v_mfma_f32_16x16x32_bf16 v[106:109], v[142:145], v[190:193], v[106:109]
	v_mfma_f32_16x16x32_bf16 v[98:101], v[134:137], v[198:201], v[98:101]
	v_mfma_f32_16x16x32_bf16 v[90:93], v[142:145], v[198:201], v[90:93]
	v_mfma_f32_16x16x32_bf16 v[82:85], v[134:137], v[206:209], v[82:85]
	v_mfma_f32_16x16x32_bf16 v[74:77], v[142:145], v[206:209], v[74:77]
	s_setprio 0
	s_setprio 1
	v_mfma_f32_16x16x32_bf16 v[118:121], v[146:149], v[172:175], v[118:121]
	v_mfma_f32_16x16x32_bf16 v[110:113], v[154:157], v[172:175], v[110:113]
	v_mfma_f32_16x16x32_bf16 v[102:105], v[146:149], v[180:183], v[102:105]
	v_mfma_f32_16x16x32_bf16 v[94:97], v[154:157], v[180:183], v[94:97]
	v_mfma_f32_16x16x32_bf16 v[86:89], v[146:149], v[194:197], v[86:89]
	v_mfma_f32_16x16x32_bf16 v[78:81], v[154:157], v[194:197], v[78:81]
	v_mfma_f32_16x16x32_bf16 v[70:73], v[146:149], v[202:205], v[70:73]
	v_mfma_f32_16x16x32_bf16 v[66:69], v[154:157], v[202:205], v[66:69]
	v_mfma_f32_16x16x32_bf16 v[118:121], v[150:153], v[176:179], v[118:121]
	v_mfma_f32_16x16x32_bf16 v[110:113], v[168:171], v[176:179], v[110:113]
	v_mfma_f32_16x16x32_bf16 v[102:105], v[150:153], v[190:193], v[102:105]
	v_mfma_f32_16x16x32_bf16 v[94:97], v[168:171], v[190:193], v[94:97]
	v_mfma_f32_16x16x32_bf16 v[86:89], v[150:153], v[198:201], v[86:89]
	v_mfma_f32_16x16x32_bf16 v[78:81], v[168:171], v[198:201], v[78:81]
	v_mfma_f32_16x16x32_bf16 v[70:73], v[150:153], v[206:209], v[70:73]
	v_mfma_f32_16x16x32_bf16 v[66:69], v[168:171], v[206:209], v[66:69]
	s_setprio 0
	s_barrier
	s_add_i32 s30, s41, s42
	v_lshl_add_u64 v[216:217], v[216:217], 0, s[56:57]
	s_mov_b32 m0, s30
	ds_read_b128 v[172:175], v188 offset:49152
	ds_read_b128 v[176:179], v188 offset:50176
	ds_read_b128 v[180:183], v188 offset:51200
	ds_read_b128 v[190:193], v188 offset:52224
	ds_read_b128 v[194:197], v188 offset:53248
	ds_read_b128 v[198:201], v188 offset:54272
	ds_read_b128 v[202:205], v188 offset:55296
	ds_read_b128 v[206:209], v188 offset:56320
	global_load_lds_dwordx4 v[216:217], off
	s_add_i32 m0, s30, 0x2000
	s_add_u32 s28, s28, 0x40080
	v_lshl_add_u64 v[216:217], v[218:219], 0, s[56:57]
	s_addc_u32 s29, s29, 0
	s_add_i32 s30, s53, s42
	global_load_lds_dwordx4 v[216:217], off
	s_mov_b32 m0, s30
	v_lshl_add_u64 v[216:217], s[28:29], 0, v[0:1]
	global_load_lds_dwordx4 v[216:217], off
	s_add_i32 m0, s30, 0x2000
	v_lshl_add_u64 v[216:217], s[28:29], 0, v[158:159]
	global_load_lds_dwordx4 v[216:217], off
	s_mov_b32 m0, s47
	v_lshl_add_u64 v[216:217], v[220:221], 0, s[56:57]
	global_load_lds_dwordx4 v[216:217], off
	s_mov_b32 m0, s48
	v_lshl_add_u64 v[216:217], v[222:223], 0, s[56:57]
	global_load_lds_dwordx4 v[216:217], off
	s_waitcnt vmcnt(8) lgkmcnt(0)
	s_barrier
	s_setprio 1
	v_mfma_f32_16x16x32_bf16 v[62:65], v[130:133], v[172:175], v[62:65]
	v_mfma_f32_16x16x32_bf16 v[58:61], v[138:141], v[172:175], v[58:61]
	v_mfma_f32_16x16x32_bf16 v[50:53], v[130:133], v[180:183], v[50:53]
	v_mfma_f32_16x16x32_bf16 v[42:45], v[138:141], v[180:183], v[42:45]
	v_mfma_f32_16x16x32_bf16 v[34:37], v[130:133], v[194:197], v[34:37]
	v_mfma_f32_16x16x32_bf16 v[26:29], v[138:141], v[194:197], v[26:29]
	v_mfma_f32_16x16x32_bf16 v[18:21], v[130:133], v[202:205], v[18:21]
	v_mfma_f32_16x16x32_bf16 v[10:13], v[138:141], v[202:205], v[10:13]
	v_mfma_f32_16x16x32_bf16 v[62:65], v[134:137], v[176:179], v[62:65]
	v_mfma_f32_16x16x32_bf16 v[58:61], v[142:145], v[176:179], v[58:61]
	v_mfma_f32_16x16x32_bf16 v[50:53], v[134:137], v[190:193], v[50:53]
	v_mfma_f32_16x16x32_bf16 v[42:45], v[142:145], v[190:193], v[42:45]
	v_mfma_f32_16x16x32_bf16 v[34:37], v[134:137], v[198:201], v[34:37]
	v_mfma_f32_16x16x32_bf16 v[26:29], v[142:145], v[198:201], v[26:29]
	v_mfma_f32_16x16x32_bf16 v[18:21], v[134:137], v[206:209], v[18:21]
	v_mfma_f32_16x16x32_bf16 v[10:13], v[142:145], v[206:209], v[10:13]
	s_setprio 0
	s_setprio 1
	v_mfma_f32_16x16x32_bf16 v[54:57], v[146:149], v[172:175], v[54:57]
	v_mfma_f32_16x16x32_bf16 v[46:49], v[154:157], v[172:175], v[46:49]
	v_mfma_f32_16x16x32_bf16 v[38:41], v[146:149], v[180:183], v[38:41]
	v_mfma_f32_16x16x32_bf16 v[30:33], v[154:157], v[180:183], v[30:33]
	v_mfma_f32_16x16x32_bf16 v[22:25], v[146:149], v[194:197], v[22:25]
	v_mfma_f32_16x16x32_bf16 v[14:17], v[154:157], v[194:197], v[14:17]
	v_mfma_f32_16x16x32_bf16 v[6:9], v[146:149], v[202:205], v[6:9]
	v_mfma_f32_16x16x32_bf16 v[2:5], v[154:157], v[202:205], v[2:5]
	v_mfma_f32_16x16x32_bf16 v[54:57], v[150:153], v[176:179], v[54:57]
	v_mfma_f32_16x16x32_bf16 v[46:49], v[168:171], v[176:179], v[46:49]
	v_mfma_f32_16x16x32_bf16 v[38:41], v[150:153], v[190:193], v[38:41]
	v_mfma_f32_16x16x32_bf16 v[30:33], v[168:171], v[190:193], v[30:33]
	v_mfma_f32_16x16x32_bf16 v[22:25], v[150:153], v[198:201], v[22:25]
	v_mfma_f32_16x16x32_bf16 v[14:17], v[168:171], v[198:201], v[14:17]
	v_mfma_f32_16x16x32_bf16 v[6:9], v[150:153], v[206:209], v[6:9]
	v_mfma_f32_16x16x32_bf16 v[2:5], v[168:171], v[206:209], v[2:5]
	s_setprio 0
	s_barrier
	s_add_i32 s40, s40, 2
	s_add_u32 s23, s23, 0x100
	s_addc_u32 s33, s33, 0
	s_add_u32 s6, s6, 0x100
	s_addc_u32 s7, s7, 0
	s_cmp_gt_u32 s40, 13
	s_cbranch_scc0 .LBB0_836
	s_and_b64 vcc, exec, s[18:19]
	s_cbranch_vccz .LBB0_839
	s_barrier

.LBB0_1525:
	s_add_u32 s36, s26, s34
	s_addc_u32 s37, s27, s35
	s_add_u32 s36, s36, 0x100
	s_addc_u32 s37, s37, 0
	s_add_u32 s82, s8, s34
	s_addc_u32 s83, s9, s35
	s_add_i32 s84, 0, 0x10000
	s_cmpk_eq_i32 s34, 0xb00
	s_cselect_b32 s45, s31, s37
	s_cselect_b32 s44, s30, s36
	s_cselect_b32 s37, s29, s83
	s_cselect_b32 s36, s28, s82
	s_add_i32 s85, 0, 0x14000
	v_add_u32_e32 v158, s84, v144
	v_add_u32_e32 v176, s85, v144
	ds_read_b128 v[146:149], v158
	ds_read_b128 v[150:153], v158 offset:1024
	ds_read_b128 v[154:157], v158 offset:2048
	ds_read_b128 v[158:161], v158 offset:3072
	ds_read_b128 v[162:165], v176
	ds_read_b128 v[168:171], v176 offset:1024
	ds_read_b128 v[172:175], v176 offset:2048
	ds_read_b128 v[176:179], v176 offset:3072
	v_lshl_add_u64 v[208:209], v[142:143], 0, s[34:35]
	s_add_i32 m0, s4, 0xc000
	ds_read_b128 v[180:183], v145
	ds_read_b128 v[184:187], v145 offset:1024
	ds_read_b128 v[188:191], v145 offset:2048
	ds_read_b128 v[192:195], v145 offset:3072
	ds_read_b128 v[196:199], v145 offset:4096
	ds_read_b128 v[200:203], v145 offset:5120
	ds_read_b128 v[204:207], v145 offset:6144
	ds_read_b128 v[216:219], v145 offset:7168
	global_load_lds_dwordx4 v[208:209], off
	s_add_i32 m0, s4, 0xe000
	v_lshl_add_u64 v[208:209], v[140:141], 0, s[34:35]
	global_load_lds_dwordx4 v[208:209], off
	s_waitcnt vmcnt(8) lgkmcnt(0)
	s_barrier
	s_setprio 1
	v_mfma_f32_16x16x32_bf16 v[134:137], v[146:149], v[180:183], v[134:137]
	v_mfma_f32_16x16x32_bf16 v[130:133], v[154:157], v[180:183], v[130:133]
	v_mfma_f32_16x16x32_bf16 v[110:113], v[146:149], v[188:191], v[110:113]
	v_mfma_f32_16x16x32_bf16 v[106:109], v[154:157], v[188:191], v[106:109]
	v_mfma_f32_16x16x32_bf16 v[94:97], v[146:149], v[196:199], v[94:97]
	v_mfma_f32_16x16x32_bf16 v[90:93], v[154:157], v[196:199], v[90:93]
	v_mfma_f32_16x16x32_bf16 v[78:81], v[146:149], v[204:207], v[78:81]
	v_mfma_f32_16x16x32_bf16 v[74:77], v[154:157], v[204:207], v[74:77]
	v_mfma_f32_16x16x32_bf16 v[134:137], v[150:153], v[184:187], v[134:137]
	v_mfma_f32_16x16x32_bf16 v[130:133], v[158:161], v[184:187], v[130:133]
	v_mfma_f32_16x16x32_bf16 v[110:113], v[150:153], v[192:195], v[110:113]
	v_mfma_f32_16x16x32_bf16 v[106:109], v[158:161], v[192:195], v[106:109]
	v_mfma_f32_16x16x32_bf16 v[94:97], v[150:153], v[200:203], v[94:97]
	v_mfma_f32_16x16x32_bf16 v[90:93], v[158:161], v[200:203], v[90:93]
	v_mfma_f32_16x16x32_bf16 v[78:81], v[150:153], v[216:219], v[78:81]
	v_mfma_f32_16x16x32_bf16 v[74:77], v[158:161], v[216:219], v[74:77]
	s_setprio 0
	s_setprio 1
	v_mfma_f32_16x16x32_bf16 v[122:125], v[162:165], v[180:183], v[122:125]
	v_mfma_f32_16x16x32_bf16 v[114:117], v[172:175], v[180:183], v[114:117]
	v_mfma_f32_16x16x32_bf16 v[102:105], v[162:165], v[188:191], v[102:105]
	v_mfma_f32_16x16x32_bf16 v[98:101], v[172:175], v[188:191], v[98:101]
	v_mfma_f32_16x16x32_bf16 v[86:89], v[162:165], v[196:199], v[86:89]
	v_mfma_f32_16x16x32_bf16 v[82:85], v[172:175], v[196:199], v[82:85]
	v_mfma_f32_16x16x32_bf16 v[70:73], v[162:165], v[204:207], v[70:73]
	v_mfma_f32_16x16x32_bf16 v[66:69], v[172:175], v[204:207], v[66:69]
	v_mfma_f32_16x16x32_bf16 v[122:125], v[168:171], v[184:187], v[122:125]
	v_mfma_f32_16x16x32_bf16 v[114:117], v[176:179], v[184:187], v[114:117]
	v_mfma_f32_16x16x32_bf16 v[102:105], v[168:171], v[192:195], v[102:105]
	v_mfma_f32_16x16x32_bf16 v[98:101], v[176:179], v[192:195], v[98:101]
	v_mfma_f32_16x16x32_bf16 v[86:89], v[168:171], v[200:203], v[86:89]
	v_mfma_f32_16x16x32_bf16 v[82:85], v[176:179], v[200:203], v[82:85]
	v_mfma_f32_16x16x32_bf16 v[70:73], v[168:171], v[216:219], v[70:73]
	v_mfma_f32_16x16x32_bf16 v[66:69], v[176:179], v[216:219], v[66:69]
	s_setprio 0
	s_barrier
	s_add_i32 s82, s84, s70
	v_lshl_add_u64 v[208:209], s[36:37], 0, v[0:1]
	s_mov_b32 m0, s82
	ds_read_b128 v[180:183], v145 offset:16384
	ds_read_b128 v[184:187], v145 offset:17408
	ds_read_b128 v[188:191], v145 offset:18432
	ds_read_b128 v[192:195], v145 offset:19456
	ds_read_b128 v[196:199], v145 offset:20480
	ds_read_b128 v[200:203], v145 offset:21504
	ds_read_b128 v[204:207], v145 offset:22528
	ds_read_b128 v[216:219], v145 offset:23552
	global_load_lds_dwordx4 v[208:209], off
	s_add_i32 m0, s82, 0x2000
	s_add_u32 s82, s36, 0x60000
	v_lshl_add_u64 v[220:221], s[36:37], 0, v[118:119]
	s_addc_u32 s83, s37, 0
	s_add_i32 s84, s85, s70
	global_load_lds_dwordx4 v[220:221], off
	v_lshl_add_u64 v[222:223], s[82:83], 0, v[0:1]
	s_mov_b32 m0, s84
	v_lshl_add_u64 v[224:225], s[44:45], 0, v[120:121]
	global_load_lds_dwordx4 v[222:223], off
	s_add_i32 m0, s84, 0x2000
	v_lshl_add_u64 v[222:223], s[82:83], 0, v[118:119]
	global_load_lds_dwordx4 v[222:223], off
	s_mov_b32 m0, s4
	v_lshl_add_u64 v[222:223], s[44:45], 0, v[126:127]
	global_load_lds_dwordx4 v[222:223], off
	s_mov_b32 m0, s33
	s_nop 0
	global_load_lds_dwordx4 v[224:225], off
	s_waitcnt vmcnt(8) lgkmcnt(0)
	s_barrier
	s_setprio 1
	v_mfma_f32_16x16x32_bf16 v[62:65], v[146:149], v[180:183], v[62:65]
	v_mfma_f32_16x16x32_bf16 v[58:61], v[154:157], v[180:183], v[58:61]
	v_mfma_f32_16x16x32_bf16 v[46:49], v[146:149], v[188:191], v[46:49]
	v_mfma_f32_16x16x32_bf16 v[42:45], v[154:157], v[188:191], v[42:45]
	v_mfma_f32_16x16x32_bf16 v[30:33], v[146:149], v[196:199], v[30:33]
	v_mfma_f32_16x16x32_bf16 v[26:29], v[154:157], v[196:199], v[26:29]
	v_mfma_f32_16x16x32_bf16 v[14:17], v[146:149], v[204:207], v[14:17]
	v_mfma_f32_16x16x32_bf16 v[10:13], v[154:157], v[204:207], v[10:13]
	v_mfma_f32_16x16x32_bf16 v[62:65], v[150:153], v[184:187], v[62:65]
	v_mfma_f32_16x16x32_bf16 v[58:61], v[158:161], v[184:187], v[58:61]
	v_mfma_f32_16x16x32_bf16 v[46:49], v[150:153], v[192:195], v[46:49]
	v_mfma_f32_16x16x32_bf16 v[42:45], v[158:161], v[192:195], v[42:45]
	v_mfma_f32_16x16x32_bf16 v[30:33], v[150:153], v[200:203], v[30:33]
	v_mfma_f32_16x16x32_bf16 v[26:29], v[158:161], v[200:203], v[26:29]
	v_mfma_f32_16x16x32_bf16 v[14:17], v[150:153], v[216:219], v[14:17]
	v_mfma_f32_16x16x32_bf16 v[10:13], v[158:161], v[216:219], v[10:13]
	s_setprio 0
	s_setprio 1
	v_mfma_f32_16x16x32_bf16 v[54:57], v[162:165], v[180:183], v[54:57]
	v_mfma_f32_16x16x32_bf16 v[50:53], v[172:175], v[180:183], v[50:53]
	v_mfma_f32_16x16x32_bf16 v[38:41], v[162:165], v[188:191], v[38:41]
	v_mfma_f32_16x16x32_bf16 v[34:37], v[172:175], v[188:191], v[34:37]
	v_mfma_f32_16x16x32_bf16 v[22:25], v[162:165], v[196:199], v[22:25]
	v_mfma_f32_16x16x32_bf16 v[18:21], v[172:175], v[196:199], v[18:21]
	v_mfma_f32_16x16x32_bf16 v[6:9], v[162:165], v[204:207], v[6:9]
	v_mfma_f32_16x16x32_bf16 v[2:5], v[172:175], v[204:207], v[2:5]
	v_mfma_f32_16x16x32_bf16 v[54:57], v[168:171], v[184:187], v[54:57]
	v_mfma_f32_16x16x32_bf16 v[50:53], v[176:179], v[184:187], v[50:53]
	v_mfma_f32_16x16x32_bf16 v[38:41], v[168:171], v[192:195], v[38:41]
	v_mfma_f32_16x16x32_bf16 v[34:37], v[176:179], v[192:195], v[34:37]
	v_mfma_f32_16x16x32_bf16 v[22:25], v[168:171], v[200:203], v[22:25]
	v_mfma_f32_16x16x32_bf16 v[18:21], v[176:179], v[200:203], v[18:21]
	v_mfma_f32_16x16x32_bf16 v[6:9], v[168:171], v[216:219], v[6:9]
	v_mfma_f32_16x16x32_bf16 v[2:5], v[176:179], v[216:219], v[2:5]
	s_setprio 0
	s_barrier
	s_add_i32 s82, 0, 0x18000
	s_add_i32 s83, 0, 0x1c000
	v_add_u32_e32 v158, s82, v144
	v_add_u32_e32 v176, s83, v144
	ds_read_b128 v[146:149], v158
	ds_read_b128 v[150:153], v158 offset:1024
	ds_read_b128 v[154:157], v158 offset:2048
	ds_read_b128 v[158:161], v158 offset:3072
	ds_read_b128 v[162:165], v176
	ds_read_b128 v[168:171], v176 offset:1024
	ds_read_b128 v[172:175], v176 offset:2048
	ds_read_b128 v[176:179], v176 offset:3072
	s_add_u32 s44, s44, 0x60000
	s_addc_u32 s45, s45, 0
	s_mov_b32 m0, s71
	v_lshl_add_u64 v[242:243], s[44:45], 0, v[126:127]
	ds_read_b128 v[180:183], v145 offset:32768
	ds_read_b128 v[184:187], v145 offset:33792
	ds_read_b128 v[188:191], v145 offset:34816
	ds_read_b128 v[192:195], v145 offset:35840
	ds_read_b128 v[196:199], v145 offset:36864
	ds_read_b128 v[200:203], v145 offset:37888
	ds_read_b128 v[204:207], v145 offset:38912
	ds_read_b128 v[216:219], v145 offset:39936
	global_load_lds_dwordx4 v[242:243], off
	s_mov_b32 m0, s76
	v_lshl_add_u64 v[242:243], s[44:45], 0, v[120:121]
	global_load_lds_dwordx4 v[242:243], off
	s_waitcnt vmcnt(8) lgkmcnt(0)
	s_barrier
	s_setprio 1
	v_mfma_f32_16x16x32_bf16 v[134:137], v[146:149], v[180:183], v[134:137]
	v_mfma_f32_16x16x32_bf16 v[130:133], v[154:157], v[180:183], v[130:133]
	v_mfma_f32_16x16x32_bf16 v[110:113], v[146:149], v[188:191], v[110:113]
	v_mfma_f32_16x16x32_bf16 v[106:109], v[154:157], v[188:191], v[106:109]
	v_mfma_f32_16x16x32_bf16 v[94:97], v[146:149], v[196:199], v[94:97]
	v_mfma_f32_16x16x32_bf16 v[90:93], v[154:157], v[196:199], v[90:93]
	v_mfma_f32_16x16x32_bf16 v[78:81], v[146:149], v[204:207], v[78:81]
	v_mfma_f32_16x16x32_bf16 v[74:77], v[154:157], v[204:207], v[74:77]
	v_mfma_f32_16x16x32_bf16 v[134:137], v[150:153], v[184:187], v[134:137]
	v_mfma_f32_16x16x32_bf16 v[130:133], v[158:161], v[184:187], v[130:133]
	v_mfma_f32_16x16x32_bf16 v[110:113], v[150:153], v[192:195], v[110:113]
	v_mfma_f32_16x16x32_bf16 v[106:109], v[158:161], v[192:195], v[106:109]
	v_mfma_f32_16x16x32_bf16 v[94:97], v[150:153], v[200:203], v[94:97]
	v_mfma_f32_16x16x32_bf16 v[90:93], v[158:161], v[200:203], v[90:93]
	v_mfma_f32_16x16x32_bf16 v[78:81], v[150:153], v[216:219], v[78:81]
	v_mfma_f32_16x16x32_bf16 v[74:77], v[158:161], v[216:219], v[74:77]
	s_setprio 0
	s_setprio 1
	v_mfma_f32_16x16x32_bf16 v[122:125], v[162:165], v[180:183], v[122:125]
	v_mfma_f32_16x16x32_bf16 v[114:117], v[172:175], v[180:183], v[114:117]
	v_mfma_f32_16x16x32_bf16 v[102:105], v[162:165], v[188:191], v[102:105]
	v_mfma_f32_16x16x32_bf16 v[98:101], v[172:175], v[188:191], v[98:101]
	v_mfma_f32_16x16x32_bf16 v[86:89], v[162:165], v[196:199], v[86:89]
	v_mfma_f32_16x16x32_bf16 v[82:85], v[172:175], v[196:199], v[82:85]
	v_mfma_f32_16x16x32_bf16 v[70:73], v[162:165], v[204:207], v[70:73]
	v_mfma_f32_16x16x32_bf16 v[66:69], v[172:175], v[204:207], v[66:69]
	v_mfma_f32_16x16x32_bf16 v[122:125], v[168:171], v[184:187], v[122:125]
	v_mfma_f32_16x16x32_bf16 v[114:117], v[176:179], v[184:187], v[114:117]
	v_mfma_f32_16x16x32_bf16 v[102:105], v[168:171], v[192:195], v[102:105]
	v_mfma_f32_16x16x32_bf16 v[98:101], v[176:179], v[192:195], v[98:101]
	v_mfma_f32_16x16x32_bf16 v[86:89], v[168:171], v[200:203], v[86:89]
	v_mfma_f32_16x16x32_bf16 v[82:85], v[176:179], v[200:203], v[82:85]
	v_mfma_f32_16x16x32_bf16 v[70:73], v[168:171], v[216:219], v[70:73]
	v_mfma_f32_16x16x32_bf16 v[66:69], v[176:179], v[216:219], v[66:69]
	s_setprio 0
	s_barrier
	s_add_i32 s44, s82, s70
	v_lshl_add_u64 v[208:209], v[208:209], 0, s[56:57]
	s_mov_b32 m0, s44
	ds_read_b128 v[180:183], v145 offset:49152
	ds_read_b128 v[184:187], v145 offset:50176
	ds_read_b128 v[188:191], v145 offset:51200
	ds_read_b128 v[192:195], v145 offset:52224
	ds_read_b128 v[196:199], v145 offset:53248
	ds_read_b128 v[200:203], v145 offset:54272
	ds_read_b128 v[204:207], v145 offset:55296
	ds_read_b128 v[216:219], v145 offset:56320
	global_load_lds_dwordx4 v[208:209], off
	s_add_i32 m0, s44, 0x2000
	s_add_u32 s36, s36, 0x60080
	v_lshl_add_u64 v[208:209], v[220:221], 0, s[56:57]
	s_addc_u32 s37, s37, 0
	s_add_i32 s44, s83, s70
	global_load_lds_dwordx4 v[208:209], off
	s_mov_b32 m0, s44
	v_lshl_add_u64 v[208:209], s[36:37], 0, v[0:1]
	global_load_lds_dwordx4 v[208:209], off
	s_add_i32 m0, s44, 0x2000
	v_lshl_add_u64 v[208:209], s[36:37], 0, v[118:119]
	global_load_lds_dwordx4 v[208:209], off
	s_mov_b32 m0, s77
	v_lshl_add_u64 v[208:209], v[222:223], 0, s[56:57]
	global_load_lds_dwordx4 v[208:209], off
	s_mov_b32 m0, s79
	v_lshl_add_u64 v[208:209], v[224:225], 0, s[56:57]
	global_load_lds_dwordx4 v[208:209], off
	s_waitcnt vmcnt(8) lgkmcnt(0)
	s_barrier
	s_setprio 1
	v_mfma_f32_16x16x32_bf16 v[62:65], v[146:149], v[180:183], v[62:65]
	v_mfma_f32_16x16x32_bf16 v[58:61], v[154:157], v[180:183], v[58:61]
	v_mfma_f32_16x16x32_bf16 v[46:49], v[146:149], v[188:191], v[46:49]
	v_mfma_f32_16x16x32_bf16 v[42:45], v[154:157], v[188:191], v[42:45]
	v_mfma_f32_16x16x32_bf16 v[30:33], v[146:149], v[196:199], v[30:33]
	v_mfma_f32_16x16x32_bf16 v[26:29], v[154:157], v[196:199], v[26:29]
	v_mfma_f32_16x16x32_bf16 v[14:17], v[146:149], v[204:207], v[14:17]
	v_mfma_f32_16x16x32_bf16 v[10:13], v[154:157], v[204:207], v[10:13]
	v_mfma_f32_16x16x32_bf16 v[62:65], v[150:153], v[184:187], v[62:65]
	v_mfma_f32_16x16x32_bf16 v[58:61], v[158:161], v[184:187], v[58:61]
	v_mfma_f32_16x16x32_bf16 v[46:49], v[150:153], v[192:195], v[46:49]
	v_mfma_f32_16x16x32_bf16 v[42:45], v[158:161], v[192:195], v[42:45]
	v_mfma_f32_16x16x32_bf16 v[30:33], v[150:153], v[200:203], v[30:33]
	v_mfma_f32_16x16x32_bf16 v[26:29], v[158:161], v[200:203], v[26:29]
	v_mfma_f32_16x16x32_bf16 v[14:17], v[150:153], v[216:219], v[14:17]
	v_mfma_f32_16x16x32_bf16 v[10:13], v[158:161], v[216:219], v[10:13]
	s_setprio 0
	s_setprio 1
	v_mfma_f32_16x16x32_bf16 v[54:57], v[162:165], v[180:183], v[54:57]
	v_mfma_f32_16x16x32_bf16 v[50:53], v[172:175], v[180:183], v[50:53]
	v_mfma_f32_16x16x32_bf16 v[38:41], v[162:165], v[188:191], v[38:41]
	v_mfma_f32_16x16x32_bf16 v[34:37], v[172:175], v[188:191], v[34:37]
	v_mfma_f32_16x16x32_bf16 v[22:25], v[162:165], v[196:199], v[22:25]
	v_mfma_f32_16x16x32_bf16 v[18:21], v[172:175], v[196:199], v[18:21]
	v_mfma_f32_16x16x32_bf16 v[6:9], v[162:165], v[204:207], v[6:9]
	v_mfma_f32_16x16x32_bf16 v[2:5], v[172:175], v[204:207], v[2:5]
	v_mfma_f32_16x16x32_bf16 v[54:57], v[168:171], v[184:187], v[54:57]
	v_mfma_f32_16x16x32_bf16 v[50:53], v[176:179], v[184:187], v[50:53]
	v_mfma_f32_16x16x32_bf16 v[38:41], v[168:171], v[192:195], v[38:41]
	v_mfma_f32_16x16x32_bf16 v[34:37], v[176:179], v[192:195], v[34:37]
	v_mfma_f32_16x16x32_bf16 v[22:25], v[168:171], v[200:203], v[22:25]
	v_mfma_f32_16x16x32_bf16 v[18:21], v[176:179], v[200:203], v[18:21]
	v_mfma_f32_16x16x32_bf16 v[6:9], v[168:171], v[216:219], v[6:9]
	v_mfma_f32_16x16x32_bf16 v[2:5], v[176:179], v[216:219], v[2:5]
	s_setprio 0
	s_barrier
	s_add_i32 s59, s59, 2
	s_add_u32 s34, s34, 0x100
	s_addc_u32 s35, s35, 0
	s_cmp_gt_u32 s59, 21
	s_cbranch_scc0 .LBB0_1525
	s_add_u32 s34, s8, 0xffffff00
	s_addc_u32 s35, s9, -1
	s_and_b64 vcc, exec, s[42:43]
	s_cbranch_vccnz .LBB0_1528
	v_mov_b32_e32 v2, 0
	s_mov_b32 s16, s80
	s_mov_b32 s47, s81
	s_mov_b64 s[26:27], s[30:31]
	s_mov_b32 s68, s58
	v_mov_b32_e32 v3, v2
	v_mov_b32_e32 v4, v2
	v_mov_b32_e32 v5, v2
	v_mov_b32_e32 v6, v2
	v_mov_b32_e32 v7, v2
	v_mov_b32_e32 v8, v2
	v_mov_b32_e32 v9, v2
	v_mov_b32_e32 v18, v2
	v_mov_b32_e32 v19, v2
	v_mov_b32_e32 v20, v2
	v_mov_b32_e32 v21, v2
	v_mov_b32_e32 v22, v2
	v_mov_b32_e32 v23, v2
	v_mov_b32_e32 v24, v2
	v_mov_b32_e32 v25, v2
	v_mov_b32_e32 v34, v2
	v_mov_b32_e32 v35, v2
	v_mov_b32_e32 v36, v2
	v_mov_b32_e32 v37, v2
	v_mov_b32_e32 v38, v2
	v_mov_b32_e32 v39, v2
	v_mov_b32_e32 v40, v2
	v_mov_b32_e32 v41, v2
	v_mov_b32_e32 v50, v2
	v_mov_b32_e32 v51, v2
	v_mov_b32_e32 v52, v2
	v_mov_b32_e32 v53, v2
	v_mov_b32_e32 v54, v2
	v_mov_b32_e32 v55, v2
	v_mov_b32_e32 v56, v2
	v_mov_b32_e32 v57, v2
	v_mov_b32_e32 v10, v2
	v_mov_b32_e32 v11, v2
	v_mov_b32_e32 v12, v2
	v_mov_b32_e32 v13, v2
	v_mov_b32_e32 v14, v2
	v_mov_b32_e32 v15, v2
	v_mov_b32_e32 v16, v2
	v_mov_b32_e32 v17, v2
	v_mov_b32_e32 v26, v2
	v_mov_b32_e32 v27, v2
	v_mov_b32_e32 v28, v2
	v_mov_b32_e32 v29, v2
	v_mov_b32_e32 v30, v2
	v_mov_b32_e32 v31, v2
	v_mov_b32_e32 v32, v2
	v_mov_b32_e32 v33, v2
	v_mov_b32_e32 v42, v2
	v_mov_b32_e32 v43, v2
	v_mov_b32_e32 v44, v2
	v_mov_b32_e32 v45, v2
	v_mov_b32_e32 v46, v2
	v_mov_b32_e32 v47, v2
	v_mov_b32_e32 v48, v2
	v_mov_b32_e32 v49, v2
	v_mov_b32_e32 v58, v2
	v_mov_b32_e32 v59, v2
	v_mov_b32_e32 v60, v2
	v_mov_b32_e32 v61, v2
	v_mov_b32_e32 v62, v2
	v_mov_b32_e32 v63, v2
	v_mov_b32_e32 v64, v2
	v_mov_b32_e32 v65, v2
	v_mov_b32_e32 v66, v2
	v_mov_b32_e32 v67, v2
	v_mov_b32_e32 v68, v2
	v_mov_b32_e32 v69, v2
	v_mov_b32_e32 v70, v2
	v_mov_b32_e32 v71, v2
	v_mov_b32_e32 v72, v2
	v_mov_b32_e32 v73, v2
	v_mov_b32_e32 v82, v2
	v_mov_b32_e32 v83, v2
	v_mov_b32_e32 v84, v2
	v_mov_b32_e32 v85, v2
	v_mov_b32_e32 v86, v2
	v_mov_b32_e32 v87, v2
	v_mov_b32_e32 v88, v2
	v_mov_b32_e32 v89, v2
	v_mov_b32_e32 v98, v2
	v_mov_b32_e32 v99, v2
	v_mov_b32_e32 v100, v2
	v_mov_b32_e32 v101, v2
	v_mov_b32_e32 v102, v2
	v_mov_b32_e32 v103, v2
	v_mov_b32_e32 v104, v2
	v_mov_b32_e32 v105, v2
	v_mov_b32_e32 v114, v2
	v_mov_b32_e32 v115, v2
	v_mov_b32_e32 v116, v2
	v_mov_b32_e32 v117, v2
	v_mov_b32_e32 v122, v2
	v_mov_b32_e32 v123, v2
	v_mov_b32_e32 v124, v2
	v_mov_b32_e32 v125, v2
	v_mov_b32_e32 v74, v2
	v_mov_b32_e32 v75, v2
	v_mov_b32_e32 v76, v2
	v_mov_b32_e32 v77, v2
	v_mov_b32_e32 v78, v2
	v_mov_b32_e32 v79, v2
	v_mov_b32_e32 v80, v2
	v_mov_b32_e32 v81, v2
	v_mov_b32_e32 v90, v2
	v_mov_b32_e32 v91, v2
	v_mov_b32_e32 v92, v2
	v_mov_b32_e32 v93, v2
	v_mov_b32_e32 v94, v2
	v_mov_b32_e32 v95, v2
	v_mov_b32_e32 v96, v2
	v_mov_b32_e32 v97, v2
	v_mov_b32_e32 v106, v2
	v_mov_b32_e32 v107, v2
	v_mov_b32_e32 v108, v2
	v_mov_b32_e32 v109, v2
	v_mov_b32_e32 v110, v2
	v_mov_b32_e32 v111, v2
	v_mov_b32_e32 v112, v2
	v_mov_b32_e32 v113, v2
	v_mov_b32_e32 v130, v2
	v_mov_b32_e32 v131, v2
	v_mov_b32_e32 v132, v2
	v_mov_b32_e32 v133, v2
	v_mov_b32_e32 v134, v2
	v_mov_b32_e32 v135, v2
	v_mov_b32_e32 v136, v2
	v_mov_b32_e32 v137, v2
	s_andn2_b64 vcc, exec, s[40:41]
	s_cbranch_vccnz .LBB0_1529
	s_branch .LBB0_1531

.LBB0_1623:
	s_add_u32 s36, s26, s34
	s_addc_u32 s37, s27, s35
	s_add_u32 s36, s36, 0x100
	s_addc_u32 s37, s37, 0
	s_add_u32 s80, s8, s34
	s_addc_u32 s81, s9, s35
	s_add_i32 s82, 0, 0x10000
	s_cmpk_eq_i32 s34, 0xb00
	s_cselect_b32 s43, s31, s37
	s_cselect_b32 s42, s30, s36
	s_cselect_b32 s37, s29, s81
	s_cselect_b32 s36, s28, s80
	s_add_i32 s83, 0, 0x14000
	v_add_u32_e32 v158, s82, v144
	v_add_u32_e32 v167, s83, v144
	ds_read_b128 v[146:149], v158
	ds_read_b128 v[150:153], v158 offset:1024
	ds_read_b128 v[154:157], v158 offset:2048
	ds_read_b128 v[158:161], v158 offset:3072
	ds_read_b128 v[162:165], v167
	ds_read_b128 v[168:171], v167 offset:1024
	ds_read_b128 v[172:175], v167 offset:2048
	ds_read_b128 v[176:179], v167 offset:3072
	v_lshl_add_u64 v[208:209], v[142:143], 0, s[34:35]
	s_add_i32 m0, s4, 0xc000
	ds_read_b128 v[180:183], v145
	ds_read_b128 v[184:187], v145 offset:1024
	ds_read_b128 v[188:191], v145 offset:2048
	ds_read_b128 v[192:195], v145 offset:3072
	ds_read_b128 v[196:199], v145 offset:4096
	ds_read_b128 v[200:203], v145 offset:5120
	ds_read_b128 v[204:207], v145 offset:6144
	ds_read_b128 v[216:219], v145 offset:7168
	global_load_lds_dwordx4 v[208:209], off
	s_add_i32 m0, s4, 0xe000
	v_lshl_add_u64 v[208:209], v[140:141], 0, s[34:35]
	global_load_lds_dwordx4 v[208:209], off
	s_waitcnt vmcnt(8) lgkmcnt(0)
	s_barrier
	s_setprio 1
	v_mfma_f32_16x16x32_bf16 v[134:137], v[146:149], v[180:183], v[134:137]
	v_mfma_f32_16x16x32_bf16 v[130:133], v[154:157], v[180:183], v[130:133]
	v_mfma_f32_16x16x32_bf16 v[110:113], v[146:149], v[188:191], v[110:113]
	v_mfma_f32_16x16x32_bf16 v[106:109], v[154:157], v[188:191], v[106:109]
	v_mfma_f32_16x16x32_bf16 v[94:97], v[146:149], v[196:199], v[94:97]
	v_mfma_f32_16x16x32_bf16 v[90:93], v[154:157], v[196:199], v[90:93]
	v_mfma_f32_16x16x32_bf16 v[78:81], v[146:149], v[204:207], v[78:81]
	v_mfma_f32_16x16x32_bf16 v[74:77], v[154:157], v[204:207], v[74:77]
	v_mfma_f32_16x16x32_bf16 v[134:137], v[150:153], v[184:187], v[134:137]
	v_mfma_f32_16x16x32_bf16 v[130:133], v[158:161], v[184:187], v[130:133]
	v_mfma_f32_16x16x32_bf16 v[110:113], v[150:153], v[192:195], v[110:113]
	v_mfma_f32_16x16x32_bf16 v[106:109], v[158:161], v[192:195], v[106:109]
	v_mfma_f32_16x16x32_bf16 v[94:97], v[150:153], v[200:203], v[94:97]
	v_mfma_f32_16x16x32_bf16 v[90:93], v[158:161], v[200:203], v[90:93]
	v_mfma_f32_16x16x32_bf16 v[78:81], v[150:153], v[216:219], v[78:81]
	v_mfma_f32_16x16x32_bf16 v[74:77], v[158:161], v[216:219], v[74:77]
	s_setprio 0
	s_setprio 1
	v_mfma_f32_16x16x32_bf16 v[122:125], v[162:165], v[180:183], v[122:125]
	v_mfma_f32_16x16x32_bf16 v[114:117], v[172:175], v[180:183], v[114:117]
	v_mfma_f32_16x16x32_bf16 v[102:105], v[162:165], v[188:191], v[102:105]
	v_mfma_f32_16x16x32_bf16 v[98:101], v[172:175], v[188:191], v[98:101]
	v_mfma_f32_16x16x32_bf16 v[86:89], v[162:165], v[196:199], v[86:89]
	v_mfma_f32_16x16x32_bf16 v[82:85], v[172:175], v[196:199], v[82:85]
	v_mfma_f32_16x16x32_bf16 v[70:73], v[162:165], v[204:207], v[70:73]
	v_mfma_f32_16x16x32_bf16 v[66:69], v[172:175], v[204:207], v[66:69]
	v_mfma_f32_16x16x32_bf16 v[122:125], v[168:171], v[184:187], v[122:125]
	v_mfma_f32_16x16x32_bf16 v[114:117], v[176:179], v[184:187], v[114:117]
	v_mfma_f32_16x16x32_bf16 v[102:105], v[168:171], v[192:195], v[102:105]
	v_mfma_f32_16x16x32_bf16 v[98:101], v[176:179], v[192:195], v[98:101]
	v_mfma_f32_16x16x32_bf16 v[86:89], v[168:171], v[200:203], v[86:89]
	v_mfma_f32_16x16x32_bf16 v[82:85], v[176:179], v[200:203], v[82:85]
	v_mfma_f32_16x16x32_bf16 v[70:73], v[168:171], v[216:219], v[70:73]
	v_mfma_f32_16x16x32_bf16 v[66:69], v[176:179], v[216:219], v[66:69]
	s_setprio 0
	s_barrier
	s_add_i32 s80, s82, s53
	v_lshl_add_u64 v[208:209], s[36:37], 0, v[0:1]
	s_mov_b32 m0, s80
	ds_read_b128 v[180:183], v145 offset:16384
	ds_read_b128 v[184:187], v145 offset:17408
	ds_read_b128 v[188:191], v145 offset:18432
	ds_read_b128 v[192:195], v145 offset:19456
	ds_read_b128 v[196:199], v145 offset:20480
	ds_read_b128 v[200:203], v145 offset:21504
	ds_read_b128 v[204:207], v145 offset:22528
	ds_read_b128 v[216:219], v145 offset:23552
	global_load_lds_dwordx4 v[208:209], off
	s_add_i32 m0, s80, 0x2000
	s_add_u32 s80, s36, 0x60000
	v_lshl_add_u64 v[220:221], s[36:37], 0, v[118:119]
	s_addc_u32 s81, s37, 0
	s_add_i32 s82, s83, s53
	global_load_lds_dwordx4 v[220:221], off
	v_lshl_add_u64 v[222:223], s[80:81], 0, v[0:1]
	s_mov_b32 m0, s82
	v_lshl_add_u64 v[224:225], s[42:43], 0, v[120:121]
	global_load_lds_dwordx4 v[222:223], off
	s_add_i32 m0, s82, 0x2000
	v_lshl_add_u64 v[222:223], s[80:81], 0, v[118:119]
	global_load_lds_dwordx4 v[222:223], off
	s_mov_b32 m0, s4
	v_lshl_add_u64 v[222:223], s[42:43], 0, v[126:127]
	global_load_lds_dwordx4 v[222:223], off
	s_mov_b32 m0, s33
	s_nop 0
	global_load_lds_dwordx4 v[224:225], off
	s_waitcnt vmcnt(8) lgkmcnt(0)
	s_barrier
	s_setprio 1
	v_mfma_f32_16x16x32_bf16 v[62:65], v[146:149], v[180:183], v[62:65]
	v_mfma_f32_16x16x32_bf16 v[58:61], v[154:157], v[180:183], v[58:61]
	v_mfma_f32_16x16x32_bf16 v[46:49], v[146:149], v[188:191], v[46:49]
	v_mfma_f32_16x16x32_bf16 v[42:45], v[154:157], v[188:191], v[42:45]
	v_mfma_f32_16x16x32_bf16 v[30:33], v[146:149], v[196:199], v[30:33]
	v_mfma_f32_16x16x32_bf16 v[26:29], v[154:157], v[196:199], v[26:29]
	v_mfma_f32_16x16x32_bf16 v[14:17], v[146:149], v[204:207], v[14:17]
	v_mfma_f32_16x16x32_bf16 v[10:13], v[154:157], v[204:207], v[10:13]
	v_mfma_f32_16x16x32_bf16 v[62:65], v[150:153], v[184:187], v[62:65]
	v_mfma_f32_16x16x32_bf16 v[58:61], v[158:161], v[184:187], v[58:61]
	v_mfma_f32_16x16x32_bf16 v[46:49], v[150:153], v[192:195], v[46:49]
	v_mfma_f32_16x16x32_bf16 v[42:45], v[158:161], v[192:195], v[42:45]
	v_mfma_f32_16x16x32_bf16 v[30:33], v[150:153], v[200:203], v[30:33]
	v_mfma_f32_16x16x32_bf16 v[26:29], v[158:161], v[200:203], v[26:29]
	v_mfma_f32_16x16x32_bf16 v[14:17], v[150:153], v[216:219], v[14:17]
	v_mfma_f32_16x16x32_bf16 v[10:13], v[158:161], v[216:219], v[10:13]
	s_setprio 0
	s_setprio 1
	v_mfma_f32_16x16x32_bf16 v[54:57], v[162:165], v[180:183], v[54:57]
	v_mfma_f32_16x16x32_bf16 v[50:53], v[172:175], v[180:183], v[50:53]
	v_mfma_f32_16x16x32_bf16 v[38:41], v[162:165], v[188:191], v[38:41]
	v_mfma_f32_16x16x32_bf16 v[34:37], v[172:175], v[188:191], v[34:37]
	v_mfma_f32_16x16x32_bf16 v[22:25], v[162:165], v[196:199], v[22:25]
	v_mfma_f32_16x16x32_bf16 v[18:21], v[172:175], v[196:199], v[18:21]
	v_mfma_f32_16x16x32_bf16 v[6:9], v[162:165], v[204:207], v[6:9]
	v_mfma_f32_16x16x32_bf16 v[2:5], v[172:175], v[204:207], v[2:5]
	v_mfma_f32_16x16x32_bf16 v[54:57], v[168:171], v[184:187], v[54:57]
	v_mfma_f32_16x16x32_bf16 v[50:53], v[176:179], v[184:187], v[50:53]
	v_mfma_f32_16x16x32_bf16 v[38:41], v[168:171], v[192:195], v[38:41]
	v_mfma_f32_16x16x32_bf16 v[34:37], v[176:179], v[192:195], v[34:37]
	v_mfma_f32_16x16x32_bf16 v[22:25], v[168:171], v[200:203], v[22:25]
	v_mfma_f32_16x16x32_bf16 v[18:21], v[176:179], v[200:203], v[18:21]
	v_mfma_f32_16x16x32_bf16 v[6:9], v[168:171], v[216:219], v[6:9]
	v_mfma_f32_16x16x32_bf16 v[2:5], v[176:179], v[216:219], v[2:5]
	s_setprio 0
	s_barrier
	s_add_i32 s80, 0, 0x18000
	s_add_i32 s81, 0, 0x1c000
	v_add_u32_e32 v158, s80, v144
	v_add_u32_e32 v167, s81, v144
	ds_read_b128 v[146:149], v158
	ds_read_b128 v[150:153], v158 offset:1024
	ds_read_b128 v[154:157], v158 offset:2048
	ds_read_b128 v[158:161], v158 offset:3072
	ds_read_b128 v[162:165], v167
	ds_read_b128 v[168:171], v167 offset:1024
	ds_read_b128 v[172:175], v167 offset:2048
	ds_read_b128 v[176:179], v167 offset:3072
	s_add_u32 s42, s42, 0x60000
	s_addc_u32 s43, s43, 0
	s_mov_b32 m0, s62
	v_lshl_add_u64 v[242:243], s[42:43], 0, v[126:127]
	ds_read_b128 v[180:183], v145 offset:32768
	ds_read_b128 v[184:187], v145 offset:33792
	ds_read_b128 v[188:191], v145 offset:34816
	ds_read_b128 v[192:195], v145 offset:35840
	ds_read_b128 v[196:199], v145 offset:36864
	ds_read_b128 v[200:203], v145 offset:37888
	ds_read_b128 v[204:207], v145 offset:38912
	ds_read_b128 v[216:219], v145 offset:39936
	global_load_lds_dwordx4 v[242:243], off
	s_mov_b32 m0, s63
	v_lshl_add_u64 v[242:243], s[42:43], 0, v[120:121]
	global_load_lds_dwordx4 v[242:243], off
	s_waitcnt vmcnt(8) lgkmcnt(0)
	s_barrier
	s_setprio 1
	v_mfma_f32_16x16x32_bf16 v[134:137], v[146:149], v[180:183], v[134:137]
	v_mfma_f32_16x16x32_bf16 v[130:133], v[154:157], v[180:183], v[130:133]
	v_mfma_f32_16x16x32_bf16 v[110:113], v[146:149], v[188:191], v[110:113]
	v_mfma_f32_16x16x32_bf16 v[106:109], v[154:157], v[188:191], v[106:109]
	v_mfma_f32_16x16x32_bf16 v[94:97], v[146:149], v[196:199], v[94:97]
	v_mfma_f32_16x16x32_bf16 v[90:93], v[154:157], v[196:199], v[90:93]
	v_mfma_f32_16x16x32_bf16 v[78:81], v[146:149], v[204:207], v[78:81]
	v_mfma_f32_16x16x32_bf16 v[74:77], v[154:157], v[204:207], v[74:77]
	v_mfma_f32_16x16x32_bf16 v[134:137], v[150:153], v[184:187], v[134:137]
	v_mfma_f32_16x16x32_bf16 v[130:133], v[158:161], v[184:187], v[130:133]
	v_mfma_f32_16x16x32_bf16 v[110:113], v[150:153], v[192:195], v[110:113]
	v_mfma_f32_16x16x32_bf16 v[106:109], v[158:161], v[192:195], v[106:109]
	v_mfma_f32_16x16x32_bf16 v[94:97], v[150:153], v[200:203], v[94:97]
	v_mfma_f32_16x16x32_bf16 v[90:93], v[158:161], v[200:203], v[90:93]
	v_mfma_f32_16x16x32_bf16 v[78:81], v[150:153], v[216:219], v[78:81]
	v_mfma_f32_16x16x32_bf16 v[74:77], v[158:161], v[216:219], v[74:77]
	s_setprio 0
	s_setprio 1
	v_mfma_f32_16x16x32_bf16 v[122:125], v[162:165], v[180:183], v[122:125]
	v_mfma_f32_16x16x32_bf16 v[114:117], v[172:175], v[180:183], v[114:117]
	v_mfma_f32_16x16x32_bf16 v[102:105], v[162:165], v[188:191], v[102:105]
	v_mfma_f32_16x16x32_bf16 v[98:101], v[172:175], v[188:191], v[98:101]
	v_mfma_f32_16x16x32_bf16 v[86:89], v[162:165], v[196:199], v[86:89]
	v_mfma_f32_16x16x32_bf16 v[82:85], v[172:175], v[196:199], v[82:85]
	v_mfma_f32_16x16x32_bf16 v[70:73], v[162:165], v[204:207], v[70:73]
	v_mfma_f32_16x16x32_bf16 v[66:69], v[172:175], v[204:207], v[66:69]
	v_mfma_f32_16x16x32_bf16 v[122:125], v[168:171], v[184:187], v[122:125]
	v_mfma_f32_16x16x32_bf16 v[114:117], v[176:179], v[184:187], v[114:117]
	v_mfma_f32_16x16x32_bf16 v[102:105], v[168:171], v[192:195], v[102:105]
	v_mfma_f32_16x16x32_bf16 v[98:101], v[176:179], v[192:195], v[98:101]
	v_mfma_f32_16x16x32_bf16 v[86:89], v[168:171], v[200:203], v[86:89]
	v_mfma_f32_16x16x32_bf16 v[82:85], v[176:179], v[200:203], v[82:85]
	v_mfma_f32_16x16x32_bf16 v[70:73], v[168:171], v[216:219], v[70:73]
	v_mfma_f32_16x16x32_bf16 v[66:69], v[176:179], v[216:219], v[66:69]
	s_setprio 0
	s_barrier
	s_add_i32 s42, s80, s53
	v_lshl_add_u64 v[208:209], v[208:209], 0, s[56:57]
	s_mov_b32 m0, s42
	ds_read_b128 v[180:183], v145 offset:49152
	ds_read_b128 v[184:187], v145 offset:50176
	ds_read_b128 v[188:191], v145 offset:51200
	ds_read_b128 v[192:195], v145 offset:52224
	ds_read_b128 v[196:199], v145 offset:53248
	ds_read_b128 v[200:203], v145 offset:54272
	ds_read_b128 v[204:207], v145 offset:55296
	ds_read_b128 v[216:219], v145 offset:56320
	global_load_lds_dwordx4 v[208:209], off
	s_add_i32 m0, s42, 0x2000
	s_add_u32 s36, s36, 0x60080
	v_lshl_add_u64 v[208:209], v[220:221], 0, s[56:57]
	s_addc_u32 s37, s37, 0
	s_add_i32 s42, s81, s53
	global_load_lds_dwordx4 v[208:209], off
	s_mov_b32 m0, s42
	v_lshl_add_u64 v[208:209], s[36:37], 0, v[0:1]
	global_load_lds_dwordx4 v[208:209], off
	s_add_i32 m0, s42, 0x2000
	v_lshl_add_u64 v[208:209], s[36:37], 0, v[118:119]
	global_load_lds_dwordx4 v[208:209], off
	s_mov_b32 m0, s70
	v_lshl_add_u64 v[208:209], v[222:223], 0, s[56:57]
	global_load_lds_dwordx4 v[208:209], off
	s_mov_b32 m0, s71
	v_lshl_add_u64 v[208:209], v[224:225], 0, s[56:57]
	global_load_lds_dwordx4 v[208:209], off
	s_waitcnt vmcnt(8) lgkmcnt(0)
	s_barrier
	s_setprio 1
	v_mfma_f32_16x16x32_bf16 v[62:65], v[146:149], v[180:183], v[62:65]
	v_mfma_f32_16x16x32_bf16 v[58:61], v[154:157], v[180:183], v[58:61]
	v_mfma_f32_16x16x32_bf16 v[46:49], v[146:149], v[188:191], v[46:49]
	v_mfma_f32_16x16x32_bf16 v[42:45], v[154:157], v[188:191], v[42:45]
	v_mfma_f32_16x16x32_bf16 v[30:33], v[146:149], v[196:199], v[30:33]
	v_mfma_f32_16x16x32_bf16 v[26:29], v[154:157], v[196:199], v[26:29]
	v_mfma_f32_16x16x32_bf16 v[14:17], v[146:149], v[204:207], v[14:17]
	v_mfma_f32_16x16x32_bf16 v[10:13], v[154:157], v[204:207], v[10:13]
	v_mfma_f32_16x16x32_bf16 v[62:65], v[150:153], v[184:187], v[62:65]
	v_mfma_f32_16x16x32_bf16 v[58:61], v[158:161], v[184:187], v[58:61]
	v_mfma_f32_16x16x32_bf16 v[46:49], v[150:153], v[192:195], v[46:49]
	v_mfma_f32_16x16x32_bf16 v[42:45], v[158:161], v[192:195], v[42:45]
	v_mfma_f32_16x16x32_bf16 v[30:33], v[150:153], v[200:203], v[30:33]
	v_mfma_f32_16x16x32_bf16 v[26:29], v[158:161], v[200:203], v[26:29]
	v_mfma_f32_16x16x32_bf16 v[14:17], v[150:153], v[216:219], v[14:17]
	v_mfma_f32_16x16x32_bf16 v[10:13], v[158:161], v[216:219], v[10:13]
	s_setprio 0
	s_setprio 1
	v_mfma_f32_16x16x32_bf16 v[54:57], v[162:165], v[180:183], v[54:57]
	v_mfma_f32_16x16x32_bf16 v[50:53], v[172:175], v[180:183], v[50:53]
	v_mfma_f32_16x16x32_bf16 v[38:41], v[162:165], v[188:191], v[38:41]
	v_mfma_f32_16x16x32_bf16 v[34:37], v[172:175], v[188:191], v[34:37]
	v_mfma_f32_16x16x32_bf16 v[22:25], v[162:165], v[196:199], v[22:25]
	v_mfma_f32_16x16x32_bf16 v[18:21], v[172:175], v[196:199], v[18:21]
	v_mfma_f32_16x16x32_bf16 v[6:9], v[162:165], v[204:207], v[6:9]
	v_mfma_f32_16x16x32_bf16 v[2:5], v[172:175], v[204:207], v[2:5]
	v_mfma_f32_16x16x32_bf16 v[54:57], v[168:171], v[184:187], v[54:57]
	v_mfma_f32_16x16x32_bf16 v[50:53], v[176:179], v[184:187], v[50:53]
	v_mfma_f32_16x16x32_bf16 v[38:41], v[168:171], v[192:195], v[38:41]
	v_mfma_f32_16x16x32_bf16 v[34:37], v[176:179], v[192:195], v[34:37]
	v_mfma_f32_16x16x32_bf16 v[22:25], v[168:171], v[200:203], v[22:25]
	v_mfma_f32_16x16x32_bf16 v[18:21], v[176:179], v[200:203], v[18:21]
	v_mfma_f32_16x16x32_bf16 v[6:9], v[168:171], v[216:219], v[6:9]
	v_mfma_f32_16x16x32_bf16 v[2:5], v[176:179], v[216:219], v[2:5]
	s_setprio 0
	s_barrier
	s_add_i32 s59, s59, 2
	s_add_u32 s34, s34, 0x100
	s_addc_u32 s35, s35, 0
	s_cmp_gt_u32 s59, 21
	s_cbranch_scc0 .LBB0_1623
	s_add_u32 s34, s8, 0xffffff00
	s_addc_u32 s35, s9, -1
	s_and_b64 vcc, exec, s[40:41]
	s_cbranch_vccnz .LBB0_1626
	v_mov_b32_e32 v2, 0
	s_mov_b32 s16, s77
	s_mov_b32 s76, s79
	s_mov_b64 s[26:27], s[30:31]
	s_mov_b32 s68, s58
	v_mov_b32_e32 v3, v2
	v_mov_b32_e32 v4, v2
	v_mov_b32_e32 v5, v2
	v_mov_b32_e32 v6, v2
	v_mov_b32_e32 v7, v2
	v_mov_b32_e32 v8, v2
	v_mov_b32_e32 v9, v2
	v_mov_b32_e32 v18, v2
	v_mov_b32_e32 v19, v2
	v_mov_b32_e32 v20, v2
	v_mov_b32_e32 v21, v2
	v_mov_b32_e32 v22, v2
	v_mov_b32_e32 v23, v2
	v_mov_b32_e32 v24, v2
	v_mov_b32_e32 v25, v2
	v_mov_b32_e32 v34, v2
	v_mov_b32_e32 v35, v2
	v_mov_b32_e32 v36, v2
	v_mov_b32_e32 v37, v2
	v_mov_b32_e32 v38, v2
	v_mov_b32_e32 v39, v2
	v_mov_b32_e32 v40, v2
	v_mov_b32_e32 v41, v2
	v_mov_b32_e32 v50, v2
	v_mov_b32_e32 v51, v2
	v_mov_b32_e32 v52, v2
	v_mov_b32_e32 v53, v2
	v_mov_b32_e32 v54, v2
	v_mov_b32_e32 v55, v2
	v_mov_b32_e32 v56, v2
	v_mov_b32_e32 v57, v2
	v_mov_b32_e32 v10, v2
	v_mov_b32_e32 v11, v2
	v_mov_b32_e32 v12, v2
	v_mov_b32_e32 v13, v2
	v_mov_b32_e32 v14, v2
	v_mov_b32_e32 v15, v2
	v_mov_b32_e32 v16, v2
	v_mov_b32_e32 v17, v2
	v_mov_b32_e32 v26, v2
	v_mov_b32_e32 v27, v2
	v_mov_b32_e32 v28, v2
	v_mov_b32_e32 v29, v2
	v_mov_b32_e32 v30, v2
	v_mov_b32_e32 v31, v2
	v_mov_b32_e32 v32, v2
	v_mov_b32_e32 v33, v2
	v_mov_b32_e32 v42, v2
	v_mov_b32_e32 v43, v2
	v_mov_b32_e32 v44, v2
	v_mov_b32_e32 v45, v2
	v_mov_b32_e32 v46, v2
	v_mov_b32_e32 v47, v2
	v_mov_b32_e32 v48, v2
	v_mov_b32_e32 v49, v2
	v_mov_b32_e32 v58, v2
	v_mov_b32_e32 v59, v2
	v_mov_b32_e32 v60, v2
	v_mov_b32_e32 v61, v2
	v_mov_b32_e32 v62, v2
	v_mov_b32_e32 v63, v2
	v_mov_b32_e32 v64, v2
	v_mov_b32_e32 v65, v2
	v_mov_b32_e32 v66, v2
	v_mov_b32_e32 v67, v2
	v_mov_b32_e32 v68, v2
	v_mov_b32_e32 v69, v2
	v_mov_b32_e32 v70, v2
	v_mov_b32_e32 v71, v2
	v_mov_b32_e32 v72, v2
	v_mov_b32_e32 v73, v2
	v_mov_b32_e32 v82, v2
	v_mov_b32_e32 v83, v2
	v_mov_b32_e32 v84, v2
	v_mov_b32_e32 v85, v2
	v_mov_b32_e32 v86, v2
	v_mov_b32_e32 v87, v2
	v_mov_b32_e32 v88, v2
	v_mov_b32_e32 v89, v2
	v_mov_b32_e32 v98, v2
	v_mov_b32_e32 v99, v2
	v_mov_b32_e32 v100, v2
	v_mov_b32_e32 v101, v2
	v_mov_b32_e32 v102, v2
	v_mov_b32_e32 v103, v2
	v_mov_b32_e32 v104, v2
	v_mov_b32_e32 v105, v2
	v_mov_b32_e32 v114, v2
	v_mov_b32_e32 v115, v2
	v_mov_b32_e32 v116, v2
	v_mov_b32_e32 v117, v2
	v_mov_b32_e32 v122, v2
	v_mov_b32_e32 v123, v2
	v_mov_b32_e32 v124, v2
	v_mov_b32_e32 v125, v2
	v_mov_b32_e32 v74, v2
	v_mov_b32_e32 v75, v2
	v_mov_b32_e32 v76, v2
	v_mov_b32_e32 v77, v2
	v_mov_b32_e32 v78, v2
	v_mov_b32_e32 v79, v2
	v_mov_b32_e32 v80, v2
	v_mov_b32_e32 v81, v2
	v_mov_b32_e32 v90, v2
	v_mov_b32_e32 v91, v2
	v_mov_b32_e32 v92, v2
	v_mov_b32_e32 v93, v2
	v_mov_b32_e32 v94, v2
	v_mov_b32_e32 v95, v2
	v_mov_b32_e32 v96, v2
	v_mov_b32_e32 v97, v2
	v_mov_b32_e32 v106, v2
	v_mov_b32_e32 v107, v2
	v_mov_b32_e32 v108, v2
	v_mov_b32_e32 v109, v2
	v_mov_b32_e32 v110, v2
	v_mov_b32_e32 v111, v2
	v_mov_b32_e32 v112, v2
	v_mov_b32_e32 v113, v2
	v_mov_b32_e32 v130, v2
	v_mov_b32_e32 v131, v2
	v_mov_b32_e32 v132, v2
	v_mov_b32_e32 v133, v2
	v_mov_b32_e32 v134, v2
	v_mov_b32_e32 v135, v2
	v_mov_b32_e32 v136, v2
	v_mov_b32_e32 v137, v2
	s_andn2_b64 vcc, exec, s[38:39]
	s_cbranch_vccnz .LBB0_1627
	s_branch .LBB0_1628

.LBB0_1783:
	s_add_u32 s28, s6, 0xfffc0080
	s_addc_u32 s29, s7, -1
	s_add_i32 s53, 0, 0x10000
	s_cmp_eq_u32 s41, 12
	s_cselect_b32 s31, s8, s29
	s_cselect_b32 s30, s9, s28
	s_cselect_b32 s29, s21, s40
	s_cselect_b32 s28, s23, s33
	s_add_i32 s62, 0, 0x14000
	v_add_u32_e32 v142, s53, v181
	v_add_u32_e32 v168, s62, v181
	ds_read_b128 v[130:133], v142
	ds_read_b128 v[134:137], v142 offset:1024
	ds_read_b128 v[138:141], v142 offset:2048
	ds_read_b128 v[142:145], v142 offset:3072
	ds_read_b128 v[146:149], v168
	ds_read_b128 v[150:153], v168 offset:1024
	ds_read_b128 v[154:157], v168 offset:2048
	ds_read_b128 v[168:171], v168 offset:3072
	v_lshl_add_u64 v[176:177], s[6:7], 0, v[166:167]
	s_add_i32 m0, s37, 0xc000
	ds_read_b128 v[172:175], v183
	ds_read_b128 v[184:187], v183 offset:1024
	ds_read_b128 v[188:191], v183 offset:2048
	ds_read_b128 v[192:195], v183 offset:3072
	ds_read_b128 v[196:199], v183 offset:4096
	ds_read_b128 v[200:203], v183 offset:5120
	ds_read_b128 v[204:207], v183 offset:6144
	ds_read_b128 v[216:219], v183 offset:7168
	global_load_lds_dwordx4 v[176:177], off
	s_add_i32 m0, s37, 0xe000
	v_lshl_add_u64 v[176:177], s[6:7], 0, v[164:165]
	global_load_lds_dwordx4 v[176:177], off
	s_waitcnt vmcnt(8) lgkmcnt(0)
	s_barrier
	s_setprio 1
	v_mfma_f32_16x16x32_bf16 v[126:129], v[130:133], v[172:175], v[126:129]
	v_mfma_f32_16x16x32_bf16 v[122:125], v[138:141], v[172:175], v[122:125]
	v_mfma_f32_16x16x32_bf16 v[114:117], v[130:133], v[188:191], v[114:117]
	v_mfma_f32_16x16x32_bf16 v[106:109], v[138:141], v[188:191], v[106:109]
	v_mfma_f32_16x16x32_bf16 v[98:101], v[130:133], v[196:199], v[98:101]
	v_mfma_f32_16x16x32_bf16 v[90:93], v[138:141], v[196:199], v[90:93]
	v_mfma_f32_16x16x32_bf16 v[82:85], v[130:133], v[204:207], v[82:85]
	v_mfma_f32_16x16x32_bf16 v[74:77], v[138:141], v[204:207], v[74:77]
	v_mfma_f32_16x16x32_bf16 v[126:129], v[134:137], v[184:187], v[126:129]
	v_mfma_f32_16x16x32_bf16 v[122:125], v[142:145], v[184:187], v[122:125]
	v_mfma_f32_16x16x32_bf16 v[114:117], v[134:137], v[192:195], v[114:117]
	v_mfma_f32_16x16x32_bf16 v[106:109], v[142:145], v[192:195], v[106:109]
	v_mfma_f32_16x16x32_bf16 v[98:101], v[134:137], v[200:203], v[98:101]
	v_mfma_f32_16x16x32_bf16 v[90:93], v[142:145], v[200:203], v[90:93]
	v_mfma_f32_16x16x32_bf16 v[82:85], v[134:137], v[216:219], v[82:85]
	v_mfma_f32_16x16x32_bf16 v[74:77], v[142:145], v[216:219], v[74:77]
	s_setprio 0
	s_setprio 1
	v_mfma_f32_16x16x32_bf16 v[118:121], v[146:149], v[172:175], v[118:121]
	v_mfma_f32_16x16x32_bf16 v[110:113], v[154:157], v[172:175], v[110:113]
	v_mfma_f32_16x16x32_bf16 v[102:105], v[146:149], v[188:191], v[102:105]
	v_mfma_f32_16x16x32_bf16 v[94:97], v[154:157], v[188:191], v[94:97]
	v_mfma_f32_16x16x32_bf16 v[86:89], v[146:149], v[196:199], v[86:89]
	v_mfma_f32_16x16x32_bf16 v[78:81], v[154:157], v[196:199], v[78:81]
	v_mfma_f32_16x16x32_bf16 v[70:73], v[146:149], v[204:207], v[70:73]
	v_mfma_f32_16x16x32_bf16 v[66:69], v[154:157], v[204:207], v[66:69]
	v_mfma_f32_16x16x32_bf16 v[118:121], v[150:153], v[184:187], v[118:121]
	v_mfma_f32_16x16x32_bf16 v[110:113], v[168:171], v[184:187], v[110:113]
	v_mfma_f32_16x16x32_bf16 v[102:105], v[150:153], v[192:195], v[102:105]
	v_mfma_f32_16x16x32_bf16 v[94:97], v[168:171], v[192:195], v[94:97]
	v_mfma_f32_16x16x32_bf16 v[86:89], v[150:153], v[200:203], v[86:89]
	v_mfma_f32_16x16x32_bf16 v[78:81], v[168:171], v[200:203], v[78:81]
	v_mfma_f32_16x16x32_bf16 v[70:73], v[150:153], v[216:219], v[70:73]
	v_mfma_f32_16x16x32_bf16 v[66:69], v[168:171], v[216:219], v[66:69]
	s_setprio 0
	s_barrier
	s_add_i32 s53, s53, s36
	v_lshl_add_u64 v[176:177], s[28:29], 0, v[162:163]
	s_mov_b32 m0, s53
	ds_read_b128 v[172:175], v183 offset:16384
	ds_read_b128 v[184:187], v183 offset:17408
	ds_read_b128 v[188:191], v183 offset:18432
	ds_read_b128 v[192:195], v183 offset:19456
	ds_read_b128 v[196:199], v183 offset:20480
	ds_read_b128 v[200:203], v183 offset:21504
	ds_read_b128 v[204:207], v183 offset:22528
	ds_read_b128 v[216:219], v183 offset:23552
	global_load_lds_dwordx4 v[176:177], off
	s_add_i32 m0, s53, 0x2000
	s_add_u32 s58, s28, 0x40000
	v_lshl_add_u64 v[208:209], s[28:29], 0, v[158:159]
	s_addc_u32 s59, s29, 0
	s_add_i32 s53, s62, s36
	global_load_lds_dwordx4 v[208:209], off
	v_lshl_add_u64 v[220:221], s[58:59], 0, v[162:163]
	s_mov_b32 m0, s53
	v_lshl_add_u64 v[222:223], s[30:31], 0, v[160:161]
	global_load_lds_dwordx4 v[220:221], off
	s_add_i32 m0, s53, 0x2000
	v_lshl_add_u64 v[220:221], s[58:59], 0, v[158:159]
	global_load_lds_dwordx4 v[220:221], off
	s_mov_b32 m0, s37
	v_lshl_add_u64 v[220:221], s[30:31], 0, v[0:1]
	global_load_lds_dwordx4 v[220:221], off
	s_mov_b32 m0, s44
	s_nop 0
	global_load_lds_dwordx4 v[222:223], off
	s_waitcnt vmcnt(8) lgkmcnt(0)
	s_barrier
	s_setprio 1
	v_mfma_f32_16x16x32_bf16 v[62:65], v[130:133], v[172:175], v[62:65]
	v_mfma_f32_16x16x32_bf16 v[58:61], v[138:141], v[172:175], v[58:61]
	v_mfma_f32_16x16x32_bf16 v[50:53], v[130:133], v[188:191], v[50:53]
	v_mfma_f32_16x16x32_bf16 v[42:45], v[138:141], v[188:191], v[42:45]
	v_mfma_f32_16x16x32_bf16 v[34:37], v[130:133], v[196:199], v[34:37]
	v_mfma_f32_16x16x32_bf16 v[26:29], v[138:141], v[196:199], v[26:29]
	v_mfma_f32_16x16x32_bf16 v[18:21], v[130:133], v[204:207], v[18:21]
	v_mfma_f32_16x16x32_bf16 v[10:13], v[138:141], v[204:207], v[10:13]
	v_mfma_f32_16x16x32_bf16 v[62:65], v[134:137], v[184:187], v[62:65]
	v_mfma_f32_16x16x32_bf16 v[58:61], v[142:145], v[184:187], v[58:61]
	v_mfma_f32_16x16x32_bf16 v[50:53], v[134:137], v[192:195], v[50:53]
	v_mfma_f32_16x16x32_bf16 v[42:45], v[142:145], v[192:195], v[42:45]
	v_mfma_f32_16x16x32_bf16 v[34:37], v[134:137], v[200:203], v[34:37]
	v_mfma_f32_16x16x32_bf16 v[26:29], v[142:145], v[200:203], v[26:29]
	v_mfma_f32_16x16x32_bf16 v[18:21], v[134:137], v[216:219], v[18:21]
	v_mfma_f32_16x16x32_bf16 v[10:13], v[142:145], v[216:219], v[10:13]
	s_setprio 0
	s_setprio 1
	v_mfma_f32_16x16x32_bf16 v[54:57], v[146:149], v[172:175], v[54:57]
	v_mfma_f32_16x16x32_bf16 v[46:49], v[154:157], v[172:175], v[46:49]
	v_mfma_f32_16x16x32_bf16 v[38:41], v[146:149], v[188:191], v[38:41]
	v_mfma_f32_16x16x32_bf16 v[30:33], v[154:157], v[188:191], v[30:33]
	v_mfma_f32_16x16x32_bf16 v[22:25], v[146:149], v[196:199], v[22:25]
	v_mfma_f32_16x16x32_bf16 v[14:17], v[154:157], v[196:199], v[14:17]
	v_mfma_f32_16x16x32_bf16 v[6:9], v[146:149], v[204:207], v[6:9]
	v_mfma_f32_16x16x32_bf16 v[2:5], v[154:157], v[204:207], v[2:5]
	v_mfma_f32_16x16x32_bf16 v[54:57], v[150:153], v[184:187], v[54:57]
	v_mfma_f32_16x16x32_bf16 v[46:49], v[168:171], v[184:187], v[46:49]
	v_mfma_f32_16x16x32_bf16 v[38:41], v[150:153], v[192:195], v[38:41]
	v_mfma_f32_16x16x32_bf16 v[30:33], v[168:171], v[192:195], v[30:33]
	v_mfma_f32_16x16x32_bf16 v[22:25], v[150:153], v[200:203], v[22:25]
	v_mfma_f32_16x16x32_bf16 v[14:17], v[168:171], v[200:203], v[14:17]
	v_mfma_f32_16x16x32_bf16 v[6:9], v[150:153], v[216:219], v[6:9]
	v_mfma_f32_16x16x32_bf16 v[2:5], v[168:171], v[216:219], v[2:5]
	s_setprio 0
	s_barrier
	s_add_i32 s53, 0, 0x18000
	s_add_i32 s58, 0, 0x1c000
	v_add_u32_e32 v142, s53, v181
	v_add_u32_e32 v168, s58, v181
	ds_read_b128 v[130:133], v142
	ds_read_b128 v[134:137], v142 offset:1024
	ds_read_b128 v[138:141], v142 offset:2048
	ds_read_b128 v[142:145], v142 offset:3072
	ds_read_b128 v[146:149], v168
	ds_read_b128 v[150:153], v168 offset:1024
	ds_read_b128 v[154:157], v168 offset:2048
	ds_read_b128 v[168:171], v168 offset:3072
	s_add_u32 s30, s30, 0x40000
	s_addc_u32 s31, s31, 0
	s_mov_b32 m0, s45
	v_lshl_add_u64 v[224:225], s[30:31], 0, v[0:1]
	ds_read_b128 v[172:175], v183 offset:32768
	ds_read_b128 v[184:187], v183 offset:33792
	ds_read_b128 v[188:191], v183 offset:34816
	ds_read_b128 v[192:195], v183 offset:35840
	ds_read_b128 v[196:199], v183 offset:36864
	ds_read_b128 v[200:203], v183 offset:37888
	ds_read_b128 v[204:207], v183 offset:38912
	ds_read_b128 v[216:219], v183 offset:39936
	global_load_lds_dwordx4 v[224:225], off
	s_mov_b32 m0, s46
	v_lshl_add_u64 v[224:225], s[30:31], 0, v[160:161]
	global_load_lds_dwordx4 v[224:225], off
	s_waitcnt vmcnt(8) lgkmcnt(0)
	s_barrier
	s_setprio 1
	v_mfma_f32_16x16x32_bf16 v[126:129], v[130:133], v[172:175], v[126:129]
	v_mfma_f32_16x16x32_bf16 v[122:125], v[138:141], v[172:175], v[122:125]
	v_mfma_f32_16x16x32_bf16 v[114:117], v[130:133], v[188:191], v[114:117]
	v_mfma_f32_16x16x32_bf16 v[106:109], v[138:141], v[188:191], v[106:109]
	v_mfma_f32_16x16x32_bf16 v[98:101], v[130:133], v[196:199], v[98:101]
	v_mfma_f32_16x16x32_bf16 v[90:93], v[138:141], v[196:199], v[90:93]
	v_mfma_f32_16x16x32_bf16 v[82:85], v[130:133], v[204:207], v[82:85]
	v_mfma_f32_16x16x32_bf16 v[74:77], v[138:141], v[204:207], v[74:77]
	v_mfma_f32_16x16x32_bf16 v[126:129], v[134:137], v[184:187], v[126:129]
	v_mfma_f32_16x16x32_bf16 v[122:125], v[142:145], v[184:187], v[122:125]
	v_mfma_f32_16x16x32_bf16 v[114:117], v[134:137], v[192:195], v[114:117]
	v_mfma_f32_16x16x32_bf16 v[106:109], v[142:145], v[192:195], v[106:109]
	v_mfma_f32_16x16x32_bf16 v[98:101], v[134:137], v[200:203], v[98:101]
	v_mfma_f32_16x16x32_bf16 v[90:93], v[142:145], v[200:203], v[90:93]
	v_mfma_f32_16x16x32_bf16 v[82:85], v[134:137], v[216:219], v[82:85]
	v_mfma_f32_16x16x32_bf16 v[74:77], v[142:145], v[216:219], v[74:77]
	s_setprio 0
	s_setprio 1
	v_mfma_f32_16x16x32_bf16 v[118:121], v[146:149], v[172:175], v[118:121]
	v_mfma_f32_16x16x32_bf16 v[110:113], v[154:157], v[172:175], v[110:113]
	v_mfma_f32_16x16x32_bf16 v[102:105], v[146:149], v[188:191], v[102:105]
	v_mfma_f32_16x16x32_bf16 v[94:97], v[154:157], v[188:191], v[94:97]
	v_mfma_f32_16x16x32_bf16 v[86:89], v[146:149], v[196:199], v[86:89]
	v_mfma_f32_16x16x32_bf16 v[78:81], v[154:157], v[196:199], v[78:81]
	v_mfma_f32_16x16x32_bf16 v[70:73], v[146:149], v[204:207], v[70:73]
	v_mfma_f32_16x16x32_bf16 v[66:69], v[154:157], v[204:207], v[66:69]
	v_mfma_f32_16x16x32_bf16 v[118:121], v[150:153], v[184:187], v[118:121]
	v_mfma_f32_16x16x32_bf16 v[110:113], v[168:171], v[184:187], v[110:113]
	v_mfma_f32_16x16x32_bf16 v[102:105], v[150:153], v[192:195], v[102:105]
	v_mfma_f32_16x16x32_bf16 v[94:97], v[168:171], v[192:195], v[94:97]
	v_mfma_f32_16x16x32_bf16 v[86:89], v[150:153], v[200:203], v[86:89]
	v_mfma_f32_16x16x32_bf16 v[78:81], v[168:171], v[200:203], v[78:81]
	v_mfma_f32_16x16x32_bf16 v[70:73], v[150:153], v[216:219], v[70:73]
	v_mfma_f32_16x16x32_bf16 v[66:69], v[168:171], v[216:219], v[66:69]
	s_setprio 0
	s_barrier
	s_add_i32 s30, s53, s36
	v_lshl_add_u64 v[176:177], v[176:177], 0, s[56:57]
	s_mov_b32 m0, s30
	ds_read_b128 v[172:175], v183 offset:49152
	ds_read_b128 v[184:187], v183 offset:50176
	ds_read_b128 v[188:191], v183 offset:51200
	ds_read_b128 v[192:195], v183 offset:52224
	ds_read_b128 v[196:199], v183 offset:53248
	ds_read_b128 v[200:203], v183 offset:54272
	ds_read_b128 v[204:207], v183 offset:55296
	ds_read_b128 v[216:219], v183 offset:56320
	global_load_lds_dwordx4 v[176:177], off
	s_add_i32 m0, s30, 0x2000
	s_add_u32 s28, s28, 0x40080
	v_lshl_add_u64 v[176:177], v[208:209], 0, s[56:57]
	s_addc_u32 s29, s29, 0
	s_add_i32 s30, s58, s36
	global_load_lds_dwordx4 v[176:177], off
	s_mov_b32 m0, s30
	v_lshl_add_u64 v[176:177], s[28:29], 0, v[162:163]
	global_load_lds_dwordx4 v[176:177], off
	s_add_i32 m0, s30, 0x2000
	v_lshl_add_u64 v[176:177], s[28:29], 0, v[158:159]
	global_load_lds_dwordx4 v[176:177], off
	s_mov_b32 m0, s47
	v_lshl_add_u64 v[176:177], v[220:221], 0, s[56:57]
	global_load_lds_dwordx4 v[176:177], off
	s_mov_b32 m0, s48
	v_lshl_add_u64 v[176:177], v[222:223], 0, s[56:57]
	global_load_lds_dwordx4 v[176:177], off
	s_waitcnt vmcnt(8) lgkmcnt(0)
	s_barrier
	s_setprio 1
	v_mfma_f32_16x16x32_bf16 v[62:65], v[130:133], v[172:175], v[62:65]
	v_mfma_f32_16x16x32_bf16 v[58:61], v[138:141], v[172:175], v[58:61]
	v_mfma_f32_16x16x32_bf16 v[50:53], v[130:133], v[188:191], v[50:53]
	v_mfma_f32_16x16x32_bf16 v[42:45], v[138:141], v[188:191], v[42:45]
	v_mfma_f32_16x16x32_bf16 v[34:37], v[130:133], v[196:199], v[34:37]
	v_mfma_f32_16x16x32_bf16 v[26:29], v[138:141], v[196:199], v[26:29]
	v_mfma_f32_16x16x32_bf16 v[18:21], v[130:133], v[204:207], v[18:21]
	v_mfma_f32_16x16x32_bf16 v[10:13], v[138:141], v[204:207], v[10:13]
	v_mfma_f32_16x16x32_bf16 v[62:65], v[134:137], v[184:187], v[62:65]
	v_mfma_f32_16x16x32_bf16 v[58:61], v[142:145], v[184:187], v[58:61]
	v_mfma_f32_16x16x32_bf16 v[50:53], v[134:137], v[192:195], v[50:53]
	v_mfma_f32_16x16x32_bf16 v[42:45], v[142:145], v[192:195], v[42:45]
	v_mfma_f32_16x16x32_bf16 v[34:37], v[134:137], v[200:203], v[34:37]
	v_mfma_f32_16x16x32_bf16 v[26:29], v[142:145], v[200:203], v[26:29]
	v_mfma_f32_16x16x32_bf16 v[18:21], v[134:137], v[216:219], v[18:21]
	v_mfma_f32_16x16x32_bf16 v[10:13], v[142:145], v[216:219], v[10:13]
	s_setprio 0
	s_setprio 1
	v_mfma_f32_16x16x32_bf16 v[54:57], v[146:149], v[172:175], v[54:57]
	v_mfma_f32_16x16x32_bf16 v[46:49], v[154:157], v[172:175], v[46:49]
	v_mfma_f32_16x16x32_bf16 v[38:41], v[146:149], v[188:191], v[38:41]
	v_mfma_f32_16x16x32_bf16 v[30:33], v[154:157], v[188:191], v[30:33]
	v_mfma_f32_16x16x32_bf16 v[22:25], v[146:149], v[196:199], v[22:25]
	v_mfma_f32_16x16x32_bf16 v[14:17], v[154:157], v[196:199], v[14:17]
	v_mfma_f32_16x16x32_bf16 v[6:9], v[146:149], v[204:207], v[6:9]
	v_mfma_f32_16x16x32_bf16 v[2:5], v[154:157], v[204:207], v[2:5]
	v_mfma_f32_16x16x32_bf16 v[54:57], v[150:153], v[184:187], v[54:57]
	v_mfma_f32_16x16x32_bf16 v[46:49], v[168:171], v[184:187], v[46:49]
	v_mfma_f32_16x16x32_bf16 v[38:41], v[150:153], v[192:195], v[38:41]
	v_mfma_f32_16x16x32_bf16 v[30:33], v[168:171], v[192:195], v[30:33]
	v_mfma_f32_16x16x32_bf16 v[22:25], v[150:153], v[200:203], v[22:25]
	v_mfma_f32_16x16x32_bf16 v[14:17], v[168:171], v[200:203], v[14:17]
	v_mfma_f32_16x16x32_bf16 v[6:9], v[150:153], v[216:219], v[6:9]
	v_mfma_f32_16x16x32_bf16 v[2:5], v[168:171], v[216:219], v[2:5]
	s_setprio 0
	s_barrier
	s_add_i32 s41, s41, 2
	s_add_u32 s33, s33, 0x100
	s_addc_u32 s40, s40, 0
	s_add_u32 s6, s6, 0x100
	s_addc_u32 s7, s7, 0
	s_cmp_gt_u32 s41, 13
	s_cbranch_scc0 .LBB0_1783
	s_and_b64 vcc, exec, s[18:19]
	s_cbranch_vccz .LBB0_1786
	s_barrier

.LBB0_1799:
	s_add_u32 s26, s24, 0xfffc0080
	s_addc_u32 s27, s25, -1
	s_add_i32 s48, 0, 0x10000
	s_cmp_eq_u32 s47, 12
	s_cselect_b32 s29, s8, s27
	s_cselect_b32 s28, s9, s26
	v_add_u32_e32 v142, s48, v144
	s_cselect_b32 s27, s15, s46
	s_cselect_b32 s26, s17, s45
	s_add_i32 s52, 0, 0x14000
	ds_read_b128 v[148:151], v142
	ds_read_b128 v[152:155], v142 offset:1024
	ds_read_b128 v[156:159], v142 offset:2048
	ds_read_b128 v[160:163], v142 offset:3072
	v_add_u32_e32 v142, s52, v144
	ds_read_b128 v[164:167], v142
	ds_read_b128 v[168:171], v142 offset:1024
	ds_read_b128 v[172:175], v142 offset:2048
	ds_read_b128 v[180:183], v142 offset:3072
	v_lshl_add_u64 v[142:143], s[24:25], 0, v[140:141]
	s_add_i32 m0, s36, 0xc000
	ds_read_b128 v[184:187], v146
	ds_read_b128 v[188:191], v146 offset:1024
	ds_read_b128 v[192:195], v146 offset:2048
	ds_read_b128 v[196:199], v146 offset:3072
	ds_read_b128 v[200:203], v146 offset:4096
	ds_read_b128 v[204:207], v146 offset:5120
	ds_read_b128 v[216:219], v146 offset:6144
	ds_read_b128 v[220:223], v146 offset:7168
	global_load_lds_dwordx4 v[142:143], off
	s_add_i32 m0, s36, 0xe000
	v_lshl_add_u64 v[142:143], s[24:25], 0, v[138:139]
	global_load_lds_dwordx4 v[142:143], off
	s_waitcnt vmcnt(8) lgkmcnt(0)
	s_barrier
	s_setprio 1
	v_mfma_f32_16x16x32_bf16 v[126:129], v[148:151], v[184:187], v[126:129]
	v_mfma_f32_16x16x32_bf16 v[122:125], v[156:159], v[184:187], v[122:125]
	v_mfma_f32_16x16x32_bf16 v[118:121], v[148:151], v[192:195], v[118:121]
	v_mfma_f32_16x16x32_bf16 v[110:113], v[156:159], v[192:195], v[110:113]
	v_mfma_f32_16x16x32_bf16 v[102:105], v[148:151], v[200:203], v[102:105]
	v_mfma_f32_16x16x32_bf16 v[94:97], v[156:159], v[200:203], v[94:97]
	v_mfma_f32_16x16x32_bf16 v[86:89], v[148:151], v[216:219], v[86:89]
	v_mfma_f32_16x16x32_bf16 v[78:81], v[156:159], v[216:219], v[78:81]
	v_mfma_f32_16x16x32_bf16 v[126:129], v[152:155], v[188:191], v[126:129]
	v_mfma_f32_16x16x32_bf16 v[122:125], v[160:163], v[188:191], v[122:125]
	v_mfma_f32_16x16x32_bf16 v[118:121], v[152:155], v[196:199], v[118:121]
	v_mfma_f32_16x16x32_bf16 v[110:113], v[160:163], v[196:199], v[110:113]
	v_mfma_f32_16x16x32_bf16 v[102:105], v[152:155], v[204:207], v[102:105]
	v_mfma_f32_16x16x32_bf16 v[94:97], v[160:163], v[204:207], v[94:97]
	v_mfma_f32_16x16x32_bf16 v[86:89], v[152:155], v[220:223], v[86:89]
	v_mfma_f32_16x16x32_bf16 v[78:81], v[160:163], v[220:223], v[78:81]
	s_setprio 0
	s_setprio 1
	v_mfma_f32_16x16x32_bf16 v[114:117], v[164:167], v[184:187], v[114:117]
	v_mfma_f32_16x16x32_bf16 v[106:109], v[172:175], v[184:187], v[106:109]
	v_mfma_f32_16x16x32_bf16 v[98:101], v[164:167], v[192:195], v[98:101]
	v_mfma_f32_16x16x32_bf16 v[90:93], v[172:175], v[192:195], v[90:93]
	v_mfma_f32_16x16x32_bf16 v[82:85], v[164:167], v[200:203], v[82:85]
	v_mfma_f32_16x16x32_bf16 v[74:77], v[172:175], v[200:203], v[74:77]
	v_mfma_f32_16x16x32_bf16 v[70:73], v[164:167], v[216:219], v[70:73]
	v_mfma_f32_16x16x32_bf16 v[66:69], v[172:175], v[216:219], v[66:69]
	v_mfma_f32_16x16x32_bf16 v[114:117], v[168:171], v[188:191], v[114:117]
	v_mfma_f32_16x16x32_bf16 v[106:109], v[180:183], v[188:191], v[106:109]
	v_mfma_f32_16x16x32_bf16 v[98:101], v[168:171], v[196:199], v[98:101]
	v_mfma_f32_16x16x32_bf16 v[90:93], v[180:183], v[196:199], v[90:93]
	v_mfma_f32_16x16x32_bf16 v[82:85], v[168:171], v[204:207], v[82:85]
	v_mfma_f32_16x16x32_bf16 v[74:77], v[180:183], v[204:207], v[74:77]
	v_mfma_f32_16x16x32_bf16 v[70:73], v[168:171], v[220:223], v[70:73]
	v_mfma_f32_16x16x32_bf16 v[66:69], v[180:183], v[220:223], v[66:69]
	s_setprio 0
	s_barrier
	s_add_i32 s48, s48, s35
	v_lshl_add_u64 v[142:143], s[26:27], 0, v[134:135]
	s_mov_b32 m0, s48
	ds_read_b128 v[184:187], v146 offset:16384
	ds_read_b128 v[188:191], v146 offset:17408
	ds_read_b128 v[192:195], v146 offset:18432
	ds_read_b128 v[196:199], v146 offset:19456
	ds_read_b128 v[200:203], v146 offset:20480
	ds_read_b128 v[204:207], v146 offset:21504
	ds_read_b128 v[216:219], v146 offset:22528
	ds_read_b128 v[220:223], v146 offset:23552
	global_load_lds_dwordx4 v[142:143], off
	s_add_i32 m0, s48, 0x2000
	s_add_u32 s48, s26, 0x40000
	v_lshl_add_u64 v[176:177], s[26:27], 0, v[130:131]
	s_addc_u32 s49, s27, 0
	s_add_i32 s52, s52, s35
	global_load_lds_dwordx4 v[176:177], off
	v_lshl_add_u64 v[208:209], s[48:49], 0, v[134:135]
	s_mov_b32 m0, s52
	v_lshl_add_u64 v[224:225], s[28:29], 0, v[132:133]
	global_load_lds_dwordx4 v[208:209], off
	s_add_i32 m0, s52, 0x2000
	v_lshl_add_u64 v[208:209], s[48:49], 0, v[130:131]
	global_load_lds_dwordx4 v[208:209], off
	s_mov_b32 m0, s36
	v_lshl_add_u64 v[208:209], s[28:29], 0, v[136:137]
	global_load_lds_dwordx4 v[208:209], off
	s_mov_b32 m0, s37
	s_nop 0
	global_load_lds_dwordx4 v[224:225], off
	s_waitcnt vmcnt(8) lgkmcnt(0)
	s_barrier
	s_setprio 1
	v_mfma_f32_16x16x32_bf16 v[62:65], v[148:151], v[184:187], v[62:65]
	v_mfma_f32_16x16x32_bf16 v[58:61], v[156:159], v[184:187], v[58:61]
	v_mfma_f32_16x16x32_bf16 v[54:57], v[148:151], v[192:195], v[54:57]
	v_mfma_f32_16x16x32_bf16 v[46:49], v[156:159], v[192:195], v[46:49]
	v_mfma_f32_16x16x32_bf16 v[38:41], v[148:151], v[200:203], v[38:41]
	v_mfma_f32_16x16x32_bf16 v[30:33], v[156:159], v[200:203], v[30:33]
	v_mfma_f32_16x16x32_bf16 v[22:25], v[148:151], v[216:219], v[22:25]
	v_mfma_f32_16x16x32_bf16 v[14:17], v[156:159], v[216:219], v[14:17]
	v_mfma_f32_16x16x32_bf16 v[62:65], v[152:155], v[188:191], v[62:65]
	v_mfma_f32_16x16x32_bf16 v[58:61], v[160:163], v[188:191], v[58:61]
	v_mfma_f32_16x16x32_bf16 v[54:57], v[152:155], v[196:199], v[54:57]
	v_mfma_f32_16x16x32_bf16 v[46:49], v[160:163], v[196:199], v[46:49]
	v_mfma_f32_16x16x32_bf16 v[38:41], v[152:155], v[204:207], v[38:41]
	v_mfma_f32_16x16x32_bf16 v[30:33], v[160:163], v[204:207], v[30:33]
	v_mfma_f32_16x16x32_bf16 v[22:25], v[152:155], v[220:223], v[22:25]
	v_mfma_f32_16x16x32_bf16 v[14:17], v[160:163], v[220:223], v[14:17]
	s_setprio 0
	s_setprio 1
	v_mfma_f32_16x16x32_bf16 v[50:53], v[164:167], v[184:187], v[50:53]
	v_mfma_f32_16x16x32_bf16 v[42:45], v[172:175], v[184:187], v[42:45]
	v_mfma_f32_16x16x32_bf16 v[34:37], v[164:167], v[192:195], v[34:37]
	v_mfma_f32_16x16x32_bf16 v[26:29], v[172:175], v[192:195], v[26:29]
	v_mfma_f32_16x16x32_bf16 v[18:21], v[164:167], v[200:203], v[18:21]
	v_mfma_f32_16x16x32_bf16 v[10:13], v[172:175], v[200:203], v[10:13]
	v_mfma_f32_16x16x32_bf16 v[6:9], v[164:167], v[216:219], v[6:9]
	v_mfma_f32_16x16x32_bf16 v[2:5], v[172:175], v[216:219], v[2:5]
	v_mfma_f32_16x16x32_bf16 v[50:53], v[168:171], v[188:191], v[50:53]
	v_mfma_f32_16x16x32_bf16 v[42:45], v[180:183], v[188:191], v[42:45]
	v_mfma_f32_16x16x32_bf16 v[34:37], v[168:171], v[196:199], v[34:37]
	v_mfma_f32_16x16x32_bf16 v[26:29], v[180:183], v[196:199], v[26:29]
	v_mfma_f32_16x16x32_bf16 v[18:21], v[168:171], v[204:207], v[18:21]
	v_mfma_f32_16x16x32_bf16 v[10:13], v[180:183], v[204:207], v[10:13]
	v_mfma_f32_16x16x32_bf16 v[6:9], v[168:171], v[220:223], v[6:9]
	v_mfma_f32_16x16x32_bf16 v[2:5], v[180:183], v[220:223], v[2:5]
	s_setprio 0
	s_barrier
	s_add_i32 s48, 0, 0x18000
	v_add_u32_e32 v147, s48, v144
	s_add_i32 s49, 0, 0x1c000
	ds_read_b128 v[148:151], v147
	ds_read_b128 v[152:155], v147 offset:1024
	ds_read_b128 v[156:159], v147 offset:2048
	ds_read_b128 v[160:163], v147 offset:3072
	v_add_u32_e32 v147, s49, v144
	ds_read_b128 v[164:167], v147
	ds_read_b128 v[168:171], v147 offset:1024
	ds_read_b128 v[172:175], v147 offset:2048
	ds_read_b128 v[180:183], v147 offset:3072
	s_add_u32 s28, s28, 0x40000
	s_addc_u32 s29, s29, 0
	s_mov_b32 m0, s4
	v_lshl_add_u64 v[240:241], s[28:29], 0, v[136:137]
	ds_read_b128 v[184:187], v146 offset:32768
	ds_read_b128 v[188:191], v146 offset:33792
	ds_read_b128 v[192:195], v146 offset:34816
	ds_read_b128 v[196:199], v146 offset:35840
	ds_read_b128 v[200:203], v146 offset:36864
	ds_read_b128 v[204:207], v146 offset:37888
	ds_read_b128 v[216:219], v146 offset:38912
	ds_read_b128 v[220:223], v146 offset:39936
	global_load_lds_dwordx4 v[240:241], off
	s_mov_b32 m0, s33
	v_lshl_add_u64 v[240:241], s[28:29], 0, v[132:133]
	global_load_lds_dwordx4 v[240:241], off
	s_waitcnt vmcnt(8) lgkmcnt(0)
	s_barrier
	s_setprio 1
	v_mfma_f32_16x16x32_bf16 v[126:129], v[148:151], v[184:187], v[126:129]
	v_mfma_f32_16x16x32_bf16 v[122:125], v[156:159], v[184:187], v[122:125]
	v_mfma_f32_16x16x32_bf16 v[118:121], v[148:151], v[192:195], v[118:121]
	v_mfma_f32_16x16x32_bf16 v[110:113], v[156:159], v[192:195], v[110:113]
	v_mfma_f32_16x16x32_bf16 v[102:105], v[148:151], v[200:203], v[102:105]
	v_mfma_f32_16x16x32_bf16 v[94:97], v[156:159], v[200:203], v[94:97]
	v_mfma_f32_16x16x32_bf16 v[86:89], v[148:151], v[216:219], v[86:89]
	v_mfma_f32_16x16x32_bf16 v[78:81], v[156:159], v[216:219], v[78:81]
	v_mfma_f32_16x16x32_bf16 v[126:129], v[152:155], v[188:191], v[126:129]
	v_mfma_f32_16x16x32_bf16 v[122:125], v[160:163], v[188:191], v[122:125]
	v_mfma_f32_16x16x32_bf16 v[118:121], v[152:155], v[196:199], v[118:121]
	v_mfma_f32_16x16x32_bf16 v[110:113], v[160:163], v[196:199], v[110:113]
	v_mfma_f32_16x16x32_bf16 v[102:105], v[152:155], v[204:207], v[102:105]
	v_mfma_f32_16x16x32_bf16 v[94:97], v[160:163], v[204:207], v[94:97]
	v_mfma_f32_16x16x32_bf16 v[86:89], v[152:155], v[220:223], v[86:89]
	v_mfma_f32_16x16x32_bf16 v[78:81], v[160:163], v[220:223], v[78:81]
	s_setprio 0
	s_setprio 1
	v_mfma_f32_16x16x32_bf16 v[114:117], v[164:167], v[184:187], v[114:117]
	v_mfma_f32_16x16x32_bf16 v[106:109], v[172:175], v[184:187], v[106:109]
	v_mfma_f32_16x16x32_bf16 v[98:101], v[164:167], v[192:195], v[98:101]
	v_mfma_f32_16x16x32_bf16 v[90:93], v[172:175], v[192:195], v[90:93]
	v_mfma_f32_16x16x32_bf16 v[82:85], v[164:167], v[200:203], v[82:85]
	v_mfma_f32_16x16x32_bf16 v[74:77], v[172:175], v[200:203], v[74:77]
	v_mfma_f32_16x16x32_bf16 v[70:73], v[164:167], v[216:219], v[70:73]
	v_mfma_f32_16x16x32_bf16 v[66:69], v[172:175], v[216:219], v[66:69]
	v_mfma_f32_16x16x32_bf16 v[114:117], v[168:171], v[188:191], v[114:117]
	v_mfma_f32_16x16x32_bf16 v[106:109], v[180:183], v[188:191], v[106:109]
	v_mfma_f32_16x16x32_bf16 v[98:101], v[168:171], v[196:199], v[98:101]
	v_mfma_f32_16x16x32_bf16 v[90:93], v[180:183], v[196:199], v[90:93]
	v_mfma_f32_16x16x32_bf16 v[82:85], v[168:171], v[204:207], v[82:85]
	v_mfma_f32_16x16x32_bf16 v[74:77], v[180:183], v[204:207], v[74:77]
	v_mfma_f32_16x16x32_bf16 v[70:73], v[168:171], v[220:223], v[70:73]
	v_mfma_f32_16x16x32_bf16 v[66:69], v[180:183], v[220:223], v[66:69]
	s_setprio 0
	s_barrier
	s_add_i32 s28, s48, s35
	v_lshl_add_u64 v[142:143], v[142:143], 0, s[56:57]
	s_mov_b32 m0, s28
	ds_read_b128 v[184:187], v146 offset:49152
	ds_read_b128 v[188:191], v146 offset:50176
	ds_read_b128 v[192:195], v146 offset:51200
	ds_read_b128 v[196:199], v146 offset:52224
	ds_read_b128 v[200:203], v146 offset:53248
	ds_read_b128 v[204:207], v146 offset:54272
	ds_read_b128 v[216:219], v146 offset:55296
	ds_read_b128 v[220:223], v146 offset:56320
	global_load_lds_dwordx4 v[142:143], off
	s_add_i32 m0, s28, 0x2000
	s_add_u32 s26, s26, 0x40080
	v_lshl_add_u64 v[142:143], v[176:177], 0, s[56:57]
	s_addc_u32 s27, s27, 0
	s_add_i32 s28, s49, s35
	global_load_lds_dwordx4 v[142:143], off
	s_mov_b32 m0, s28
	v_lshl_add_u64 v[142:143], s[26:27], 0, v[134:135]
	global_load_lds_dwordx4 v[142:143], off
	s_add_i32 m0, s28, 0x2000
	v_lshl_add_u64 v[142:143], s[26:27], 0, v[130:131]
	global_load_lds_dwordx4 v[142:143], off
	s_mov_b32 m0, s38
	v_lshl_add_u64 v[142:143], v[208:209], 0, s[56:57]
	global_load_lds_dwordx4 v[142:143], off
	s_mov_b32 m0, s39
	v_lshl_add_u64 v[142:143], v[224:225], 0, s[56:57]
	global_load_lds_dwordx4 v[142:143], off
	s_waitcnt vmcnt(8) lgkmcnt(0)
	s_barrier
	s_setprio 1
	v_mfma_f32_16x16x32_bf16 v[62:65], v[148:151], v[184:187], v[62:65]
	v_mfma_f32_16x16x32_bf16 v[58:61], v[156:159], v[184:187], v[58:61]
	v_mfma_f32_16x16x32_bf16 v[54:57], v[148:151], v[192:195], v[54:57]
	v_mfma_f32_16x16x32_bf16 v[46:49], v[156:159], v[192:195], v[46:49]
	v_mfma_f32_16x16x32_bf16 v[38:41], v[148:151], v[200:203], v[38:41]
	v_mfma_f32_16x16x32_bf16 v[30:33], v[156:159], v[200:203], v[30:33]
	v_mfma_f32_16x16x32_bf16 v[22:25], v[148:151], v[216:219], v[22:25]
	v_mfma_f32_16x16x32_bf16 v[14:17], v[156:159], v[216:219], v[14:17]
	v_mfma_f32_16x16x32_bf16 v[62:65], v[152:155], v[188:191], v[62:65]
	v_mfma_f32_16x16x32_bf16 v[58:61], v[160:163], v[188:191], v[58:61]
	v_mfma_f32_16x16x32_bf16 v[54:57], v[152:155], v[196:199], v[54:57]
	v_mfma_f32_16x16x32_bf16 v[46:49], v[160:163], v[196:199], v[46:49]
	v_mfma_f32_16x16x32_bf16 v[38:41], v[152:155], v[204:207], v[38:41]
	v_mfma_f32_16x16x32_bf16 v[30:33], v[160:163], v[204:207], v[30:33]
	v_mfma_f32_16x16x32_bf16 v[22:25], v[152:155], v[220:223], v[22:25]
	v_mfma_f32_16x16x32_bf16 v[14:17], v[160:163], v[220:223], v[14:17]
	s_setprio 0
	s_setprio 1
	v_mfma_f32_16x16x32_bf16 v[50:53], v[164:167], v[184:187], v[50:53]
	v_mfma_f32_16x16x32_bf16 v[42:45], v[172:175], v[184:187], v[42:45]
	v_mfma_f32_16x16x32_bf16 v[34:37], v[164:167], v[192:195], v[34:37]
	v_mfma_f32_16x16x32_bf16 v[26:29], v[172:175], v[192:195], v[26:29]
	v_mfma_f32_16x16x32_bf16 v[18:21], v[164:167], v[200:203], v[18:21]
	v_mfma_f32_16x16x32_bf16 v[10:13], v[172:175], v[200:203], v[10:13]
	v_mfma_f32_16x16x32_bf16 v[6:9], v[164:167], v[216:219], v[6:9]
	v_mfma_f32_16x16x32_bf16 v[2:5], v[172:175], v[216:219], v[2:5]
	v_mfma_f32_16x16x32_bf16 v[50:53], v[168:171], v[188:191], v[50:53]
	v_mfma_f32_16x16x32_bf16 v[42:45], v[180:183], v[188:191], v[42:45]
	v_mfma_f32_16x16x32_bf16 v[34:37], v[168:171], v[196:199], v[34:37]
	v_mfma_f32_16x16x32_bf16 v[26:29], v[180:183], v[196:199], v[26:29]
	v_mfma_f32_16x16x32_bf16 v[18:21], v[168:171], v[204:207], v[18:21]
	v_mfma_f32_16x16x32_bf16 v[10:13], v[180:183], v[204:207], v[10:13]
	v_mfma_f32_16x16x32_bf16 v[6:9], v[168:171], v[220:223], v[6:9]
	v_mfma_f32_16x16x32_bf16 v[2:5], v[180:183], v[220:223], v[2:5]
	s_setprio 0
	s_barrier
	s_add_i32 s47, s47, 2
	s_add_u32 s45, s45, 0x100
	s_addc_u32 s46, s46, 0
	s_add_u32 s24, s24, 0x100
	s_addc_u32 s25, s25, 0
	s_cmp_gt_u32 s47, 13
	s_cbranch_scc0 .LBB0_1799
	s_and_b64 vcc, exec, s[12:13]
	s_cbranch_vccz .LBB0_1802
	s_barrier

.LBB0_2367:
	s_add_u32 s10, s34, s38
	s_addc_u32 s11, s35, 0
	s_add_u32 s39, s10, 0x100
	s_addc_u32 s76, s11, 0
	s_and_b64 s[70:71], s[62:63], exec
	s_cselect_b32 s77, s45, s76
	s_cselect_b32 s76, s59, s39
	s_add_u32 s38, s30, s38
	s_addc_u32 s39, s31, 0
	s_add_u32 s70, s38, 0x100
	s_addc_u32 s71, s39, 0
	s_add_i32 s91, 0, 0x10000
	s_and_b64 s[38:39], s[62:63], exec
	s_cselect_b32 s79, s37, s71
	s_cselect_b32 s78, s82, s70
	s_add_i32 s38, 0, 0x14000
	s_add_u32 s10, s10, 0x10080
	s_addc_u32 s11, s11, 0
	s_add_i32 s8, s91, s95
	s_add_i32 m0, s65, 0xc000
	s_add_i32 s14, s65, 0xe000
	s_add_i32 s9, s8, 0x2000
	s_add_u32 s80, s78, 0x10000
	s_addc_u32 s81, s79, 0
	s_add_i32 s50, s38, s95
	v_add_u32_e32 v152, s91, v138
	v_add_u32_e32 v164, s38, v138
	s_add_i32 s74, s50, 0x2000
	s_add_i32 vcc_hi, 0, 0x18000
	s_add_i32 s39, 0, 0x1c000
	ds_read_b128 v[140:143], v152
	ds_read_b128 v[144:147], v152 offset:1024
	ds_read_b128 v[148:151], v152 offset:2048
	ds_read_b128 v[152:155], v152 offset:3072
	ds_read_b128 v[156:159], v164
	ds_read_b128 v[160:163], v164 offset:1024
	ds_read_b128 v[168:171], v164 offset:2048
	ds_read_b128 v[172:175], v164 offset:3072
	s_add_u32 s70, s76, 0x10000
	s_addc_u32 s71, s77, 0
	s_add_i32 vcc_lo, vcc_hi, s95
	s_add_i32 s64, vcc_lo, 0x2000
	s_add_u32 s62, s78, 0x10080
	s_addc_u32 s63, s79, 0
	s_add_i32 s91, s39, s95
	s_add_i32 s38, s91, 0x2000
	v_lshl_add_u64 v[164:165], s[10:11], 0, v[128:129]
	ds_read_b128 v[176:179], v139
	ds_read_b128 v[180:183], v139 offset:1024
	ds_read_b128 v[184:187], v139 offset:2048
	ds_read_b128 v[188:191], v139 offset:3072
	ds_read_b128 v[192:195], v139 offset:4096
	ds_read_b128 v[196:199], v139 offset:5120
	ds_read_b128 v[200:203], v139 offset:6144
	ds_read_b128 v[204:207], v139 offset:7168
	global_load_lds_dwordx4 v[164:165], off
	s_mov_b32 m0, s14
	v_lshl_add_u64 v[164:165], s[10:11], 0, v[124:125]
	global_load_lds_dwordx4 v[164:165], off
	s_waitcnt vmcnt(8) lgkmcnt(0)
	s_barrier
	s_setprio 1
	v_mfma_f32_16x16x32_bf16 v[134:137], v[140:143], v[176:179], v[134:137]
	v_mfma_f32_16x16x32_bf16 v[130:133], v[148:151], v[176:179], v[130:133]
	v_mfma_f32_16x16x32_bf16 v[110:113], v[140:143], v[184:187], v[110:113]
	v_mfma_f32_16x16x32_bf16 v[106:109], v[148:151], v[184:187], v[106:109]
	v_mfma_f32_16x16x32_bf16 v[94:97], v[140:143], v[192:195], v[94:97]
	v_mfma_f32_16x16x32_bf16 v[90:93], v[148:151], v[192:195], v[90:93]
	v_mfma_f32_16x16x32_bf16 v[78:81], v[140:143], v[200:203], v[78:81]
	v_mfma_f32_16x16x32_bf16 v[74:77], v[148:151], v[200:203], v[74:77]
	v_mfma_f32_16x16x32_bf16 v[134:137], v[144:147], v[180:183], v[134:137]
	v_mfma_f32_16x16x32_bf16 v[130:133], v[152:155], v[180:183], v[130:133]
	v_mfma_f32_16x16x32_bf16 v[110:113], v[144:147], v[188:191], v[110:113]
	v_mfma_f32_16x16x32_bf16 v[106:109], v[152:155], v[188:191], v[106:109]
	v_mfma_f32_16x16x32_bf16 v[94:97], v[144:147], v[196:199], v[94:97]
	v_mfma_f32_16x16x32_bf16 v[90:93], v[152:155], v[196:199], v[90:93]
	v_mfma_f32_16x16x32_bf16 v[78:81], v[144:147], v[204:207], v[78:81]
	v_mfma_f32_16x16x32_bf16 v[74:77], v[152:155], v[204:207], v[74:77]
	s_setprio 0
	s_setprio 1
	v_mfma_f32_16x16x32_bf16 v[118:121], v[156:159], v[176:179], v[118:121]
	v_mfma_f32_16x16x32_bf16 v[114:117], v[168:171], v[176:179], v[114:117]
	v_mfma_f32_16x16x32_bf16 v[102:105], v[156:159], v[184:187], v[102:105]
	v_mfma_f32_16x16x32_bf16 v[98:101], v[168:171], v[184:187], v[98:101]
	v_mfma_f32_16x16x32_bf16 v[86:89], v[156:159], v[192:195], v[86:89]
	v_mfma_f32_16x16x32_bf16 v[82:85], v[168:171], v[192:195], v[82:85]
	v_mfma_f32_16x16x32_bf16 v[70:73], v[156:159], v[200:203], v[70:73]
	v_mfma_f32_16x16x32_bf16 v[66:69], v[168:171], v[200:203], v[66:69]
	v_mfma_f32_16x16x32_bf16 v[118:121], v[160:163], v[180:183], v[118:121]
	v_mfma_f32_16x16x32_bf16 v[114:117], v[172:175], v[180:183], v[114:117]
	v_mfma_f32_16x16x32_bf16 v[102:105], v[160:163], v[188:191], v[102:105]
	v_mfma_f32_16x16x32_bf16 v[98:101], v[172:175], v[188:191], v[98:101]
	v_mfma_f32_16x16x32_bf16 v[86:89], v[160:163], v[196:199], v[86:89]
	v_mfma_f32_16x16x32_bf16 v[82:85], v[172:175], v[196:199], v[82:85]
	v_mfma_f32_16x16x32_bf16 v[70:73], v[160:163], v[204:207], v[70:73]
	v_mfma_f32_16x16x32_bf16 v[66:69], v[172:175], v[204:207], v[66:69]
	s_setprio 0
	s_barrier
	s_mov_b32 m0, s8
	v_lshl_add_u64 v[164:165], s[78:79], 0, v[126:127]
	ds_read_b128 v[176:179], v139 offset:16384
	ds_read_b128 v[180:183], v139 offset:17408
	ds_read_b128 v[184:187], v139 offset:18432
	ds_read_b128 v[188:191], v139 offset:19456
	ds_read_b128 v[192:195], v139 offset:20480
	ds_read_b128 v[196:199], v139 offset:21504
	ds_read_b128 v[200:203], v139 offset:22528
	ds_read_b128 v[204:207], v139 offset:23552
	global_load_lds_dwordx4 v[164:165], off
	v_lshl_add_u64 v[208:209], s[78:79], 0, v[122:123]
	s_mov_b32 m0, s9
	v_lshl_add_u64 v[216:217], s[80:81], 0, v[126:127]
	global_load_lds_dwordx4 v[208:209], off
	s_mov_b32 m0, s50
	v_lshl_add_u64 v[218:219], s[76:77], 0, v[124:125]
	global_load_lds_dwordx4 v[216:217], off
	s_mov_b32 m0, s74
	v_lshl_add_u64 v[216:217], s[80:81], 0, v[122:123]
	global_load_lds_dwordx4 v[216:217], off
	s_mov_b32 m0, s65
	v_lshl_add_u64 v[216:217], s[76:77], 0, v[128:129]
	global_load_lds_dwordx4 v[216:217], off
	s_mov_b32 m0, s15
	s_nop 0
	global_load_lds_dwordx4 v[218:219], off
	s_waitcnt vmcnt(8) lgkmcnt(0)
	s_barrier
	s_setprio 1
	v_mfma_f32_16x16x32_bf16 v[62:65], v[140:143], v[176:179], v[62:65]
	v_mfma_f32_16x16x32_bf16 v[58:61], v[148:151], v[176:179], v[58:61]
	v_mfma_f32_16x16x32_bf16 v[46:49], v[140:143], v[184:187], v[46:49]
	v_mfma_f32_16x16x32_bf16 v[42:45], v[148:151], v[184:187], v[42:45]
	v_mfma_f32_16x16x32_bf16 v[30:33], v[140:143], v[192:195], v[30:33]
	v_mfma_f32_16x16x32_bf16 v[26:29], v[148:151], v[192:195], v[26:29]
	v_mfma_f32_16x16x32_bf16 v[14:17], v[140:143], v[200:203], v[14:17]
	v_mfma_f32_16x16x32_bf16 v[10:13], v[148:151], v[200:203], v[10:13]
	v_mfma_f32_16x16x32_bf16 v[62:65], v[144:147], v[180:183], v[62:65]
	v_mfma_f32_16x16x32_bf16 v[58:61], v[152:155], v[180:183], v[58:61]
	v_mfma_f32_16x16x32_bf16 v[46:49], v[144:147], v[188:191], v[46:49]
	v_mfma_f32_16x16x32_bf16 v[42:45], v[152:155], v[188:191], v[42:45]
	v_mfma_f32_16x16x32_bf16 v[30:33], v[144:147], v[196:199], v[30:33]
	v_mfma_f32_16x16x32_bf16 v[26:29], v[152:155], v[196:199], v[26:29]
	v_mfma_f32_16x16x32_bf16 v[14:17], v[144:147], v[204:207], v[14:17]
	v_mfma_f32_16x16x32_bf16 v[10:13], v[152:155], v[204:207], v[10:13]
	s_setprio 0
	s_setprio 1
	v_mfma_f32_16x16x32_bf16 v[54:57], v[156:159], v[176:179], v[54:57]
	v_mfma_f32_16x16x32_bf16 v[50:53], v[168:171], v[176:179], v[50:53]
	v_mfma_f32_16x16x32_bf16 v[38:41], v[156:159], v[184:187], v[38:41]
	v_mfma_f32_16x16x32_bf16 v[34:37], v[168:171], v[184:187], v[34:37]
	v_mfma_f32_16x16x32_bf16 v[22:25], v[156:159], v[192:195], v[22:25]
	v_mfma_f32_16x16x32_bf16 v[18:21], v[168:171], v[192:195], v[18:21]
	v_mfma_f32_16x16x32_bf16 v[6:9], v[156:159], v[200:203], v[6:9]
	v_mfma_f32_16x16x32_bf16 v[2:5], v[168:171], v[200:203], v[2:5]
	v_mfma_f32_16x16x32_bf16 v[54:57], v[160:163], v[180:183], v[54:57]
	v_mfma_f32_16x16x32_bf16 v[50:53], v[172:175], v[180:183], v[50:53]
	v_mfma_f32_16x16x32_bf16 v[38:41], v[160:163], v[188:191], v[38:41]
	v_mfma_f32_16x16x32_bf16 v[34:37], v[172:175], v[188:191], v[34:37]
	v_mfma_f32_16x16x32_bf16 v[22:25], v[160:163], v[196:199], v[22:25]
	v_mfma_f32_16x16x32_bf16 v[18:21], v[172:175], v[196:199], v[18:21]
	v_mfma_f32_16x16x32_bf16 v[6:9], v[160:163], v[204:207], v[6:9]
	v_mfma_f32_16x16x32_bf16 v[2:5], v[172:175], v[204:207], v[2:5]
	s_setprio 0
	s_barrier
	v_add_u32_e32 v152, vcc_hi, v138
	v_add_u32_e32 v167, s39, v138
	ds_read_b128 v[140:143], v152
	ds_read_b128 v[144:147], v152 offset:1024
	ds_read_b128 v[148:151], v152 offset:2048
	ds_read_b128 v[152:155], v152 offset:3072
	ds_read_b128 v[156:159], v167
	ds_read_b128 v[160:163], v167 offset:1024
	ds_read_b128 v[168:171], v167 offset:2048
	ds_read_b128 v[172:175], v167 offset:3072
	s_mov_b32 m0, s84
	v_lshl_add_u64 v[220:221], s[70:71], 0, v[128:129]
	ds_read_b128 v[176:179], v139 offset:32768
	ds_read_b128 v[180:183], v139 offset:33792
	ds_read_b128 v[184:187], v139 offset:34816
	ds_read_b128 v[188:191], v139 offset:35840
	ds_read_b128 v[192:195], v139 offset:36864
	ds_read_b128 v[196:199], v139 offset:37888
	ds_read_b128 v[200:203], v139 offset:38912
	ds_read_b128 v[204:207], v139 offset:39936
	global_load_lds_dwordx4 v[220:221], off
	s_mov_b32 m0, s90
	v_lshl_add_u64 v[220:221], s[70:71], 0, v[124:125]
	global_load_lds_dwordx4 v[220:221], off
	s_waitcnt vmcnt(8) lgkmcnt(0)
	s_barrier
	s_setprio 1
	v_mfma_f32_16x16x32_bf16 v[134:137], v[140:143], v[176:179], v[134:137]
	v_mfma_f32_16x16x32_bf16 v[130:133], v[148:151], v[176:179], v[130:133]
	v_mfma_f32_16x16x32_bf16 v[110:113], v[140:143], v[184:187], v[110:113]
	v_mfma_f32_16x16x32_bf16 v[106:109], v[148:151], v[184:187], v[106:109]
	v_mfma_f32_16x16x32_bf16 v[94:97], v[140:143], v[192:195], v[94:97]
	v_mfma_f32_16x16x32_bf16 v[90:93], v[148:151], v[192:195], v[90:93]
	v_mfma_f32_16x16x32_bf16 v[78:81], v[140:143], v[200:203], v[78:81]
	v_mfma_f32_16x16x32_bf16 v[74:77], v[148:151], v[200:203], v[74:77]
	v_mfma_f32_16x16x32_bf16 v[134:137], v[144:147], v[180:183], v[134:137]
	v_mfma_f32_16x16x32_bf16 v[130:133], v[152:155], v[180:183], v[130:133]
	v_mfma_f32_16x16x32_bf16 v[110:113], v[144:147], v[188:191], v[110:113]
	v_mfma_f32_16x16x32_bf16 v[106:109], v[152:155], v[188:191], v[106:109]
	v_mfma_f32_16x16x32_bf16 v[94:97], v[144:147], v[196:199], v[94:97]
	v_mfma_f32_16x16x32_bf16 v[90:93], v[152:155], v[196:199], v[90:93]
	v_mfma_f32_16x16x32_bf16 v[78:81], v[144:147], v[204:207], v[78:81]
	v_mfma_f32_16x16x32_bf16 v[74:77], v[152:155], v[204:207], v[74:77]
	s_setprio 0
	s_setprio 1
	v_mfma_f32_16x16x32_bf16 v[118:121], v[156:159], v[176:179], v[118:121]
	v_mfma_f32_16x16x32_bf16 v[114:117], v[168:171], v[176:179], v[114:117]
	v_mfma_f32_16x16x32_bf16 v[102:105], v[156:159], v[184:187], v[102:105]
	v_mfma_f32_16x16x32_bf16 v[98:101], v[168:171], v[184:187], v[98:101]
	v_mfma_f32_16x16x32_bf16 v[86:89], v[156:159], v[192:195], v[86:89]
	v_mfma_f32_16x16x32_bf16 v[82:85], v[168:171], v[192:195], v[82:85]
	v_mfma_f32_16x16x32_bf16 v[70:73], v[156:159], v[200:203], v[70:73]
	v_mfma_f32_16x16x32_bf16 v[66:69], v[168:171], v[200:203], v[66:69]
	v_mfma_f32_16x16x32_bf16 v[118:121], v[160:163], v[180:183], v[118:121]
	v_mfma_f32_16x16x32_bf16 v[114:117], v[172:175], v[180:183], v[114:117]
	v_mfma_f32_16x16x32_bf16 v[102:105], v[160:163], v[188:191], v[102:105]
	v_mfma_f32_16x16x32_bf16 v[98:101], v[172:175], v[188:191], v[98:101]
	v_mfma_f32_16x16x32_bf16 v[86:89], v[160:163], v[196:199], v[86:89]
	v_mfma_f32_16x16x32_bf16 v[82:85], v[172:175], v[196:199], v[82:85]
	v_mfma_f32_16x16x32_bf16 v[70:73], v[160:163], v[204:207], v[70:73]
	v_mfma_f32_16x16x32_bf16 v[66:69], v[172:175], v[204:207], v[66:69]
	s_setprio 0
	s_barrier
	s_mov_b32 m0, vcc_lo
	v_lshl_add_u64 v[164:165], v[164:165], 0, s[56:57]
	ds_read_b128 v[176:179], v139 offset:49152
	ds_read_b128 v[180:183], v139 offset:50176
	ds_read_b128 v[184:187], v139 offset:51200
	ds_read_b128 v[188:191], v139 offset:52224
	ds_read_b128 v[192:195], v139 offset:53248
	ds_read_b128 v[196:199], v139 offset:54272
	ds_read_b128 v[200:203], v139 offset:55296
	ds_read_b128 v[204:207], v139 offset:56320
	global_load_lds_dwordx4 v[164:165], off
	s_mov_b32 m0, s64
	v_lshl_add_u64 v[164:165], v[208:209], 0, s[56:57]
	global_load_lds_dwordx4 v[164:165], off
	s_mov_b32 m0, s91
	v_lshl_add_u64 v[164:165], s[62:63], 0, v[126:127]
	global_load_lds_dwordx4 v[164:165], off
	s_mov_b32 m0, s38
	v_lshl_add_u64 v[164:165], s[62:63], 0, v[122:123]
	global_load_lds_dwordx4 v[164:165], off
	s_mov_b32 m0, s68
	v_lshl_add_u64 v[164:165], v[216:217], 0, s[56:57]
	global_load_lds_dwordx4 v[164:165], off
	s_mov_b32 m0, s22
	v_lshl_add_u64 v[164:165], v[218:219], 0, s[56:57]
	global_load_lds_dwordx4 v[164:165], off
	s_waitcnt vmcnt(8) lgkmcnt(0)
	s_barrier
	s_setprio 1
	v_mfma_f32_16x16x32_bf16 v[62:65], v[140:143], v[176:179], v[62:65]
	v_mfma_f32_16x16x32_bf16 v[58:61], v[148:151], v[176:179], v[58:61]
	v_mfma_f32_16x16x32_bf16 v[46:49], v[140:143], v[184:187], v[46:49]
	v_mfma_f32_16x16x32_bf16 v[42:45], v[148:151], v[184:187], v[42:45]
	v_mfma_f32_16x16x32_bf16 v[30:33], v[140:143], v[192:195], v[30:33]
	v_mfma_f32_16x16x32_bf16 v[26:29], v[148:151], v[192:195], v[26:29]
	v_mfma_f32_16x16x32_bf16 v[14:17], v[140:143], v[200:203], v[14:17]
	v_mfma_f32_16x16x32_bf16 v[10:13], v[148:151], v[200:203], v[10:13]
	v_mfma_f32_16x16x32_bf16 v[62:65], v[144:147], v[180:183], v[62:65]
	v_mfma_f32_16x16x32_bf16 v[58:61], v[152:155], v[180:183], v[58:61]
	v_mfma_f32_16x16x32_bf16 v[46:49], v[144:147], v[188:191], v[46:49]
	v_mfma_f32_16x16x32_bf16 v[42:45], v[152:155], v[188:191], v[42:45]
	v_mfma_f32_16x16x32_bf16 v[30:33], v[144:147], v[196:199], v[30:33]
	v_mfma_f32_16x16x32_bf16 v[26:29], v[152:155], v[196:199], v[26:29]
	v_mfma_f32_16x16x32_bf16 v[14:17], v[144:147], v[204:207], v[14:17]
	v_mfma_f32_16x16x32_bf16 v[10:13], v[152:155], v[204:207], v[10:13]
	s_setprio 0
	s_setprio 1
	v_mfma_f32_16x16x32_bf16 v[54:57], v[156:159], v[176:179], v[54:57]
	v_mfma_f32_16x16x32_bf16 v[50:53], v[168:171], v[176:179], v[50:53]
	v_mfma_f32_16x16x32_bf16 v[38:41], v[156:159], v[184:187], v[38:41]
	v_mfma_f32_16x16x32_bf16 v[34:37], v[168:171], v[184:187], v[34:37]
	v_mfma_f32_16x16x32_bf16 v[22:25], v[156:159], v[192:195], v[22:25]
	v_mfma_f32_16x16x32_bf16 v[18:21], v[168:171], v[192:195], v[18:21]
	v_mfma_f32_16x16x32_bf16 v[6:9], v[156:159], v[200:203], v[6:9]
	v_mfma_f32_16x16x32_bf16 v[2:5], v[168:171], v[200:203], v[2:5]
	v_mfma_f32_16x16x32_bf16 v[54:57], v[160:163], v[180:183], v[54:57]
	v_mfma_f32_16x16x32_bf16 v[50:53], v[172:175], v[180:183], v[50:53]
	v_mfma_f32_16x16x32_bf16 v[38:41], v[160:163], v[188:191], v[38:41]
	v_mfma_f32_16x16x32_bf16 v[34:37], v[172:175], v[188:191], v[34:37]
	v_mfma_f32_16x16x32_bf16 v[22:25], v[160:163], v[196:199], v[22:25]
	v_mfma_f32_16x16x32_bf16 v[18:21], v[172:175], v[196:199], v[18:21]
	v_mfma_f32_16x16x32_bf16 v[6:9], v[160:163], v[204:207], v[6:9]
	v_mfma_f32_16x16x32_bf16 v[2:5], v[172:175], v[204:207], v[2:5]
	s_setprio 0
	s_barrier
	s_movk_i32 s38, 0x100
	s_andn2_b64 vcc, exec, s[52:53]
	s_mov_b64 s[62:63], -1
	s_mov_b64 s[52:53], 0
	s_cbranch_vccz .LBB0_2367
	s_andn2_b64 vcc, exec, s[42:43]
	s_cbranch_vccnz .LBB0_2359
	v_mov_b32_e32 v2, 0
	s_mov_b32 s16, s36
	s_mov_b32 s94, s44
	s_mov_b64 s[30:31], s[48:49]
	s_mov_b64 s[34:35], s[46:47]
	s_mov_b32 s58, s23
	v_mov_b32_e32 v3, v2
	v_mov_b32_e32 v4, v2
	v_mov_b32_e32 v5, v2
	v_mov_b32_e32 v6, v2
	v_mov_b32_e32 v7, v2
	v_mov_b32_e32 v8, v2
	v_mov_b32_e32 v9, v2
	v_mov_b32_e32 v18, v2
	v_mov_b32_e32 v19, v2
	v_mov_b32_e32 v20, v2
	v_mov_b32_e32 v21, v2
	v_mov_b32_e32 v22, v2
	v_mov_b32_e32 v23, v2
	v_mov_b32_e32 v24, v2
	v_mov_b32_e32 v25, v2
	v_mov_b32_e32 v34, v2
	v_mov_b32_e32 v35, v2
	v_mov_b32_e32 v36, v2
	v_mov_b32_e32 v37, v2
	v_mov_b32_e32 v38, v2
	v_mov_b32_e32 v39, v2
	v_mov_b32_e32 v40, v2
	v_mov_b32_e32 v41, v2
	v_mov_b32_e32 v50, v2
	v_mov_b32_e32 v51, v2
	v_mov_b32_e32 v52, v2
	v_mov_b32_e32 v53, v2
	v_mov_b32_e32 v54, v2
	v_mov_b32_e32 v55, v2
	v_mov_b32_e32 v56, v2
	v_mov_b32_e32 v57, v2
	v_mov_b32_e32 v10, v2
	v_mov_b32_e32 v11, v2
	v_mov_b32_e32 v12, v2
	v_mov_b32_e32 v13, v2
	v_mov_b32_e32 v14, v2
	v_mov_b32_e32 v15, v2
	v_mov_b32_e32 v16, v2
	v_mov_b32_e32 v17, v2
	v_mov_b32_e32 v26, v2
	v_mov_b32_e32 v27, v2
	v_mov_b32_e32 v28, v2
	v_mov_b32_e32 v29, v2
	v_mov_b32_e32 v30, v2
	v_mov_b32_e32 v31, v2
	v_mov_b32_e32 v32, v2
	v_mov_b32_e32 v33, v2
	v_mov_b32_e32 v42, v2
	v_mov_b32_e32 v43, v2
	v_mov_b32_e32 v44, v2
	v_mov_b32_e32 v45, v2
	v_mov_b32_e32 v46, v2
	v_mov_b32_e32 v47, v2
	v_mov_b32_e32 v48, v2
	v_mov_b32_e32 v49, v2
	v_mov_b32_e32 v58, v2
	v_mov_b32_e32 v59, v2
	v_mov_b32_e32 v60, v2
	v_mov_b32_e32 v61, v2
	v_mov_b32_e32 v62, v2
	v_mov_b32_e32 v63, v2
	v_mov_b32_e32 v64, v2
	v_mov_b32_e32 v65, v2
	v_mov_b32_e32 v66, v2
	v_mov_b32_e32 v67, v2
	v_mov_b32_e32 v68, v2
	v_mov_b32_e32 v69, v2
	v_mov_b32_e32 v70, v2
	v_mov_b32_e32 v71, v2
	v_mov_b32_e32 v72, v2
	v_mov_b32_e32 v73, v2
	v_mov_b32_e32 v82, v2
	v_mov_b32_e32 v83, v2
	v_mov_b32_e32 v84, v2
	v_mov_b32_e32 v85, v2
	v_mov_b32_e32 v86, v2
	v_mov_b32_e32 v87, v2
	v_mov_b32_e32 v88, v2
	v_mov_b32_e32 v89, v2
	v_mov_b32_e32 v98, v2
	v_mov_b32_e32 v99, v2
	v_mov_b32_e32 v100, v2
	v_mov_b32_e32 v101, v2
	v_mov_b32_e32 v102, v2
	v_mov_b32_e32 v103, v2
	v_mov_b32_e32 v104, v2
	v_mov_b32_e32 v105, v2
	v_mov_b32_e32 v114, v2
	v_mov_b32_e32 v115, v2
	v_mov_b32_e32 v116, v2
	v_mov_b32_e32 v117, v2
	v_mov_b32_e32 v118, v2
	v_mov_b32_e32 v119, v2
	v_mov_b32_e32 v120, v2
	v_mov_b32_e32 v121, v2
	v_mov_b32_e32 v74, v2
	v_mov_b32_e32 v75, v2
	v_mov_b32_e32 v76, v2
	v_mov_b32_e32 v77, v2
	v_mov_b32_e32 v78, v2
	v_mov_b32_e32 v79, v2
	v_mov_b32_e32 v80, v2
	v_mov_b32_e32 v81, v2
	v_mov_b32_e32 v90, v2
	v_mov_b32_e32 v91, v2
	v_mov_b32_e32 v92, v2
	v_mov_b32_e32 v93, v2
	v_mov_b32_e32 v94, v2
	v_mov_b32_e32 v95, v2
	v_mov_b32_e32 v96, v2
	v_mov_b32_e32 v97, v2
	v_mov_b32_e32 v106, v2
	v_mov_b32_e32 v107, v2
	v_mov_b32_e32 v108, v2
	v_mov_b32_e32 v109, v2
	v_mov_b32_e32 v110, v2
	v_mov_b32_e32 v111, v2
	v_mov_b32_e32 v112, v2
	v_mov_b32_e32 v113, v2
	v_mov_b32_e32 v130, v2
	v_mov_b32_e32 v131, v2
	v_mov_b32_e32 v132, v2
	v_mov_b32_e32 v133, v2
	v_mov_b32_e32 v134, v2
	v_mov_b32_e32 v135, v2
	v_mov_b32_e32 v136, v2
	v_mov_b32_e32 v137, v2
	s_branch .LBB0_2359

.LBB0_2467:
	s_add_u32 s8, s30, s12
	s_addc_u32 s9, s31, 0
	s_add_u32 s13, s8, 0x100
	s_addc_u32 s50, s9, 0
	s_and_b64 s[10:11], s[48:49], exec
	s_cselect_b32 s63, s37, s50
	s_cselect_b32 s62, s59, s13
	s_add_u32 s10, s28, s12
	s_addc_u32 s11, s29, 0
	s_add_u32 s12, s10, 0x100
	s_addc_u32 s13, s11, 0
	s_add_i32 s50, 0, 0x10000
	s_and_b64 s[10:11], s[48:49], exec
	s_cselect_b32 s71, s35, s13
	s_cselect_b32 s70, s96, s12
	s_add_i32 s12, 0, 0x14000
	s_add_u32 s10, s8, 0x10080
	s_addc_u32 s11, s9, 0
	s_add_i32 s9, s50, s81
	s_add_i32 m0, s82, 0xc000
	s_add_i32 s8, s82, 0xe000
	s_add_i32 s64, s9, 0x2000
	s_add_u32 s76, s70, 0x10000
	s_addc_u32 s77, s71, 0
	s_add_i32 s65, s12, s81
	v_add_u32_e32 v152, s50, v138
	v_add_u32_e32 v168, s12, v138
	s_add_i32 s74, s65, 0x2000
	s_add_i32 s91, 0, 0x18000
	s_add_i32 s13, 0, 0x1c000
	ds_read_b128 v[140:143], v152
	ds_read_b128 v[144:147], v152 offset:1024
	ds_read_b128 v[148:151], v152 offset:2048
	ds_read_b128 v[152:155], v152 offset:3072
	ds_read_b128 v[156:159], v168
	ds_read_b128 v[160:163], v168 offset:1024
	ds_read_b128 v[164:167], v168 offset:2048
	ds_read_b128 v[168:171], v168 offset:3072
	s_add_u32 s52, s62, 0x10000
	s_addc_u32 s53, s63, 0
	s_add_i32 vcc_hi, s91, s81
	s_add_i32 vcc_lo, vcc_hi, 0x2000
	s_add_u32 s48, s70, 0x10080
	s_addc_u32 s49, s71, 0
	s_add_i32 s50, s13, s81
	s_add_i32 s12, s50, 0x2000
	v_lshl_add_u64 v[204:205], s[10:11], 0, v[128:129]
	ds_read_b128 v[172:175], v139
	ds_read_b128 v[176:179], v139 offset:1024
	ds_read_b128 v[180:183], v139 offset:2048
	ds_read_b128 v[184:187], v139 offset:3072
	ds_read_b128 v[188:191], v139 offset:4096
	ds_read_b128 v[192:195], v139 offset:5120
	ds_read_b128 v[196:199], v139 offset:6144
	ds_read_b128 v[200:203], v139 offset:7168
	global_load_lds_dwordx4 v[204:205], off
	s_mov_b32 m0, s8
	v_lshl_add_u64 v[204:205], s[10:11], 0, v[124:125]
	global_load_lds_dwordx4 v[204:205], off
	s_waitcnt vmcnt(8) lgkmcnt(0)
	s_barrier
	s_setprio 1
	v_mfma_f32_16x16x32_bf16 v[134:137], v[140:143], v[172:175], v[134:137]
	v_mfma_f32_16x16x32_bf16 v[130:133], v[148:151], v[172:175], v[130:133]
	v_mfma_f32_16x16x32_bf16 v[110:113], v[140:143], v[180:183], v[110:113]
	v_mfma_f32_16x16x32_bf16 v[106:109], v[148:151], v[180:183], v[106:109]
	v_mfma_f32_16x16x32_bf16 v[94:97], v[140:143], v[188:191], v[94:97]
	v_mfma_f32_16x16x32_bf16 v[90:93], v[148:151], v[188:191], v[90:93]
	v_mfma_f32_16x16x32_bf16 v[78:81], v[140:143], v[196:199], v[78:81]
	v_mfma_f32_16x16x32_bf16 v[74:77], v[148:151], v[196:199], v[74:77]
	v_mfma_f32_16x16x32_bf16 v[134:137], v[144:147], v[176:179], v[134:137]
	v_mfma_f32_16x16x32_bf16 v[130:133], v[152:155], v[176:179], v[130:133]
	v_mfma_f32_16x16x32_bf16 v[110:113], v[144:147], v[184:187], v[110:113]
	v_mfma_f32_16x16x32_bf16 v[106:109], v[152:155], v[184:187], v[106:109]
	v_mfma_f32_16x16x32_bf16 v[94:97], v[144:147], v[192:195], v[94:97]
	v_mfma_f32_16x16x32_bf16 v[90:93], v[152:155], v[192:195], v[90:93]
	v_mfma_f32_16x16x32_bf16 v[78:81], v[144:147], v[200:203], v[78:81]
	v_mfma_f32_16x16x32_bf16 v[74:77], v[152:155], v[200:203], v[74:77]
	s_setprio 0
	s_setprio 1
	v_mfma_f32_16x16x32_bf16 v[118:121], v[156:159], v[172:175], v[118:121]
	v_mfma_f32_16x16x32_bf16 v[114:117], v[164:167], v[172:175], v[114:117]
	v_mfma_f32_16x16x32_bf16 v[102:105], v[156:159], v[180:183], v[102:105]
	v_mfma_f32_16x16x32_bf16 v[98:101], v[164:167], v[180:183], v[98:101]
	v_mfma_f32_16x16x32_bf16 v[86:89], v[156:159], v[188:191], v[86:89]
	v_mfma_f32_16x16x32_bf16 v[82:85], v[164:167], v[188:191], v[82:85]
	v_mfma_f32_16x16x32_bf16 v[70:73], v[156:159], v[196:199], v[70:73]
	v_mfma_f32_16x16x32_bf16 v[66:69], v[164:167], v[196:199], v[66:69]
	v_mfma_f32_16x16x32_bf16 v[118:121], v[160:163], v[176:179], v[118:121]
	v_mfma_f32_16x16x32_bf16 v[114:117], v[168:171], v[176:179], v[114:117]
	v_mfma_f32_16x16x32_bf16 v[102:105], v[160:163], v[184:187], v[102:105]
	v_mfma_f32_16x16x32_bf16 v[98:101], v[168:171], v[184:187], v[98:101]
	v_mfma_f32_16x16x32_bf16 v[86:89], v[160:163], v[192:195], v[86:89]
	v_mfma_f32_16x16x32_bf16 v[82:85], v[168:171], v[192:195], v[82:85]
	v_mfma_f32_16x16x32_bf16 v[70:73], v[160:163], v[200:203], v[70:73]
	v_mfma_f32_16x16x32_bf16 v[66:69], v[168:171], v[200:203], v[66:69]
	s_setprio 0
	s_barrier
	s_mov_b32 m0, s9
	v_lshl_add_u64 v[204:205], s[70:71], 0, v[126:127]
	ds_read_b128 v[172:175], v139 offset:16384
	ds_read_b128 v[176:179], v139 offset:17408
	ds_read_b128 v[180:183], v139 offset:18432
	ds_read_b128 v[184:187], v139 offset:19456
	ds_read_b128 v[188:191], v139 offset:20480
	ds_read_b128 v[192:195], v139 offset:21504
	ds_read_b128 v[196:199], v139 offset:22528
	ds_read_b128 v[200:203], v139 offset:23552
	global_load_lds_dwordx4 v[204:205], off
	v_lshl_add_u64 v[206:207], s[70:71], 0, v[122:123]
	s_mov_b32 m0, s64
	v_lshl_add_u64 v[208:209], s[76:77], 0, v[126:127]
	global_load_lds_dwordx4 v[206:207], off
	s_mov_b32 m0, s65
	v_lshl_add_u64 v[216:217], s[62:63], 0, v[124:125]
	global_load_lds_dwordx4 v[208:209], off
	s_mov_b32 m0, s74
	v_lshl_add_u64 v[208:209], s[76:77], 0, v[122:123]
	global_load_lds_dwordx4 v[208:209], off
	s_mov_b32 m0, s82
	v_lshl_add_u64 v[208:209], s[62:63], 0, v[128:129]
	global_load_lds_dwordx4 v[208:209], off
	s_mov_b32 m0, s92
	s_nop 0
	global_load_lds_dwordx4 v[216:217], off
	s_waitcnt vmcnt(8) lgkmcnt(0)
	s_barrier
	s_setprio 1
	v_mfma_f32_16x16x32_bf16 v[62:65], v[140:143], v[172:175], v[62:65]
	v_mfma_f32_16x16x32_bf16 v[58:61], v[148:151], v[172:175], v[58:61]
	v_mfma_f32_16x16x32_bf16 v[46:49], v[140:143], v[180:183], v[46:49]
	v_mfma_f32_16x16x32_bf16 v[42:45], v[148:151], v[180:183], v[42:45]
	v_mfma_f32_16x16x32_bf16 v[30:33], v[140:143], v[188:191], v[30:33]
	v_mfma_f32_16x16x32_bf16 v[26:29], v[148:151], v[188:191], v[26:29]
	v_mfma_f32_16x16x32_bf16 v[14:17], v[140:143], v[196:199], v[14:17]
	v_mfma_f32_16x16x32_bf16 v[10:13], v[148:151], v[196:199], v[10:13]
	v_mfma_f32_16x16x32_bf16 v[62:65], v[144:147], v[176:179], v[62:65]
	v_mfma_f32_16x16x32_bf16 v[58:61], v[152:155], v[176:179], v[58:61]
	v_mfma_f32_16x16x32_bf16 v[46:49], v[144:147], v[184:187], v[46:49]
	v_mfma_f32_16x16x32_bf16 v[42:45], v[152:155], v[184:187], v[42:45]
	v_mfma_f32_16x16x32_bf16 v[30:33], v[144:147], v[192:195], v[30:33]
	v_mfma_f32_16x16x32_bf16 v[26:29], v[152:155], v[192:195], v[26:29]
	v_mfma_f32_16x16x32_bf16 v[14:17], v[144:147], v[200:203], v[14:17]
	v_mfma_f32_16x16x32_bf16 v[10:13], v[152:155], v[200:203], v[10:13]
	s_setprio 0
	s_setprio 1
	v_mfma_f32_16x16x32_bf16 v[54:57], v[156:159], v[172:175], v[54:57]
	v_mfma_f32_16x16x32_bf16 v[50:53], v[164:167], v[172:175], v[50:53]
	v_mfma_f32_16x16x32_bf16 v[38:41], v[156:159], v[180:183], v[38:41]
	v_mfma_f32_16x16x32_bf16 v[34:37], v[164:167], v[180:183], v[34:37]
	v_mfma_f32_16x16x32_bf16 v[22:25], v[156:159], v[188:191], v[22:25]
	v_mfma_f32_16x16x32_bf16 v[18:21], v[164:167], v[188:191], v[18:21]
	v_mfma_f32_16x16x32_bf16 v[6:9], v[156:159], v[196:199], v[6:9]
	v_mfma_f32_16x16x32_bf16 v[2:5], v[164:167], v[196:199], v[2:5]
	v_mfma_f32_16x16x32_bf16 v[54:57], v[160:163], v[176:179], v[54:57]
	v_mfma_f32_16x16x32_bf16 v[50:53], v[168:171], v[176:179], v[50:53]
	v_mfma_f32_16x16x32_bf16 v[38:41], v[160:163], v[184:187], v[38:41]
	v_mfma_f32_16x16x32_bf16 v[34:37], v[168:171], v[184:187], v[34:37]
	v_mfma_f32_16x16x32_bf16 v[22:25], v[160:163], v[192:195], v[22:25]
	v_mfma_f32_16x16x32_bf16 v[18:21], v[168:171], v[192:195], v[18:21]
	v_mfma_f32_16x16x32_bf16 v[6:9], v[160:163], v[200:203], v[6:9]
	v_mfma_f32_16x16x32_bf16 v[2:5], v[168:171], v[200:203], v[2:5]
	s_setprio 0
	s_barrier
	v_add_u32_e32 v152, s91, v138
	v_add_u32_e32 v168, s13, v138
	ds_read_b128 v[140:143], v152
	ds_read_b128 v[144:147], v152 offset:1024
	ds_read_b128 v[148:151], v152 offset:2048
	ds_read_b128 v[152:155], v152 offset:3072
	ds_read_b128 v[156:159], v168
	ds_read_b128 v[160:163], v168 offset:1024
	ds_read_b128 v[164:167], v168 offset:2048
	ds_read_b128 v[168:171], v168 offset:3072
	s_mov_b32 m0, s84
	v_lshl_add_u64 v[218:219], s[52:53], 0, v[128:129]
	ds_read_b128 v[172:175], v139 offset:32768
	ds_read_b128 v[176:179], v139 offset:33792
	ds_read_b128 v[180:183], v139 offset:34816
	ds_read_b128 v[184:187], v139 offset:35840
	ds_read_b128 v[188:191], v139 offset:36864
	ds_read_b128 v[192:195], v139 offset:37888
	ds_read_b128 v[196:199], v139 offset:38912
	ds_read_b128 v[200:203], v139 offset:39936
	global_load_lds_dwordx4 v[218:219], off
	s_mov_b32 m0, s90
	v_lshl_add_u64 v[218:219], s[52:53], 0, v[124:125]
	global_load_lds_dwordx4 v[218:219], off
	s_waitcnt vmcnt(8) lgkmcnt(0)
	s_barrier
	s_setprio 1
	v_mfma_f32_16x16x32_bf16 v[134:137], v[140:143], v[172:175], v[134:137]
	v_mfma_f32_16x16x32_bf16 v[130:133], v[148:151], v[172:175], v[130:133]
	v_mfma_f32_16x16x32_bf16 v[110:113], v[140:143], v[180:183], v[110:113]
	v_mfma_f32_16x16x32_bf16 v[106:109], v[148:151], v[180:183], v[106:109]
	v_mfma_f32_16x16x32_bf16 v[94:97], v[140:143], v[188:191], v[94:97]
	v_mfma_f32_16x16x32_bf16 v[90:93], v[148:151], v[188:191], v[90:93]
	v_mfma_f32_16x16x32_bf16 v[78:81], v[140:143], v[196:199], v[78:81]
	v_mfma_f32_16x16x32_bf16 v[74:77], v[148:151], v[196:199], v[74:77]
	v_mfma_f32_16x16x32_bf16 v[134:137], v[144:147], v[176:179], v[134:137]
	v_mfma_f32_16x16x32_bf16 v[130:133], v[152:155], v[176:179], v[130:133]
	v_mfma_f32_16x16x32_bf16 v[110:113], v[144:147], v[184:187], v[110:113]
	v_mfma_f32_16x16x32_bf16 v[106:109], v[152:155], v[184:187], v[106:109]
	v_mfma_f32_16x16x32_bf16 v[94:97], v[144:147], v[192:195], v[94:97]
	v_mfma_f32_16x16x32_bf16 v[90:93], v[152:155], v[192:195], v[90:93]
	v_mfma_f32_16x16x32_bf16 v[78:81], v[144:147], v[200:203], v[78:81]
	v_mfma_f32_16x16x32_bf16 v[74:77], v[152:155], v[200:203], v[74:77]
	s_setprio 0
	s_setprio 1
	v_mfma_f32_16x16x32_bf16 v[118:121], v[156:159], v[172:175], v[118:121]
	v_mfma_f32_16x16x32_bf16 v[114:117], v[164:167], v[172:175], v[114:117]
	v_mfma_f32_16x16x32_bf16 v[102:105], v[156:159], v[180:183], v[102:105]
	v_mfma_f32_16x16x32_bf16 v[98:101], v[164:167], v[180:183], v[98:101]
	v_mfma_f32_16x16x32_bf16 v[86:89], v[156:159], v[188:191], v[86:89]
	v_mfma_f32_16x16x32_bf16 v[82:85], v[164:167], v[188:191], v[82:85]
	v_mfma_f32_16x16x32_bf16 v[70:73], v[156:159], v[196:199], v[70:73]
	v_mfma_f32_16x16x32_bf16 v[66:69], v[164:167], v[196:199], v[66:69]
	v_mfma_f32_16x16x32_bf16 v[118:121], v[160:163], v[176:179], v[118:121]
	v_mfma_f32_16x16x32_bf16 v[114:117], v[168:171], v[176:179], v[114:117]
	v_mfma_f32_16x16x32_bf16 v[102:105], v[160:163], v[184:187], v[102:105]
	v_mfma_f32_16x16x32_bf16 v[98:101], v[168:171], v[184:187], v[98:101]
	v_mfma_f32_16x16x32_bf16 v[86:89], v[160:163], v[192:195], v[86:89]
	v_mfma_f32_16x16x32_bf16 v[82:85], v[168:171], v[192:195], v[82:85]
	v_mfma_f32_16x16x32_bf16 v[70:73], v[160:163], v[200:203], v[70:73]
	v_mfma_f32_16x16x32_bf16 v[66:69], v[168:171], v[200:203], v[66:69]
	s_setprio 0
	s_barrier
	s_mov_b32 m0, vcc_hi
	v_lshl_add_u64 v[204:205], v[204:205], 0, s[56:57]
	ds_read_b128 v[172:175], v139 offset:49152
	ds_read_b128 v[176:179], v139 offset:50176
	ds_read_b128 v[180:183], v139 offset:51200
	ds_read_b128 v[184:187], v139 offset:52224
	ds_read_b128 v[188:191], v139 offset:53248
	ds_read_b128 v[192:195], v139 offset:54272
	ds_read_b128 v[196:199], v139 offset:55296
	ds_read_b128 v[200:203], v139 offset:56320
	global_load_lds_dwordx4 v[204:205], off
	s_mov_b32 m0, vcc_lo
	v_lshl_add_u64 v[204:205], v[206:207], 0, s[56:57]
	global_load_lds_dwordx4 v[204:205], off
	s_mov_b32 m0, s50
	v_lshl_add_u64 v[204:205], s[48:49], 0, v[126:127]
	global_load_lds_dwordx4 v[204:205], off
	s_mov_b32 m0, s12
	v_lshl_add_u64 v[204:205], s[48:49], 0, v[122:123]
	global_load_lds_dwordx4 v[204:205], off
	s_mov_b32 m0, s68
	v_lshl_add_u64 v[204:205], v[208:209], 0, s[56:57]
	global_load_lds_dwordx4 v[204:205], off
	s_mov_b32 m0, s93
	v_lshl_add_u64 v[204:205], v[216:217], 0, s[56:57]
	global_load_lds_dwordx4 v[204:205], off
	s_waitcnt vmcnt(8) lgkmcnt(0)
	s_barrier
	s_setprio 1
	v_mfma_f32_16x16x32_bf16 v[62:65], v[140:143], v[172:175], v[62:65]
	v_mfma_f32_16x16x32_bf16 v[58:61], v[148:151], v[172:175], v[58:61]
	v_mfma_f32_16x16x32_bf16 v[46:49], v[140:143], v[180:183], v[46:49]
	v_mfma_f32_16x16x32_bf16 v[42:45], v[148:151], v[180:183], v[42:45]
	v_mfma_f32_16x16x32_bf16 v[30:33], v[140:143], v[188:191], v[30:33]
	v_mfma_f32_16x16x32_bf16 v[26:29], v[148:151], v[188:191], v[26:29]
	v_mfma_f32_16x16x32_bf16 v[14:17], v[140:143], v[196:199], v[14:17]
	v_mfma_f32_16x16x32_bf16 v[10:13], v[148:151], v[196:199], v[10:13]
	v_mfma_f32_16x16x32_bf16 v[62:65], v[144:147], v[176:179], v[62:65]
	v_mfma_f32_16x16x32_bf16 v[58:61], v[152:155], v[176:179], v[58:61]
	v_mfma_f32_16x16x32_bf16 v[46:49], v[144:147], v[184:187], v[46:49]
	v_mfma_f32_16x16x32_bf16 v[42:45], v[152:155], v[184:187], v[42:45]
	v_mfma_f32_16x16x32_bf16 v[30:33], v[144:147], v[192:195], v[30:33]
	v_mfma_f32_16x16x32_bf16 v[26:29], v[152:155], v[192:195], v[26:29]
	v_mfma_f32_16x16x32_bf16 v[14:17], v[144:147], v[200:203], v[14:17]
	v_mfma_f32_16x16x32_bf16 v[10:13], v[152:155], v[200:203], v[10:13]
	s_setprio 0
	s_setprio 1
	v_mfma_f32_16x16x32_bf16 v[54:57], v[156:159], v[172:175], v[54:57]
	v_mfma_f32_16x16x32_bf16 v[50:53], v[164:167], v[172:175], v[50:53]
	v_mfma_f32_16x16x32_bf16 v[38:41], v[156:159], v[180:183], v[38:41]
	v_mfma_f32_16x16x32_bf16 v[34:37], v[164:167], v[180:183], v[34:37]
	v_mfma_f32_16x16x32_bf16 v[22:25], v[156:159], v[188:191], v[22:25]
	v_mfma_f32_16x16x32_bf16 v[18:21], v[164:167], v[188:191], v[18:21]
	v_mfma_f32_16x16x32_bf16 v[6:9], v[156:159], v[196:199], v[6:9]
	v_mfma_f32_16x16x32_bf16 v[2:5], v[164:167], v[196:199], v[2:5]
	v_mfma_f32_16x16x32_bf16 v[54:57], v[160:163], v[176:179], v[54:57]
	v_mfma_f32_16x16x32_bf16 v[50:53], v[168:171], v[176:179], v[50:53]
	v_mfma_f32_16x16x32_bf16 v[38:41], v[160:163], v[184:187], v[38:41]
	v_mfma_f32_16x16x32_bf16 v[34:37], v[168:171], v[184:187], v[34:37]
	v_mfma_f32_16x16x32_bf16 v[22:25], v[160:163], v[192:195], v[22:25]
	v_mfma_f32_16x16x32_bf16 v[18:21], v[168:171], v[192:195], v[18:21]
	v_mfma_f32_16x16x32_bf16 v[6:9], v[160:163], v[200:203], v[6:9]
	v_mfma_f32_16x16x32_bf16 v[2:5], v[168:171], v[200:203], v[2:5]
	s_setprio 0
	s_barrier
	s_movk_i32 s12, 0x100
	s_andn2_b64 vcc, exec, s[46:47]
	s_mov_b64 s[48:49], -1
	s_mov_b64 s[46:47], 0
	s_cbranch_vccz .LBB0_2467
	s_andn2_b64 vcc, exec, s[40:41]
	s_cbranch_vccnz .LBB0_2459
	v_mov_b32_e32 v2, 0
	s_mov_b32 s14, s34
	s_mov_b32 s95, s36
	s_mov_b64 s[28:29], s[44:45]
	s_mov_b64 s[30:31], s[42:43]
	s_mov_b32 s94, s58
	v_mov_b32_e32 v3, v2
	v_mov_b32_e32 v4, v2
	v_mov_b32_e32 v5, v2
	v_mov_b32_e32 v6, v2
	v_mov_b32_e32 v7, v2
	v_mov_b32_e32 v8, v2
	v_mov_b32_e32 v9, v2
	v_mov_b32_e32 v18, v2
	v_mov_b32_e32 v19, v2
	v_mov_b32_e32 v20, v2
	v_mov_b32_e32 v21, v2
	v_mov_b32_e32 v22, v2
	v_mov_b32_e32 v23, v2
	v_mov_b32_e32 v24, v2
	v_mov_b32_e32 v25, v2
	v_mov_b32_e32 v34, v2
	v_mov_b32_e32 v35, v2
	v_mov_b32_e32 v36, v2
	v_mov_b32_e32 v37, v2
	v_mov_b32_e32 v38, v2
	v_mov_b32_e32 v39, v2
	v_mov_b32_e32 v40, v2
	v_mov_b32_e32 v41, v2
	v_mov_b32_e32 v50, v2
	v_mov_b32_e32 v51, v2
	v_mov_b32_e32 v52, v2
	v_mov_b32_e32 v53, v2
	v_mov_b32_e32 v54, v2
	v_mov_b32_e32 v55, v2
	v_mov_b32_e32 v56, v2
	v_mov_b32_e32 v57, v2
	v_mov_b32_e32 v10, v2
	v_mov_b32_e32 v11, v2
	v_mov_b32_e32 v12, v2
	v_mov_b32_e32 v13, v2
	v_mov_b32_e32 v14, v2
	v_mov_b32_e32 v15, v2
	v_mov_b32_e32 v16, v2
	v_mov_b32_e32 v17, v2
	v_mov_b32_e32 v26, v2
	v_mov_b32_e32 v27, v2
	v_mov_b32_e32 v28, v2
	v_mov_b32_e32 v29, v2
	v_mov_b32_e32 v30, v2
	v_mov_b32_e32 v31, v2
	v_mov_b32_e32 v32, v2
	v_mov_b32_e32 v33, v2
	v_mov_b32_e32 v42, v2
	v_mov_b32_e32 v43, v2
	v_mov_b32_e32 v44, v2
	v_mov_b32_e32 v45, v2
	v_mov_b32_e32 v46, v2
	v_mov_b32_e32 v47, v2
	v_mov_b32_e32 v48, v2
	v_mov_b32_e32 v49, v2
	v_mov_b32_e32 v58, v2
	v_mov_b32_e32 v59, v2
	v_mov_b32_e32 v60, v2
	v_mov_b32_e32 v61, v2
	v_mov_b32_e32 v62, v2
	v_mov_b32_e32 v63, v2
	v_mov_b32_e32 v64, v2
	v_mov_b32_e32 v65, v2
	v_mov_b32_e32 v66, v2
	v_mov_b32_e32 v67, v2
	v_mov_b32_e32 v68, v2
	v_mov_b32_e32 v69, v2
	v_mov_b32_e32 v70, v2
	v_mov_b32_e32 v71, v2
	v_mov_b32_e32 v72, v2
	v_mov_b32_e32 v73, v2
	v_mov_b32_e32 v82, v2
	v_mov_b32_e32 v83, v2
	v_mov_b32_e32 v84, v2
	v_mov_b32_e32 v85, v2
	v_mov_b32_e32 v86, v2
	v_mov_b32_e32 v87, v2
	v_mov_b32_e32 v88, v2
	v_mov_b32_e32 v89, v2
	v_mov_b32_e32 v98, v2
	v_mov_b32_e32 v99, v2
	v_mov_b32_e32 v100, v2
	v_mov_b32_e32 v101, v2
	v_mov_b32_e32 v102, v2
	v_mov_b32_e32 v103, v2
	v_mov_b32_e32 v104, v2
	v_mov_b32_e32 v105, v2
	v_mov_b32_e32 v114, v2
	v_mov_b32_e32 v115, v2
	v_mov_b32_e32 v116, v2
	v_mov_b32_e32 v117, v2
	v_mov_b32_e32 v118, v2
	v_mov_b32_e32 v119, v2
	v_mov_b32_e32 v120, v2
	v_mov_b32_e32 v121, v2
	v_mov_b32_e32 v74, v2
	v_mov_b32_e32 v75, v2
	v_mov_b32_e32 v76, v2
	v_mov_b32_e32 v77, v2
	v_mov_b32_e32 v78, v2
	v_mov_b32_e32 v79, v2
	v_mov_b32_e32 v80, v2
	v_mov_b32_e32 v81, v2
	v_mov_b32_e32 v90, v2
	v_mov_b32_e32 v91, v2
	v_mov_b32_e32 v92, v2
	v_mov_b32_e32 v93, v2
	v_mov_b32_e32 v94, v2
	v_mov_b32_e32 v95, v2
	v_mov_b32_e32 v96, v2
	v_mov_b32_e32 v97, v2
	v_mov_b32_e32 v106, v2
	v_mov_b32_e32 v107, v2
	v_mov_b32_e32 v108, v2
	v_mov_b32_e32 v109, v2
	v_mov_b32_e32 v110, v2
	v_mov_b32_e32 v111, v2
	v_mov_b32_e32 v112, v2
	v_mov_b32_e32 v113, v2
	v_mov_b32_e32 v130, v2
	v_mov_b32_e32 v131, v2
	v_mov_b32_e32 v132, v2
	v_mov_b32_e32 v133, v2
	v_mov_b32_e32 v134, v2
	v_mov_b32_e32 v135, v2
	v_mov_b32_e32 v136, v2
	v_mov_b32_e32 v137, v2
	s_branch .LBB0_2459

.Lnobar_c6:
.LBB0_2626:
	s_add_u32 s26, s6, 0xfffc0080
	s_addc_u32 s27, s7, -1
	s_add_i32 s50, 0, 0x10000
	s_cmp_eq_u32 s49, 12
	s_cselect_b32 s29, s21, s27
	s_cselect_b32 s28, s33, s26
	v_add_u32_e32 v0, s50, v181
	s_cselect_b32 s27, s19, s48
	s_cselect_b32 s26, s40, s41
	s_add_i32 s58, 0, 0x14000
	ds_read_b128 v[130:133], v0
	ds_read_b128 v[134:137], v0 offset:1024
	ds_read_b128 v[138:141], v0 offset:2048
	ds_read_b128 v[142:145], v0 offset:3072
	v_add_u32_e32 v0, s58, v181
	ds_read_b128 v[146:149], v0
	ds_read_b128 v[150:153], v0 offset:1024
	ds_read_b128 v[154:157], v0 offset:2048
	ds_read_b128 v[170:173], v0 offset:3072
	v_lshl_add_u64 v[178:179], s[6:7], 0, v[168:169]
	s_add_i32 m0, s36, 0xc000
	ds_read_b128 v[174:177], v183
	ds_read_b128 v[184:187], v183 offset:1024
	ds_read_b128 v[188:191], v183 offset:2048
	ds_read_b128 v[192:195], v183 offset:3072
	ds_read_b128 v[196:199], v183 offset:4096
	ds_read_b128 v[200:203], v183 offset:5120
	ds_read_b128 v[204:207], v183 offset:6144
	ds_read_b128 v[216:219], v183 offset:7168
	global_load_lds_dwordx4 v[178:179], off
	s_add_i32 m0, s36, 0xe000
	v_lshl_add_u64 v[178:179], s[6:7], 0, v[166:167]
	global_load_lds_dwordx4 v[178:179], off
	s_waitcnt vmcnt(8) lgkmcnt(0)
	s_barrier
	s_setprio 1
	v_mfma_f32_16x16x32_bf16 v[126:129], v[130:133], v[174:177], v[126:129]
	v_mfma_f32_16x16x32_bf16 v[122:125], v[138:141], v[174:177], v[122:125]
	v_mfma_f32_16x16x32_bf16 v[110:113], v[130:133], v[188:191], v[110:113]
	v_mfma_f32_16x16x32_bf16 v[106:109], v[138:141], v[188:191], v[106:109]
	v_mfma_f32_16x16x32_bf16 v[94:97], v[130:133], v[196:199], v[94:97]
	v_mfma_f32_16x16x32_bf16 v[90:93], v[138:141], v[196:199], v[90:93]
	v_mfma_f32_16x16x32_bf16 v[78:81], v[130:133], v[204:207], v[78:81]
	v_mfma_f32_16x16x32_bf16 v[74:77], v[138:141], v[204:207], v[74:77]
	v_mfma_f32_16x16x32_bf16 v[126:129], v[134:137], v[184:187], v[126:129]
	v_mfma_f32_16x16x32_bf16 v[122:125], v[142:145], v[184:187], v[122:125]
	v_mfma_f32_16x16x32_bf16 v[110:113], v[134:137], v[192:195], v[110:113]
	v_mfma_f32_16x16x32_bf16 v[106:109], v[142:145], v[192:195], v[106:109]
	v_mfma_f32_16x16x32_bf16 v[94:97], v[134:137], v[200:203], v[94:97]
	v_mfma_f32_16x16x32_bf16 v[90:93], v[142:145], v[200:203], v[90:93]
	v_mfma_f32_16x16x32_bf16 v[78:81], v[134:137], v[216:219], v[78:81]
	v_mfma_f32_16x16x32_bf16 v[74:77], v[142:145], v[216:219], v[74:77]
	s_setprio 0
	s_setprio 1
	v_mfma_f32_16x16x32_bf16 v[118:121], v[146:149], v[174:177], v[118:121]
	v_mfma_f32_16x16x32_bf16 v[114:117], v[154:157], v[174:177], v[114:117]
	v_mfma_f32_16x16x32_bf16 v[102:105], v[146:149], v[188:191], v[102:105]
	v_mfma_f32_16x16x32_bf16 v[98:101], v[154:157], v[188:191], v[98:101]
	v_mfma_f32_16x16x32_bf16 v[86:89], v[146:149], v[196:199], v[86:89]
	v_mfma_f32_16x16x32_bf16 v[82:85], v[154:157], v[196:199], v[82:85]
	v_mfma_f32_16x16x32_bf16 v[70:73], v[146:149], v[204:207], v[70:73]
	v_mfma_f32_16x16x32_bf16 v[66:69], v[154:157], v[204:207], v[66:69]
	v_mfma_f32_16x16x32_bf16 v[118:121], v[150:153], v[184:187], v[118:121]
	v_mfma_f32_16x16x32_bf16 v[114:117], v[170:173], v[184:187], v[114:117]
	v_mfma_f32_16x16x32_bf16 v[102:105], v[150:153], v[192:195], v[102:105]
	v_mfma_f32_16x16x32_bf16 v[98:101], v[170:173], v[192:195], v[98:101]
	v_mfma_f32_16x16x32_bf16 v[86:89], v[150:153], v[200:203], v[86:89]
	v_mfma_f32_16x16x32_bf16 v[82:85], v[170:173], v[200:203], v[82:85]
	v_mfma_f32_16x16x32_bf16 v[70:73], v[150:153], v[216:219], v[70:73]
	v_mfma_f32_16x16x32_bf16 v[66:69], v[170:173], v[216:219], v[66:69]
	s_setprio 0
	s_barrier
	s_add_i32 s50, s50, s35
	v_lshl_add_u64 v[178:179], s[26:27], 0, v[162:163]
	s_mov_b32 m0, s50
	ds_read_b128 v[174:177], v183 offset:16384
	ds_read_b128 v[184:187], v183 offset:17408
	ds_read_b128 v[188:191], v183 offset:18432
	ds_read_b128 v[192:195], v183 offset:19456
	ds_read_b128 v[196:199], v183 offset:20480
	ds_read_b128 v[200:203], v183 offset:21504
	ds_read_b128 v[204:207], v183 offset:22528
	ds_read_b128 v[216:219], v183 offset:23552
	global_load_lds_dwordx4 v[178:179], off
	s_add_i32 m0, s50, 0x2000
	s_add_u32 s52, s26, 0x40000
	v_lshl_add_u64 v[208:209], s[26:27], 0, v[158:159]
	s_addc_u32 s53, s27, 0
	s_add_i32 s50, s58, s35
	global_load_lds_dwordx4 v[208:209], off
	v_lshl_add_u64 v[220:221], s[52:53], 0, v[162:163]
	s_mov_b32 m0, s50
	v_lshl_add_u64 v[222:223], s[28:29], 0, v[160:161]
	global_load_lds_dwordx4 v[220:221], off
	s_add_i32 m0, s50, 0x2000
	v_lshl_add_u64 v[220:221], s[52:53], 0, v[158:159]
	global_load_lds_dwordx4 v[220:221], off
	s_mov_b32 m0, s36
	v_lshl_add_u64 v[220:221], s[28:29], 0, v[164:165]
	global_load_lds_dwordx4 v[220:221], off
	s_mov_b32 m0, s37
	s_nop 0
	global_load_lds_dwordx4 v[222:223], off
	s_waitcnt vmcnt(8) lgkmcnt(0)
	s_barrier
	s_setprio 1
	v_mfma_f32_16x16x32_bf16 v[62:65], v[130:133], v[174:177], v[62:65]
	v_mfma_f32_16x16x32_bf16 v[58:61], v[138:141], v[174:177], v[58:61]
	v_mfma_f32_16x16x32_bf16 v[46:49], v[130:133], v[188:191], v[46:49]
	v_mfma_f32_16x16x32_bf16 v[42:45], v[138:141], v[188:191], v[42:45]
	v_mfma_f32_16x16x32_bf16 v[30:33], v[130:133], v[196:199], v[30:33]
	v_mfma_f32_16x16x32_bf16 v[26:29], v[138:141], v[196:199], v[26:29]
	v_mfma_f32_16x16x32_bf16 v[14:17], v[130:133], v[204:207], v[14:17]
	v_mfma_f32_16x16x32_bf16 v[10:13], v[138:141], v[204:207], v[10:13]
	v_mfma_f32_16x16x32_bf16 v[62:65], v[134:137], v[184:187], v[62:65]
	v_mfma_f32_16x16x32_bf16 v[58:61], v[142:145], v[184:187], v[58:61]
	v_mfma_f32_16x16x32_bf16 v[46:49], v[134:137], v[192:195], v[46:49]
	v_mfma_f32_16x16x32_bf16 v[42:45], v[142:145], v[192:195], v[42:45]
	v_mfma_f32_16x16x32_bf16 v[30:33], v[134:137], v[200:203], v[30:33]
	v_mfma_f32_16x16x32_bf16 v[26:29], v[142:145], v[200:203], v[26:29]
	v_mfma_f32_16x16x32_bf16 v[14:17], v[134:137], v[216:219], v[14:17]
	v_mfma_f32_16x16x32_bf16 v[10:13], v[142:145], v[216:219], v[10:13]
	s_setprio 0
	s_setprio 1
	v_mfma_f32_16x16x32_bf16 v[54:57], v[146:149], v[174:177], v[54:57]
	v_mfma_f32_16x16x32_bf16 v[50:53], v[154:157], v[174:177], v[50:53]
	v_mfma_f32_16x16x32_bf16 v[38:41], v[146:149], v[188:191], v[38:41]
	v_mfma_f32_16x16x32_bf16 v[34:37], v[154:157], v[188:191], v[34:37]
	v_mfma_f32_16x16x32_bf16 v[22:25], v[146:149], v[196:199], v[22:25]
	v_mfma_f32_16x16x32_bf16 v[18:21], v[154:157], v[196:199], v[18:21]
	v_mfma_f32_16x16x32_bf16 v[6:9], v[146:149], v[204:207], v[6:9]
	v_mfma_f32_16x16x32_bf16 v[2:5], v[154:157], v[204:207], v[2:5]
	v_mfma_f32_16x16x32_bf16 v[54:57], v[150:153], v[184:187], v[54:57]
	v_mfma_f32_16x16x32_bf16 v[50:53], v[170:173], v[184:187], v[50:53]
	v_mfma_f32_16x16x32_bf16 v[38:41], v[150:153], v[192:195], v[38:41]
	v_mfma_f32_16x16x32_bf16 v[34:37], v[170:173], v[192:195], v[34:37]
	v_mfma_f32_16x16x32_bf16 v[22:25], v[150:153], v[200:203], v[22:25]
	v_mfma_f32_16x16x32_bf16 v[18:21], v[170:173], v[200:203], v[18:21]
	v_mfma_f32_16x16x32_bf16 v[6:9], v[150:153], v[216:219], v[6:9]
	v_mfma_f32_16x16x32_bf16 v[2:5], v[170:173], v[216:219], v[2:5]
	s_setprio 0
	s_barrier
	s_add_i32 s50, 0, 0x18000
	v_add_u32_e32 v0, s50, v181
	s_add_i32 s52, 0, 0x1c000
	ds_read_b128 v[130:133], v0
	ds_read_b128 v[134:137], v0 offset:1024
	ds_read_b128 v[138:141], v0 offset:2048
	ds_read_b128 v[142:145], v0 offset:3072
	v_add_u32_e32 v0, s52, v181
	ds_read_b128 v[146:149], v0
	ds_read_b128 v[150:153], v0 offset:1024
	ds_read_b128 v[154:157], v0 offset:2048
	ds_read_b128 v[170:173], v0 offset:3072
	s_add_u32 s28, s28, 0x40000
	s_addc_u32 s29, s29, 0
	s_mov_b32 m0, s42
	v_lshl_add_u64 v[224:225], s[28:29], 0, v[164:165]
	ds_read_b128 v[174:177], v183 offset:32768
	ds_read_b128 v[184:187], v183 offset:33792
	ds_read_b128 v[188:191], v183 offset:34816
	ds_read_b128 v[192:195], v183 offset:35840
	ds_read_b128 v[196:199], v183 offset:36864
	ds_read_b128 v[200:203], v183 offset:37888
	ds_read_b128 v[204:207], v183 offset:38912
	ds_read_b128 v[216:219], v183 offset:39936
	global_load_lds_dwordx4 v[224:225], off
	s_mov_b32 m0, s43
	v_lshl_add_u64 v[224:225], s[28:29], 0, v[160:161]
	global_load_lds_dwordx4 v[224:225], off
	s_waitcnt vmcnt(8) lgkmcnt(0)
	s_barrier
	s_setprio 1
	v_mfma_f32_16x16x32_bf16 v[126:129], v[130:133], v[174:177], v[126:129]
	v_mfma_f32_16x16x32_bf16 v[122:125], v[138:141], v[174:177], v[122:125]
	v_mfma_f32_16x16x32_bf16 v[110:113], v[130:133], v[188:191], v[110:113]
	v_mfma_f32_16x16x32_bf16 v[106:109], v[138:141], v[188:191], v[106:109]
	v_mfma_f32_16x16x32_bf16 v[94:97], v[130:133], v[196:199], v[94:97]
	v_mfma_f32_16x16x32_bf16 v[90:93], v[138:141], v[196:199], v[90:93]
	v_mfma_f32_16x16x32_bf16 v[78:81], v[130:133], v[204:207], v[78:81]
	v_mfma_f32_16x16x32_bf16 v[74:77], v[138:141], v[204:207], v[74:77]
	v_mfma_f32_16x16x32_bf16 v[126:129], v[134:137], v[184:187], v[126:129]
	v_mfma_f32_16x16x32_bf16 v[122:125], v[142:145], v[184:187], v[122:125]
	v_mfma_f32_16x16x32_bf16 v[110:113], v[134:137], v[192:195], v[110:113]
	v_mfma_f32_16x16x32_bf16 v[106:109], v[142:145], v[192:195], v[106:109]
	v_mfma_f32_16x16x32_bf16 v[94:97], v[134:137], v[200:203], v[94:97]
	v_mfma_f32_16x16x32_bf16 v[90:93], v[142:145], v[200:203], v[90:93]
	v_mfma_f32_16x16x32_bf16 v[78:81], v[134:137], v[216:219], v[78:81]
	v_mfma_f32_16x16x32_bf16 v[74:77], v[142:145], v[216:219], v[74:77]
	s_setprio 0
	s_setprio 1
	v_mfma_f32_16x16x32_bf16 v[118:121], v[146:149], v[174:177], v[118:121]
	v_mfma_f32_16x16x32_bf16 v[114:117], v[154:157], v[174:177], v[114:117]
	v_mfma_f32_16x16x32_bf16 v[102:105], v[146:149], v[188:191], v[102:105]
	v_mfma_f32_16x16x32_bf16 v[98:101], v[154:157], v[188:191], v[98:101]
	v_mfma_f32_16x16x32_bf16 v[86:89], v[146:149], v[196:199], v[86:89]
	v_mfma_f32_16x16x32_bf16 v[82:85], v[154:157], v[196:199], v[82:85]
	v_mfma_f32_16x16x32_bf16 v[70:73], v[146:149], v[204:207], v[70:73]
	v_mfma_f32_16x16x32_bf16 v[66:69], v[154:157], v[204:207], v[66:69]
	v_mfma_f32_16x16x32_bf16 v[118:121], v[150:153], v[184:187], v[118:121]
	v_mfma_f32_16x16x32_bf16 v[114:117], v[170:173], v[184:187], v[114:117]
	v_mfma_f32_16x16x32_bf16 v[102:105], v[150:153], v[192:195], v[102:105]
	v_mfma_f32_16x16x32_bf16 v[98:101], v[170:173], v[192:195], v[98:101]
	v_mfma_f32_16x16x32_bf16 v[86:89], v[150:153], v[200:203], v[86:89]
	v_mfma_f32_16x16x32_bf16 v[82:85], v[170:173], v[200:203], v[82:85]
	v_mfma_f32_16x16x32_bf16 v[70:73], v[150:153], v[216:219], v[70:73]
	v_mfma_f32_16x16x32_bf16 v[66:69], v[170:173], v[216:219], v[66:69]
	s_setprio 0
	s_barrier
	s_add_i32 s28, s50, s35
	v_lshl_add_u64 v[178:179], v[178:179], 0, s[56:57]
	s_mov_b32 m0, s28
	ds_read_b128 v[174:177], v183 offset:49152
	ds_read_b128 v[184:187], v183 offset:50176
	ds_read_b128 v[188:191], v183 offset:51200
	ds_read_b128 v[192:195], v183 offset:52224
	ds_read_b128 v[196:199], v183 offset:53248
	ds_read_b128 v[200:203], v183 offset:54272
	ds_read_b128 v[204:207], v183 offset:55296
	ds_read_b128 v[216:219], v183 offset:56320
	global_load_lds_dwordx4 v[178:179], off
	s_add_i32 m0, s28, 0x2000
	s_add_u32 s26, s26, 0x40080
	v_lshl_add_u64 v[178:179], v[208:209], 0, s[56:57]
	s_addc_u32 s27, s27, 0
	s_add_i32 s28, s52, s35
	global_load_lds_dwordx4 v[178:179], off
	s_mov_b32 m0, s28
	v_lshl_add_u64 v[178:179], s[26:27], 0, v[162:163]
	global_load_lds_dwordx4 v[178:179], off
	s_add_i32 m0, s28, 0x2000
	v_lshl_add_u64 v[178:179], s[26:27], 0, v[158:159]
	global_load_lds_dwordx4 v[178:179], off
	s_mov_b32 m0, s44
	v_lshl_add_u64 v[178:179], v[220:221], 0, s[56:57]
	global_load_lds_dwordx4 v[178:179], off
	s_mov_b32 m0, s45
	v_lshl_add_u64 v[178:179], v[222:223], 0, s[56:57]
	global_load_lds_dwordx4 v[178:179], off
	s_waitcnt vmcnt(8) lgkmcnt(0)
	s_barrier
	s_setprio 1
	v_mfma_f32_16x16x32_bf16 v[62:65], v[130:133], v[174:177], v[62:65]
	v_mfma_f32_16x16x32_bf16 v[58:61], v[138:141], v[174:177], v[58:61]
	v_mfma_f32_16x16x32_bf16 v[46:49], v[130:133], v[188:191], v[46:49]
	v_mfma_f32_16x16x32_bf16 v[42:45], v[138:141], v[188:191], v[42:45]
	v_mfma_f32_16x16x32_bf16 v[30:33], v[130:133], v[196:199], v[30:33]
	v_mfma_f32_16x16x32_bf16 v[26:29], v[138:141], v[196:199], v[26:29]
	v_mfma_f32_16x16x32_bf16 v[14:17], v[130:133], v[204:207], v[14:17]
	v_mfma_f32_16x16x32_bf16 v[10:13], v[138:141], v[204:207], v[10:13]
	v_mfma_f32_16x16x32_bf16 v[62:65], v[134:137], v[184:187], v[62:65]
	v_mfma_f32_16x16x32_bf16 v[58:61], v[142:145], v[184:187], v[58:61]
	v_mfma_f32_16x16x32_bf16 v[46:49], v[134:137], v[192:195], v[46:49]
	v_mfma_f32_16x16x32_bf16 v[42:45], v[142:145], v[192:195], v[42:45]
	v_mfma_f32_16x16x32_bf16 v[30:33], v[134:137], v[200:203], v[30:33]
	v_mfma_f32_16x16x32_bf16 v[26:29], v[142:145], v[200:203], v[26:29]
	v_mfma_f32_16x16x32_bf16 v[14:17], v[134:137], v[216:219], v[14:17]
	v_mfma_f32_16x16x32_bf16 v[10:13], v[142:145], v[216:219], v[10:13]
	s_setprio 0
	s_setprio 1
	v_mfma_f32_16x16x32_bf16 v[54:57], v[146:149], v[174:177], v[54:57]
	v_mfma_f32_16x16x32_bf16 v[50:53], v[154:157], v[174:177], v[50:53]
	v_mfma_f32_16x16x32_bf16 v[38:41], v[146:149], v[188:191], v[38:41]
	v_mfma_f32_16x16x32_bf16 v[34:37], v[154:157], v[188:191], v[34:37]
	v_mfma_f32_16x16x32_bf16 v[22:25], v[146:149], v[196:199], v[22:25]
	v_mfma_f32_16x16x32_bf16 v[18:21], v[154:157], v[196:199], v[18:21]
	v_mfma_f32_16x16x32_bf16 v[6:9], v[146:149], v[204:207], v[6:9]
	v_mfma_f32_16x16x32_bf16 v[2:5], v[154:157], v[204:207], v[2:5]
	v_mfma_f32_16x16x32_bf16 v[54:57], v[150:153], v[184:187], v[54:57]
	v_mfma_f32_16x16x32_bf16 v[50:53], v[170:173], v[184:187], v[50:53]
	v_mfma_f32_16x16x32_bf16 v[38:41], v[150:153], v[192:195], v[38:41]
	v_mfma_f32_16x16x32_bf16 v[34:37], v[170:173], v[192:195], v[34:37]
	v_mfma_f32_16x16x32_bf16 v[22:25], v[150:153], v[200:203], v[22:25]
	v_mfma_f32_16x16x32_bf16 v[18:21], v[170:173], v[200:203], v[18:21]
	v_mfma_f32_16x16x32_bf16 v[6:9], v[150:153], v[216:219], v[6:9]
	v_mfma_f32_16x16x32_bf16 v[2:5], v[170:173], v[216:219], v[2:5]
	s_setprio 0
	s_barrier
	s_add_i32 s49, s49, 2
	s_add_u32 s41, s41, 0x100
	s_addc_u32 s48, s48, 0
	s_add_u32 s6, s6, 0x100
	s_addc_u32 s7, s7, 0
	s_cmp_gt_u32 s49, 13
	s_cbranch_scc0 .LBB0_2626
	s_and_b64 vcc, exec, s[16:17]
	s_cbranch_vccz .LBB0_2629
	s_barrier

.LBB0_2703:
	s_add_u32 s44, s24, s36
	s_addc_u32 s45, s25, s37
	s_add_u32 s44, s44, 0x100
	s_addc_u32 s45, s45, 0
	s_add_u32 s50, s59, s36
	s_addc_u32 s64, s82, s37
	s_add_i32 s65, 0, 0x10000
	s_cmpk_eq_i32 s36, 0x1f00
	s_cselect_b32 s47, s29, s45
	s_cselect_b32 s46, s83, s44
	s_cselect_b32 s45, s27, s64
	s_cselect_b32 s44, s84, s50
	s_add_i32 s50, 0, 0x14000
	v_add_u32_e32 v160, s65, v146
	v_add_u32_e32 v164, s50, v146
	ds_read_b128 v[148:151], v160
	ds_read_b128 v[152:155], v160 offset:1024
	ds_read_b128 v[156:159], v160 offset:2048
	ds_read_b128 v[160:163], v160 offset:3072
	ds_read_b128 v[168:171], v164
	ds_read_b128 v[172:175], v164 offset:1024
	ds_read_b128 v[176:179], v164 offset:2048
	ds_read_b128 v[180:183], v164 offset:3072
	v_lshl_add_u64 v[164:165], v[144:145], 0, s[36:37]
	s_add_i32 m0, s4, 0xc000
	ds_read_b128 v[184:187], v147
	ds_read_b128 v[188:191], v147 offset:1024
	ds_read_b128 v[192:195], v147 offset:2048
	ds_read_b128 v[196:199], v147 offset:3072
	ds_read_b128 v[200:203], v147 offset:4096
	ds_read_b128 v[204:207], v147 offset:5120
	ds_read_b128 v[216:219], v147 offset:6144
	ds_read_b128 v[220:223], v147 offset:7168
	global_load_lds_dwordx4 v[164:165], off
	s_add_i32 m0, s4, 0xe000
	v_lshl_add_u64 v[164:165], v[142:143], 0, s[36:37]
	global_load_lds_dwordx4 v[164:165], off
	s_waitcnt vmcnt(8) lgkmcnt(0)
	s_barrier
	s_setprio 1
	v_mfma_f32_16x16x32_bf16 v[134:137], v[148:151], v[184:187], v[134:137]
	v_mfma_f32_16x16x32_bf16 v[130:133], v[156:159], v[184:187], v[130:133]
	v_mfma_f32_16x16x32_bf16 v[110:113], v[148:151], v[192:195], v[110:113]
	v_mfma_f32_16x16x32_bf16 v[106:109], v[156:159], v[192:195], v[106:109]
	v_mfma_f32_16x16x32_bf16 v[94:97], v[148:151], v[200:203], v[94:97]
	v_mfma_f32_16x16x32_bf16 v[90:93], v[156:159], v[200:203], v[90:93]
	v_mfma_f32_16x16x32_bf16 v[78:81], v[148:151], v[216:219], v[78:81]
	v_mfma_f32_16x16x32_bf16 v[74:77], v[156:159], v[216:219], v[74:77]
	v_mfma_f32_16x16x32_bf16 v[134:137], v[152:155], v[188:191], v[134:137]
	v_mfma_f32_16x16x32_bf16 v[130:133], v[160:163], v[188:191], v[130:133]
	v_mfma_f32_16x16x32_bf16 v[110:113], v[152:155], v[196:199], v[110:113]
	v_mfma_f32_16x16x32_bf16 v[106:109], v[160:163], v[196:199], v[106:109]
	v_mfma_f32_16x16x32_bf16 v[94:97], v[152:155], v[204:207], v[94:97]
	v_mfma_f32_16x16x32_bf16 v[90:93], v[160:163], v[204:207], v[90:93]
	v_mfma_f32_16x16x32_bf16 v[78:81], v[152:155], v[220:223], v[78:81]
	v_mfma_f32_16x16x32_bf16 v[74:77], v[160:163], v[220:223], v[74:77]
	s_setprio 0
	s_setprio 1
	v_mfma_f32_16x16x32_bf16 v[122:125], v[168:171], v[184:187], v[122:125]
	v_mfma_f32_16x16x32_bf16 v[114:117], v[176:179], v[184:187], v[114:117]
	v_mfma_f32_16x16x32_bf16 v[102:105], v[168:171], v[192:195], v[102:105]
	v_mfma_f32_16x16x32_bf16 v[98:101], v[176:179], v[192:195], v[98:101]
	v_mfma_f32_16x16x32_bf16 v[86:89], v[168:171], v[200:203], v[86:89]
	v_mfma_f32_16x16x32_bf16 v[82:85], v[176:179], v[200:203], v[82:85]
	v_mfma_f32_16x16x32_bf16 v[70:73], v[168:171], v[216:219], v[70:73]
	v_mfma_f32_16x16x32_bf16 v[66:69], v[176:179], v[216:219], v[66:69]
	v_mfma_f32_16x16x32_bf16 v[122:125], v[172:175], v[188:191], v[122:125]
	v_mfma_f32_16x16x32_bf16 v[114:117], v[180:183], v[188:191], v[114:117]
	v_mfma_f32_16x16x32_bf16 v[102:105], v[172:175], v[196:199], v[102:105]
	v_mfma_f32_16x16x32_bf16 v[98:101], v[180:183], v[196:199], v[98:101]
	v_mfma_f32_16x16x32_bf16 v[86:89], v[172:175], v[204:207], v[86:89]
	v_mfma_f32_16x16x32_bf16 v[82:85], v[180:183], v[204:207], v[82:85]
	v_mfma_f32_16x16x32_bf16 v[70:73], v[172:175], v[220:223], v[70:73]
	v_mfma_f32_16x16x32_bf16 v[66:69], v[180:183], v[220:223], v[66:69]
	s_setprio 0
	s_barrier
	s_add_i32 s64, s65, s77
	v_lshl_add_u64 v[164:165], s[44:45], 0, v[126:127]
	s_mov_b32 m0, s64
	ds_read_b128 v[184:187], v147 offset:16384
	ds_read_b128 v[188:191], v147 offset:17408
	ds_read_b128 v[192:195], v147 offset:18432
	ds_read_b128 v[196:199], v147 offset:19456
	ds_read_b128 v[200:203], v147 offset:20480
	ds_read_b128 v[204:207], v147 offset:21504
	ds_read_b128 v[216:219], v147 offset:22528
	ds_read_b128 v[220:223], v147 offset:23552
	global_load_lds_dwordx4 v[164:165], off
	s_add_i32 m0, s64, 0x2000
	s_add_u32 s92, s44, 0x100000
	v_lshl_add_u64 v[208:209], s[44:45], 0, v[118:119]
	s_addc_u32 s93, s45, 0
	s_add_i32 s50, s50, s77
	global_load_lds_dwordx4 v[208:209], off
	v_lshl_add_u64 v[224:225], s[92:93], 0, v[126:127]
	s_mov_b32 m0, s50
	v_lshl_add_u64 v[242:243], s[46:47], 0, v[120:121]
	global_load_lds_dwordx4 v[224:225], off
	s_add_i32 m0, s50, 0x2000
	v_lshl_add_u64 v[224:225], s[92:93], 0, v[118:119]
	global_load_lds_dwordx4 v[224:225], off
	s_mov_b32 m0, s4
	v_lshl_add_u64 v[224:225], s[46:47], 0, v[128:129]
	global_load_lds_dwordx4 v[224:225], off
	s_mov_b32 m0, s33
	s_nop 0
	global_load_lds_dwordx4 v[242:243], off
	s_waitcnt vmcnt(8) lgkmcnt(0)
	s_barrier
	s_setprio 1
	v_mfma_f32_16x16x32_bf16 v[62:65], v[148:151], v[184:187], v[62:65]
	v_mfma_f32_16x16x32_bf16 v[58:61], v[156:159], v[184:187], v[58:61]
	v_mfma_f32_16x16x32_bf16 v[46:49], v[148:151], v[192:195], v[46:49]
	v_mfma_f32_16x16x32_bf16 v[42:45], v[156:159], v[192:195], v[42:45]
	v_mfma_f32_16x16x32_bf16 v[30:33], v[148:151], v[200:203], v[30:33]
	v_mfma_f32_16x16x32_bf16 v[26:29], v[156:159], v[200:203], v[26:29]
	v_mfma_f32_16x16x32_bf16 v[14:17], v[148:151], v[216:219], v[14:17]
	v_mfma_f32_16x16x32_bf16 v[10:13], v[156:159], v[216:219], v[10:13]
	v_mfma_f32_16x16x32_bf16 v[62:65], v[152:155], v[188:191], v[62:65]
	v_mfma_f32_16x16x32_bf16 v[58:61], v[160:163], v[188:191], v[58:61]
	v_mfma_f32_16x16x32_bf16 v[46:49], v[152:155], v[196:199], v[46:49]
	v_mfma_f32_16x16x32_bf16 v[42:45], v[160:163], v[196:199], v[42:45]
	v_mfma_f32_16x16x32_bf16 v[30:33], v[152:155], v[204:207], v[30:33]
	v_mfma_f32_16x16x32_bf16 v[26:29], v[160:163], v[204:207], v[26:29]
	v_mfma_f32_16x16x32_bf16 v[14:17], v[152:155], v[220:223], v[14:17]
	v_mfma_f32_16x16x32_bf16 v[10:13], v[160:163], v[220:223], v[10:13]
	s_setprio 0
	s_setprio 1
	v_mfma_f32_16x16x32_bf16 v[54:57], v[168:171], v[184:187], v[54:57]
	v_mfma_f32_16x16x32_bf16 v[50:53], v[176:179], v[184:187], v[50:53]
	v_mfma_f32_16x16x32_bf16 v[38:41], v[168:171], v[192:195], v[38:41]
	v_mfma_f32_16x16x32_bf16 v[34:37], v[176:179], v[192:195], v[34:37]
	v_mfma_f32_16x16x32_bf16 v[22:25], v[168:171], v[200:203], v[22:25]
	v_mfma_f32_16x16x32_bf16 v[18:21], v[176:179], v[200:203], v[18:21]
	v_mfma_f32_16x16x32_bf16 v[6:9], v[168:171], v[216:219], v[6:9]
	v_mfma_f32_16x16x32_bf16 v[2:5], v[176:179], v[216:219], v[2:5]
	v_mfma_f32_16x16x32_bf16 v[54:57], v[172:175], v[188:191], v[54:57]
	v_mfma_f32_16x16x32_bf16 v[50:53], v[180:183], v[188:191], v[50:53]
	v_mfma_f32_16x16x32_bf16 v[38:41], v[172:175], v[196:199], v[38:41]
	v_mfma_f32_16x16x32_bf16 v[34:37], v[180:183], v[196:199], v[34:37]
	v_mfma_f32_16x16x32_bf16 v[22:25], v[172:175], v[204:207], v[22:25]
	v_mfma_f32_16x16x32_bf16 v[18:21], v[180:183], v[204:207], v[18:21]
	v_mfma_f32_16x16x32_bf16 v[6:9], v[172:175], v[220:223], v[6:9]
	v_mfma_f32_16x16x32_bf16 v[2:5], v[180:183], v[220:223], v[2:5]
	s_setprio 0
	s_barrier
	s_add_i32 s50, 0, 0x18000
	s_add_i32 s64, 0, 0x1c000
	v_add_u32_e32 v160, s50, v146
	v_add_u32_e32 v167, s64, v146
	ds_read_b128 v[148:151], v160
	ds_read_b128 v[152:155], v160 offset:1024
	ds_read_b128 v[156:159], v160 offset:2048
	ds_read_b128 v[160:163], v160 offset:3072
	ds_read_b128 v[168:171], v167
	ds_read_b128 v[172:175], v167 offset:1024
	ds_read_b128 v[176:179], v167 offset:2048
	ds_read_b128 v[180:183], v167 offset:3072
	s_add_u32 s46, s46, 0x100000
	s_addc_u32 s47, s47, 0
	s_mov_b32 m0, s78
	v_lshl_add_u64 v[244:245], s[46:47], 0, v[128:129]
	ds_read_b128 v[184:187], v147 offset:32768
	ds_read_b128 v[188:191], v147 offset:33792
	ds_read_b128 v[192:195], v147 offset:34816
	ds_read_b128 v[196:199], v147 offset:35840
	ds_read_b128 v[200:203], v147 offset:36864
	ds_read_b128 v[204:207], v147 offset:37888
	ds_read_b128 v[216:219], v147 offset:38912
	ds_read_b128 v[220:223], v147 offset:39936
	global_load_lds_dwordx4 v[244:245], off
	s_mov_b32 m0, s79
	v_lshl_add_u64 v[244:245], s[46:47], 0, v[120:121]
	global_load_lds_dwordx4 v[244:245], off
	s_waitcnt vmcnt(8) lgkmcnt(0)
	s_barrier
	s_setprio 1
	v_mfma_f32_16x16x32_bf16 v[134:137], v[148:151], v[184:187], v[134:137]
	v_mfma_f32_16x16x32_bf16 v[130:133], v[156:159], v[184:187], v[130:133]
	v_mfma_f32_16x16x32_bf16 v[110:113], v[148:151], v[192:195], v[110:113]
	v_mfma_f32_16x16x32_bf16 v[106:109], v[156:159], v[192:195], v[106:109]
	v_mfma_f32_16x16x32_bf16 v[94:97], v[148:151], v[200:203], v[94:97]
	v_mfma_f32_16x16x32_bf16 v[90:93], v[156:159], v[200:203], v[90:93]
	v_mfma_f32_16x16x32_bf16 v[78:81], v[148:151], v[216:219], v[78:81]
	v_mfma_f32_16x16x32_bf16 v[74:77], v[156:159], v[216:219], v[74:77]
	v_mfma_f32_16x16x32_bf16 v[134:137], v[152:155], v[188:191], v[134:137]
	v_mfma_f32_16x16x32_bf16 v[130:133], v[160:163], v[188:191], v[130:133]
	v_mfma_f32_16x16x32_bf16 v[110:113], v[152:155], v[196:199], v[110:113]
	v_mfma_f32_16x16x32_bf16 v[106:109], v[160:163], v[196:199], v[106:109]
	v_mfma_f32_16x16x32_bf16 v[94:97], v[152:155], v[204:207], v[94:97]
	v_mfma_f32_16x16x32_bf16 v[90:93], v[160:163], v[204:207], v[90:93]
	v_mfma_f32_16x16x32_bf16 v[78:81], v[152:155], v[220:223], v[78:81]
	v_mfma_f32_16x16x32_bf16 v[74:77], v[160:163], v[220:223], v[74:77]
	s_setprio 0
	s_setprio 1
	v_mfma_f32_16x16x32_bf16 v[122:125], v[168:171], v[184:187], v[122:125]
	v_mfma_f32_16x16x32_bf16 v[114:117], v[176:179], v[184:187], v[114:117]
	v_mfma_f32_16x16x32_bf16 v[102:105], v[168:171], v[192:195], v[102:105]
	v_mfma_f32_16x16x32_bf16 v[98:101], v[176:179], v[192:195], v[98:101]
	v_mfma_f32_16x16x32_bf16 v[86:89], v[168:171], v[200:203], v[86:89]
	v_mfma_f32_16x16x32_bf16 v[82:85], v[176:179], v[200:203], v[82:85]
	v_mfma_f32_16x16x32_bf16 v[70:73], v[168:171], v[216:219], v[70:73]
	v_mfma_f32_16x16x32_bf16 v[66:69], v[176:179], v[216:219], v[66:69]
	v_mfma_f32_16x16x32_bf16 v[122:125], v[172:175], v[188:191], v[122:125]
	v_mfma_f32_16x16x32_bf16 v[114:117], v[180:183], v[188:191], v[114:117]
	v_mfma_f32_16x16x32_bf16 v[102:105], v[172:175], v[196:199], v[102:105]
	v_mfma_f32_16x16x32_bf16 v[98:101], v[180:183], v[196:199], v[98:101]
	v_mfma_f32_16x16x32_bf16 v[86:89], v[172:175], v[204:207], v[86:89]
	v_mfma_f32_16x16x32_bf16 v[82:85], v[180:183], v[204:207], v[82:85]
	v_mfma_f32_16x16x32_bf16 v[70:73], v[172:175], v[220:223], v[70:73]
	v_mfma_f32_16x16x32_bf16 v[66:69], v[180:183], v[220:223], v[66:69]
	s_setprio 0
	s_barrier
	s_add_i32 s46, s50, s77
	v_lshl_add_u64 v[164:165], v[164:165], 0, s[56:57]
	s_mov_b32 m0, s46
	ds_read_b128 v[184:187], v147 offset:49152
	ds_read_b128 v[188:191], v147 offset:50176
	ds_read_b128 v[192:195], v147 offset:51200
	ds_read_b128 v[196:199], v147 offset:52224
	ds_read_b128 v[200:203], v147 offset:53248
	ds_read_b128 v[204:207], v147 offset:54272
	ds_read_b128 v[216:219], v147 offset:55296
	ds_read_b128 v[220:223], v147 offset:56320
	global_load_lds_dwordx4 v[164:165], off
	s_add_i32 m0, s46, 0x2000
	s_add_u32 s44, s44, 0x100080
	v_lshl_add_u64 v[164:165], v[208:209], 0, s[56:57]
	s_addc_u32 s45, s45, 0
	s_add_i32 s46, s64, s77
	global_load_lds_dwordx4 v[164:165], off
	s_mov_b32 m0, s46
	v_lshl_add_u64 v[164:165], s[44:45], 0, v[126:127]
	global_load_lds_dwordx4 v[164:165], off
	s_add_i32 m0, s46, 0x2000
	v_lshl_add_u64 v[164:165], s[44:45], 0, v[118:119]
	global_load_lds_dwordx4 v[164:165], off
	s_mov_b32 m0, s80
	v_lshl_add_u64 v[164:165], v[224:225], 0, s[56:57]
	global_load_lds_dwordx4 v[164:165], off
	s_mov_b32 m0, s81
	v_lshl_add_u64 v[164:165], v[242:243], 0, s[56:57]
	global_load_lds_dwordx4 v[164:165], off
	s_waitcnt vmcnt(8) lgkmcnt(0)
	s_barrier
	s_setprio 1
	v_mfma_f32_16x16x32_bf16 v[62:65], v[148:151], v[184:187], v[62:65]
	v_mfma_f32_16x16x32_bf16 v[58:61], v[156:159], v[184:187], v[58:61]
	v_mfma_f32_16x16x32_bf16 v[46:49], v[148:151], v[192:195], v[46:49]
	v_mfma_f32_16x16x32_bf16 v[42:45], v[156:159], v[192:195], v[42:45]
	v_mfma_f32_16x16x32_bf16 v[30:33], v[148:151], v[200:203], v[30:33]
	v_mfma_f32_16x16x32_bf16 v[26:29], v[156:159], v[200:203], v[26:29]
	v_mfma_f32_16x16x32_bf16 v[14:17], v[148:151], v[216:219], v[14:17]
	v_mfma_f32_16x16x32_bf16 v[10:13], v[156:159], v[216:219], v[10:13]
	v_mfma_f32_16x16x32_bf16 v[62:65], v[152:155], v[188:191], v[62:65]
	v_mfma_f32_16x16x32_bf16 v[58:61], v[160:163], v[188:191], v[58:61]
	v_mfma_f32_16x16x32_bf16 v[46:49], v[152:155], v[196:199], v[46:49]
	v_mfma_f32_16x16x32_bf16 v[42:45], v[160:163], v[196:199], v[42:45]
	v_mfma_f32_16x16x32_bf16 v[30:33], v[152:155], v[204:207], v[30:33]
	v_mfma_f32_16x16x32_bf16 v[26:29], v[160:163], v[204:207], v[26:29]
	v_mfma_f32_16x16x32_bf16 v[14:17], v[152:155], v[220:223], v[14:17]
	v_mfma_f32_16x16x32_bf16 v[10:13], v[160:163], v[220:223], v[10:13]
	s_setprio 0
	s_setprio 1
	v_mfma_f32_16x16x32_bf16 v[54:57], v[168:171], v[184:187], v[54:57]
	v_mfma_f32_16x16x32_bf16 v[50:53], v[176:179], v[184:187], v[50:53]
	v_mfma_f32_16x16x32_bf16 v[38:41], v[168:171], v[192:195], v[38:41]
	v_mfma_f32_16x16x32_bf16 v[34:37], v[176:179], v[192:195], v[34:37]
	v_mfma_f32_16x16x32_bf16 v[22:25], v[168:171], v[200:203], v[22:25]
	v_mfma_f32_16x16x32_bf16 v[18:21], v[176:179], v[200:203], v[18:21]
	v_mfma_f32_16x16x32_bf16 v[6:9], v[168:171], v[216:219], v[6:9]
	v_mfma_f32_16x16x32_bf16 v[2:5], v[176:179], v[216:219], v[2:5]
	v_mfma_f32_16x16x32_bf16 v[54:57], v[172:175], v[188:191], v[54:57]
	v_mfma_f32_16x16x32_bf16 v[50:53], v[180:183], v[188:191], v[50:53]
	v_mfma_f32_16x16x32_bf16 v[38:41], v[172:175], v[196:199], v[38:41]
	v_mfma_f32_16x16x32_bf16 v[34:37], v[180:183], v[196:199], v[34:37]
	v_mfma_f32_16x16x32_bf16 v[22:25], v[172:175], v[204:207], v[22:25]
	v_mfma_f32_16x16x32_bf16 v[18:21], v[180:183], v[204:207], v[18:21]
	v_mfma_f32_16x16x32_bf16 v[6:9], v[172:175], v[220:223], v[6:9]
	v_mfma_f32_16x16x32_bf16 v[2:5], v[180:183], v[220:223], v[2:5]
	s_setprio 0
	s_barrier
	s_add_i32 s85, s85, 2
	s_add_u32 s36, s36, 0x100
	s_addc_u32 s37, s37, 0
	s_cmp_gt_u32 s85, 61
	s_cbranch_scc0 .LBB0_2703
	s_add_u32 s36, s59, 0xffffff00
	s_addc_u32 s37, s82, -1
	s_andn2_b64 vcc, exec, s[42:43]
	s_cbranch_vccnz .LBB0_2706
	v_mov_b32_e32 v2, 0
	s_mov_b32 s12, s26
	s_mov_b32 s53, s28
	s_mov_b64 s[24:25], s[34:35]
	s_mov_b32 s68, s58
	v_mov_b32_e32 v3, v2
	v_mov_b32_e32 v4, v2
	v_mov_b32_e32 v5, v2
	v_mov_b32_e32 v6, v2
	v_mov_b32_e32 v7, v2
	v_mov_b32_e32 v8, v2
	v_mov_b32_e32 v9, v2
	v_mov_b32_e32 v18, v2
	v_mov_b32_e32 v19, v2
	v_mov_b32_e32 v20, v2
	v_mov_b32_e32 v21, v2
	v_mov_b32_e32 v22, v2
	v_mov_b32_e32 v23, v2
	v_mov_b32_e32 v24, v2
	v_mov_b32_e32 v25, v2
	v_mov_b32_e32 v34, v2
	v_mov_b32_e32 v35, v2
	v_mov_b32_e32 v36, v2
	v_mov_b32_e32 v37, v2
	v_mov_b32_e32 v38, v2
	v_mov_b32_e32 v39, v2
	v_mov_b32_e32 v40, v2
	v_mov_b32_e32 v41, v2
	v_mov_b32_e32 v50, v2
	v_mov_b32_e32 v51, v2
	v_mov_b32_e32 v52, v2
	v_mov_b32_e32 v53, v2
	v_mov_b32_e32 v54, v2
	v_mov_b32_e32 v55, v2
	v_mov_b32_e32 v56, v2
	v_mov_b32_e32 v57, v2
	v_mov_b32_e32 v10, v2
	v_mov_b32_e32 v11, v2
	v_mov_b32_e32 v12, v2
	v_mov_b32_e32 v13, v2
	v_mov_b32_e32 v14, v2
	v_mov_b32_e32 v15, v2
	v_mov_b32_e32 v16, v2
	v_mov_b32_e32 v17, v2
	v_mov_b32_e32 v26, v2
	v_mov_b32_e32 v27, v2
	v_mov_b32_e32 v28, v2
	v_mov_b32_e32 v29, v2
	v_mov_b32_e32 v30, v2
	v_mov_b32_e32 v31, v2
	v_mov_b32_e32 v32, v2
	v_mov_b32_e32 v33, v2
	v_mov_b32_e32 v42, v2
	v_mov_b32_e32 v43, v2
	v_mov_b32_e32 v44, v2
	v_mov_b32_e32 v45, v2
	v_mov_b32_e32 v46, v2
	v_mov_b32_e32 v47, v2
	v_mov_b32_e32 v48, v2
	v_mov_b32_e32 v49, v2
	v_mov_b32_e32 v58, v2
	v_mov_b32_e32 v59, v2
	v_mov_b32_e32 v60, v2
	v_mov_b32_e32 v61, v2
	v_mov_b32_e32 v62, v2
	v_mov_b32_e32 v63, v2
	v_mov_b32_e32 v64, v2
	v_mov_b32_e32 v65, v2
	v_mov_b32_e32 v66, v2
	v_mov_b32_e32 v67, v2
	v_mov_b32_e32 v68, v2
	v_mov_b32_e32 v69, v2
	v_mov_b32_e32 v70, v2
	v_mov_b32_e32 v71, v2
	v_mov_b32_e32 v72, v2
	v_mov_b32_e32 v73, v2
	v_mov_b32_e32 v82, v2
	v_mov_b32_e32 v83, v2
	v_mov_b32_e32 v84, v2
	v_mov_b32_e32 v85, v2
	v_mov_b32_e32 v86, v2
	v_mov_b32_e32 v87, v2
	v_mov_b32_e32 v88, v2
	v_mov_b32_e32 v89, v2
	v_mov_b32_e32 v98, v2
	v_mov_b32_e32 v99, v2
	v_mov_b32_e32 v100, v2
	v_mov_b32_e32 v101, v2
	v_mov_b32_e32 v102, v2
	v_mov_b32_e32 v103, v2
	v_mov_b32_e32 v104, v2
	v_mov_b32_e32 v105, v2
	v_mov_b32_e32 v114, v2
	v_mov_b32_e32 v115, v2
	v_mov_b32_e32 v116, v2
	v_mov_b32_e32 v117, v2
	v_mov_b32_e32 v122, v2
	v_mov_b32_e32 v123, v2
	v_mov_b32_e32 v124, v2
	v_mov_b32_e32 v125, v2
	v_mov_b32_e32 v74, v2
	v_mov_b32_e32 v75, v2
	v_mov_b32_e32 v76, v2
	v_mov_b32_e32 v77, v2
	v_mov_b32_e32 v78, v2
	v_mov_b32_e32 v79, v2
	v_mov_b32_e32 v80, v2
	v_mov_b32_e32 v81, v2
	v_mov_b32_e32 v90, v2
	v_mov_b32_e32 v91, v2
	v_mov_b32_e32 v92, v2
	v_mov_b32_e32 v93, v2
	v_mov_b32_e32 v94, v2
	v_mov_b32_e32 v95, v2
	v_mov_b32_e32 v96, v2
	v_mov_b32_e32 v97, v2
	v_mov_b32_e32 v106, v2
	v_mov_b32_e32 v107, v2
	v_mov_b32_e32 v108, v2
	v_mov_b32_e32 v109, v2
	v_mov_b32_e32 v110, v2
	v_mov_b32_e32 v111, v2
	v_mov_b32_e32 v112, v2
	v_mov_b32_e32 v113, v2
	v_mov_b32_e32 v130, v2
	v_mov_b32_e32 v131, v2
	v_mov_b32_e32 v132, v2
	v_mov_b32_e32 v133, v2
	v_mov_b32_e32 v134, v2
	v_mov_b32_e32 v135, v2
	v_mov_b32_e32 v136, v2
	v_mov_b32_e32 v137, v2
	s_movk_i32 s92, 0x2b20
	s_andn2_b64 vcc, exec, s[40:41]
	s_cbranch_vccnz .LBB0_2707
	s_branch .LBB0_2708

.LBB0_2796:
	s_add_u32 s44, s24, s36
	s_addc_u32 s45, s25, s37
	s_add_u32 s44, s44, 0x100
	s_addc_u32 s45, s45, 0
	s_add_u32 s50, s59, s36
	s_addc_u32 s64, s81, s37
	s_add_i32 s65, 0, 0x10000
	s_cmpk_eq_i32 s36, 0x1f00
	s_cselect_b32 s47, s29, s45
	s_cselect_b32 s46, s82, s44
	s_cselect_b32 s45, s27, s64
	s_cselect_b32 s44, s83, s50
	s_add_i32 s50, 0, 0x14000
	v_add_u32_e32 v160, s65, v146
	v_add_u32_e32 v164, s50, v146
	ds_read_b128 v[148:151], v160
	ds_read_b128 v[152:155], v160 offset:1024
	ds_read_b128 v[156:159], v160 offset:2048
	ds_read_b128 v[160:163], v160 offset:3072
	ds_read_b128 v[168:171], v164
	ds_read_b128 v[172:175], v164 offset:1024
	ds_read_b128 v[176:179], v164 offset:2048
	ds_read_b128 v[180:183], v164 offset:3072
	v_lshl_add_u64 v[164:165], v[144:145], 0, s[36:37]
	s_add_i32 m0, s4, 0xc000
	ds_read_b128 v[184:187], v147
	ds_read_b128 v[188:191], v147 offset:1024
	ds_read_b128 v[192:195], v147 offset:2048
	ds_read_b128 v[196:199], v147 offset:3072
	ds_read_b128 v[200:203], v147 offset:4096
	ds_read_b128 v[204:207], v147 offset:5120
	ds_read_b128 v[216:219], v147 offset:6144
	ds_read_b128 v[220:223], v147 offset:7168
	global_load_lds_dwordx4 v[164:165], off
	s_add_i32 m0, s4, 0xe000
	v_lshl_add_u64 v[164:165], v[142:143], 0, s[36:37]
	global_load_lds_dwordx4 v[164:165], off
	s_waitcnt vmcnt(8) lgkmcnt(0)
	s_barrier
	s_setprio 1
	v_mfma_f32_16x16x32_bf16 v[134:137], v[148:151], v[184:187], v[134:137]
	v_mfma_f32_16x16x32_bf16 v[130:133], v[156:159], v[184:187], v[130:133]
	v_mfma_f32_16x16x32_bf16 v[110:113], v[148:151], v[192:195], v[110:113]
	v_mfma_f32_16x16x32_bf16 v[106:109], v[156:159], v[192:195], v[106:109]
	v_mfma_f32_16x16x32_bf16 v[94:97], v[148:151], v[200:203], v[94:97]
	v_mfma_f32_16x16x32_bf16 v[90:93], v[156:159], v[200:203], v[90:93]
	v_mfma_f32_16x16x32_bf16 v[78:81], v[148:151], v[216:219], v[78:81]
	v_mfma_f32_16x16x32_bf16 v[74:77], v[156:159], v[216:219], v[74:77]
	v_mfma_f32_16x16x32_bf16 v[134:137], v[152:155], v[188:191], v[134:137]
	v_mfma_f32_16x16x32_bf16 v[130:133], v[160:163], v[188:191], v[130:133]
	v_mfma_f32_16x16x32_bf16 v[110:113], v[152:155], v[196:199], v[110:113]
	v_mfma_f32_16x16x32_bf16 v[106:109], v[160:163], v[196:199], v[106:109]
	v_mfma_f32_16x16x32_bf16 v[94:97], v[152:155], v[204:207], v[94:97]
	v_mfma_f32_16x16x32_bf16 v[90:93], v[160:163], v[204:207], v[90:93]
	v_mfma_f32_16x16x32_bf16 v[78:81], v[152:155], v[220:223], v[78:81]
	v_mfma_f32_16x16x32_bf16 v[74:77], v[160:163], v[220:223], v[74:77]
	s_setprio 0
	s_setprio 1
	v_mfma_f32_16x16x32_bf16 v[122:125], v[168:171], v[184:187], v[122:125]
	v_mfma_f32_16x16x32_bf16 v[114:117], v[176:179], v[184:187], v[114:117]
	v_mfma_f32_16x16x32_bf16 v[102:105], v[168:171], v[192:195], v[102:105]
	v_mfma_f32_16x16x32_bf16 v[98:101], v[176:179], v[192:195], v[98:101]
	v_mfma_f32_16x16x32_bf16 v[86:89], v[168:171], v[200:203], v[86:89]
	v_mfma_f32_16x16x32_bf16 v[82:85], v[176:179], v[200:203], v[82:85]
	v_mfma_f32_16x16x32_bf16 v[70:73], v[168:171], v[216:219], v[70:73]
	v_mfma_f32_16x16x32_bf16 v[66:69], v[176:179], v[216:219], v[66:69]
	v_mfma_f32_16x16x32_bf16 v[122:125], v[172:175], v[188:191], v[122:125]
	v_mfma_f32_16x16x32_bf16 v[114:117], v[180:183], v[188:191], v[114:117]
	v_mfma_f32_16x16x32_bf16 v[102:105], v[172:175], v[196:199], v[102:105]
	v_mfma_f32_16x16x32_bf16 v[98:101], v[180:183], v[196:199], v[98:101]
	v_mfma_f32_16x16x32_bf16 v[86:89], v[172:175], v[204:207], v[86:89]
	v_mfma_f32_16x16x32_bf16 v[82:85], v[180:183], v[204:207], v[82:85]
	v_mfma_f32_16x16x32_bf16 v[70:73], v[172:175], v[220:223], v[70:73]
	v_mfma_f32_16x16x32_bf16 v[66:69], v[180:183], v[220:223], v[66:69]
	s_setprio 0
	s_barrier
	s_add_i32 s64, s65, s71
	v_lshl_add_u64 v[164:165], s[44:45], 0, v[126:127]
	s_mov_b32 m0, s64
	ds_read_b128 v[184:187], v147 offset:16384
	ds_read_b128 v[188:191], v147 offset:17408
	ds_read_b128 v[192:195], v147 offset:18432
	ds_read_b128 v[196:199], v147 offset:19456
	ds_read_b128 v[200:203], v147 offset:20480
	ds_read_b128 v[204:207], v147 offset:21504
	ds_read_b128 v[216:219], v147 offset:22528
	ds_read_b128 v[220:223], v147 offset:23552
	global_load_lds_dwordx4 v[164:165], off
	s_add_i32 m0, s64, 0x2000
	s_add_u32 s92, s44, 0x100000
	v_lshl_add_u64 v[208:209], s[44:45], 0, v[118:119]
	s_addc_u32 s93, s45, 0
	s_add_i32 s50, s50, s71
	global_load_lds_dwordx4 v[208:209], off
	v_lshl_add_u64 v[224:225], s[92:93], 0, v[126:127]
	s_mov_b32 m0, s50
	v_lshl_add_u64 v[242:243], s[46:47], 0, v[120:121]
	global_load_lds_dwordx4 v[224:225], off
	s_add_i32 m0, s50, 0x2000
	v_lshl_add_u64 v[224:225], s[92:93], 0, v[118:119]
	global_load_lds_dwordx4 v[224:225], off
	s_mov_b32 m0, s4
	v_lshl_add_u64 v[224:225], s[46:47], 0, v[128:129]
	global_load_lds_dwordx4 v[224:225], off
	s_mov_b32 m0, s33
	s_nop 0
	global_load_lds_dwordx4 v[242:243], off
	s_waitcnt vmcnt(8) lgkmcnt(0)
	s_barrier
	s_setprio 1
	v_mfma_f32_16x16x32_bf16 v[62:65], v[148:151], v[184:187], v[62:65]
	v_mfma_f32_16x16x32_bf16 v[58:61], v[156:159], v[184:187], v[58:61]
	v_mfma_f32_16x16x32_bf16 v[46:49], v[148:151], v[192:195], v[46:49]
	v_mfma_f32_16x16x32_bf16 v[42:45], v[156:159], v[192:195], v[42:45]
	v_mfma_f32_16x16x32_bf16 v[30:33], v[148:151], v[200:203], v[30:33]
	v_mfma_f32_16x16x32_bf16 v[26:29], v[156:159], v[200:203], v[26:29]
	v_mfma_f32_16x16x32_bf16 v[14:17], v[148:151], v[216:219], v[14:17]
	v_mfma_f32_16x16x32_bf16 v[10:13], v[156:159], v[216:219], v[10:13]
	v_mfma_f32_16x16x32_bf16 v[62:65], v[152:155], v[188:191], v[62:65]
	v_mfma_f32_16x16x32_bf16 v[58:61], v[160:163], v[188:191], v[58:61]
	v_mfma_f32_16x16x32_bf16 v[46:49], v[152:155], v[196:199], v[46:49]
	v_mfma_f32_16x16x32_bf16 v[42:45], v[160:163], v[196:199], v[42:45]
	v_mfma_f32_16x16x32_bf16 v[30:33], v[152:155], v[204:207], v[30:33]
	v_mfma_f32_16x16x32_bf16 v[26:29], v[160:163], v[204:207], v[26:29]
	v_mfma_f32_16x16x32_bf16 v[14:17], v[152:155], v[220:223], v[14:17]
	v_mfma_f32_16x16x32_bf16 v[10:13], v[160:163], v[220:223], v[10:13]
	s_setprio 0
	s_setprio 1
	v_mfma_f32_16x16x32_bf16 v[54:57], v[168:171], v[184:187], v[54:57]
	v_mfma_f32_16x16x32_bf16 v[50:53], v[176:179], v[184:187], v[50:53]
	v_mfma_f32_16x16x32_bf16 v[38:41], v[168:171], v[192:195], v[38:41]
	v_mfma_f32_16x16x32_bf16 v[34:37], v[176:179], v[192:195], v[34:37]
	v_mfma_f32_16x16x32_bf16 v[22:25], v[168:171], v[200:203], v[22:25]
	v_mfma_f32_16x16x32_bf16 v[18:21], v[176:179], v[200:203], v[18:21]
	v_mfma_f32_16x16x32_bf16 v[6:9], v[168:171], v[216:219], v[6:9]
	v_mfma_f32_16x16x32_bf16 v[2:5], v[176:179], v[216:219], v[2:5]
	v_mfma_f32_16x16x32_bf16 v[54:57], v[172:175], v[188:191], v[54:57]
	v_mfma_f32_16x16x32_bf16 v[50:53], v[180:183], v[188:191], v[50:53]
	v_mfma_f32_16x16x32_bf16 v[38:41], v[172:175], v[196:199], v[38:41]
	v_mfma_f32_16x16x32_bf16 v[34:37], v[180:183], v[196:199], v[34:37]
	v_mfma_f32_16x16x32_bf16 v[22:25], v[172:175], v[204:207], v[22:25]
	v_mfma_f32_16x16x32_bf16 v[18:21], v[180:183], v[204:207], v[18:21]
	v_mfma_f32_16x16x32_bf16 v[6:9], v[172:175], v[220:223], v[6:9]
	v_mfma_f32_16x16x32_bf16 v[2:5], v[180:183], v[220:223], v[2:5]
	s_setprio 0
	s_barrier
	s_add_i32 s50, 0, 0x18000
	s_add_i32 s64, 0, 0x1c000
	v_add_u32_e32 v160, s50, v146
	v_add_u32_e32 v167, s64, v146
	ds_read_b128 v[148:151], v160
	ds_read_b128 v[152:155], v160 offset:1024
	ds_read_b128 v[156:159], v160 offset:2048
	ds_read_b128 v[160:163], v160 offset:3072
	ds_read_b128 v[168:171], v167
	ds_read_b128 v[172:175], v167 offset:1024
	ds_read_b128 v[176:179], v167 offset:2048
	ds_read_b128 v[180:183], v167 offset:3072
	s_add_u32 s46, s46, 0x100000
	s_addc_u32 s47, s47, 0
	s_mov_b32 m0, s76
	v_lshl_add_u64 v[244:245], s[46:47], 0, v[128:129]
	ds_read_b128 v[184:187], v147 offset:32768
	ds_read_b128 v[188:191], v147 offset:33792
	ds_read_b128 v[192:195], v147 offset:34816
	ds_read_b128 v[196:199], v147 offset:35840
	ds_read_b128 v[200:203], v147 offset:36864
	ds_read_b128 v[204:207], v147 offset:37888
	ds_read_b128 v[216:219], v147 offset:38912
	ds_read_b128 v[220:223], v147 offset:39936
	global_load_lds_dwordx4 v[244:245], off
	s_mov_b32 m0, s77
	v_lshl_add_u64 v[244:245], s[46:47], 0, v[120:121]
	global_load_lds_dwordx4 v[244:245], off
	s_waitcnt vmcnt(8) lgkmcnt(0)
	s_barrier
	s_setprio 1
	v_mfma_f32_16x16x32_bf16 v[134:137], v[148:151], v[184:187], v[134:137]
	v_mfma_f32_16x16x32_bf16 v[130:133], v[156:159], v[184:187], v[130:133]
	v_mfma_f32_16x16x32_bf16 v[110:113], v[148:151], v[192:195], v[110:113]
	v_mfma_f32_16x16x32_bf16 v[106:109], v[156:159], v[192:195], v[106:109]
	v_mfma_f32_16x16x32_bf16 v[94:97], v[148:151], v[200:203], v[94:97]
	v_mfma_f32_16x16x32_bf16 v[90:93], v[156:159], v[200:203], v[90:93]
	v_mfma_f32_16x16x32_bf16 v[78:81], v[148:151], v[216:219], v[78:81]
	v_mfma_f32_16x16x32_bf16 v[74:77], v[156:159], v[216:219], v[74:77]
	v_mfma_f32_16x16x32_bf16 v[134:137], v[152:155], v[188:191], v[134:137]
	v_mfma_f32_16x16x32_bf16 v[130:133], v[160:163], v[188:191], v[130:133]
	v_mfma_f32_16x16x32_bf16 v[110:113], v[152:155], v[196:199], v[110:113]
	v_mfma_f32_16x16x32_bf16 v[106:109], v[160:163], v[196:199], v[106:109]
	v_mfma_f32_16x16x32_bf16 v[94:97], v[152:155], v[204:207], v[94:97]
	v_mfma_f32_16x16x32_bf16 v[90:93], v[160:163], v[204:207], v[90:93]
	v_mfma_f32_16x16x32_bf16 v[78:81], v[152:155], v[220:223], v[78:81]
	v_mfma_f32_16x16x32_bf16 v[74:77], v[160:163], v[220:223], v[74:77]
	s_setprio 0
	s_setprio 1
	v_mfma_f32_16x16x32_bf16 v[122:125], v[168:171], v[184:187], v[122:125]
	v_mfma_f32_16x16x32_bf16 v[114:117], v[176:179], v[184:187], v[114:117]
	v_mfma_f32_16x16x32_bf16 v[102:105], v[168:171], v[192:195], v[102:105]
	v_mfma_f32_16x16x32_bf16 v[98:101], v[176:179], v[192:195], v[98:101]
	v_mfma_f32_16x16x32_bf16 v[86:89], v[168:171], v[200:203], v[86:89]
	v_mfma_f32_16x16x32_bf16 v[82:85], v[176:179], v[200:203], v[82:85]
	v_mfma_f32_16x16x32_bf16 v[70:73], v[168:171], v[216:219], v[70:73]
	v_mfma_f32_16x16x32_bf16 v[66:69], v[176:179], v[216:219], v[66:69]
	v_mfma_f32_16x16x32_bf16 v[122:125], v[172:175], v[188:191], v[122:125]
	v_mfma_f32_16x16x32_bf16 v[114:117], v[180:183], v[188:191], v[114:117]
	v_mfma_f32_16x16x32_bf16 v[102:105], v[172:175], v[196:199], v[102:105]
	v_mfma_f32_16x16x32_bf16 v[98:101], v[180:183], v[196:199], v[98:101]
	v_mfma_f32_16x16x32_bf16 v[86:89], v[172:175], v[204:207], v[86:89]
	v_mfma_f32_16x16x32_bf16 v[82:85], v[180:183], v[204:207], v[82:85]
	v_mfma_f32_16x16x32_bf16 v[70:73], v[172:175], v[220:223], v[70:73]
	v_mfma_f32_16x16x32_bf16 v[66:69], v[180:183], v[220:223], v[66:69]
	s_setprio 0
	s_barrier
	s_add_i32 s46, s50, s71
	v_lshl_add_u64 v[164:165], v[164:165], 0, s[56:57]
	s_mov_b32 m0, s46
	ds_read_b128 v[184:187], v147 offset:49152
	ds_read_b128 v[188:191], v147 offset:50176
	ds_read_b128 v[192:195], v147 offset:51200
	ds_read_b128 v[196:199], v147 offset:52224
	ds_read_b128 v[200:203], v147 offset:53248
	ds_read_b128 v[204:207], v147 offset:54272
	ds_read_b128 v[216:219], v147 offset:55296
	ds_read_b128 v[220:223], v147 offset:56320
	global_load_lds_dwordx4 v[164:165], off
	s_add_i32 m0, s46, 0x2000
	s_add_u32 s44, s44, 0x100080
	v_lshl_add_u64 v[164:165], v[208:209], 0, s[56:57]
	s_addc_u32 s45, s45, 0
	s_add_i32 s46, s64, s71
	global_load_lds_dwordx4 v[164:165], off
	s_mov_b32 m0, s46
	v_lshl_add_u64 v[164:165], s[44:45], 0, v[126:127]
	global_load_lds_dwordx4 v[164:165], off
	s_add_i32 m0, s46, 0x2000
	v_lshl_add_u64 v[164:165], s[44:45], 0, v[118:119]
	global_load_lds_dwordx4 v[164:165], off
	s_mov_b32 m0, s78
	v_lshl_add_u64 v[164:165], v[224:225], 0, s[56:57]
	global_load_lds_dwordx4 v[164:165], off
	s_mov_b32 m0, s79
	v_lshl_add_u64 v[164:165], v[242:243], 0, s[56:57]
	global_load_lds_dwordx4 v[164:165], off
	s_waitcnt vmcnt(8) lgkmcnt(0)
	s_barrier
	s_setprio 1
	v_mfma_f32_16x16x32_bf16 v[62:65], v[148:151], v[184:187], v[62:65]
	v_mfma_f32_16x16x32_bf16 v[58:61], v[156:159], v[184:187], v[58:61]
	v_mfma_f32_16x16x32_bf16 v[46:49], v[148:151], v[192:195], v[46:49]
	v_mfma_f32_16x16x32_bf16 v[42:45], v[156:159], v[192:195], v[42:45]
	v_mfma_f32_16x16x32_bf16 v[30:33], v[148:151], v[200:203], v[30:33]
	v_mfma_f32_16x16x32_bf16 v[26:29], v[156:159], v[200:203], v[26:29]
	v_mfma_f32_16x16x32_bf16 v[14:17], v[148:151], v[216:219], v[14:17]
	v_mfma_f32_16x16x32_bf16 v[10:13], v[156:159], v[216:219], v[10:13]
	v_mfma_f32_16x16x32_bf16 v[62:65], v[152:155], v[188:191], v[62:65]
	v_mfma_f32_16x16x32_bf16 v[58:61], v[160:163], v[188:191], v[58:61]
	v_mfma_f32_16x16x32_bf16 v[46:49], v[152:155], v[196:199], v[46:49]
	v_mfma_f32_16x16x32_bf16 v[42:45], v[160:163], v[196:199], v[42:45]
	v_mfma_f32_16x16x32_bf16 v[30:33], v[152:155], v[204:207], v[30:33]
	v_mfma_f32_16x16x32_bf16 v[26:29], v[160:163], v[204:207], v[26:29]
	v_mfma_f32_16x16x32_bf16 v[14:17], v[152:155], v[220:223], v[14:17]
	v_mfma_f32_16x16x32_bf16 v[10:13], v[160:163], v[220:223], v[10:13]
	s_setprio 0
	s_setprio 1
	v_mfma_f32_16x16x32_bf16 v[54:57], v[168:171], v[184:187], v[54:57]
	v_mfma_f32_16x16x32_bf16 v[50:53], v[176:179], v[184:187], v[50:53]
	v_mfma_f32_16x16x32_bf16 v[38:41], v[168:171], v[192:195], v[38:41]
	v_mfma_f32_16x16x32_bf16 v[34:37], v[176:179], v[192:195], v[34:37]
	v_mfma_f32_16x16x32_bf16 v[22:25], v[168:171], v[200:203], v[22:25]
	v_mfma_f32_16x16x32_bf16 v[18:21], v[176:179], v[200:203], v[18:21]
	v_mfma_f32_16x16x32_bf16 v[6:9], v[168:171], v[216:219], v[6:9]
	v_mfma_f32_16x16x32_bf16 v[2:5], v[176:179], v[216:219], v[2:5]
	v_mfma_f32_16x16x32_bf16 v[54:57], v[172:175], v[188:191], v[54:57]
	v_mfma_f32_16x16x32_bf16 v[50:53], v[180:183], v[188:191], v[50:53]
	v_mfma_f32_16x16x32_bf16 v[38:41], v[172:175], v[196:199], v[38:41]
	v_mfma_f32_16x16x32_bf16 v[34:37], v[180:183], v[196:199], v[34:37]
	v_mfma_f32_16x16x32_bf16 v[22:25], v[172:175], v[204:207], v[22:25]
	v_mfma_f32_16x16x32_bf16 v[18:21], v[180:183], v[204:207], v[18:21]
	v_mfma_f32_16x16x32_bf16 v[6:9], v[172:175], v[220:223], v[6:9]
	v_mfma_f32_16x16x32_bf16 v[2:5], v[180:183], v[220:223], v[2:5]
	s_setprio 0
	s_barrier
	s_add_i32 s84, s84, 2
	s_add_u32 s36, s36, 0x100
	s_addc_u32 s37, s37, 0
	s_cmp_gt_u32 s84, 61
	s_cbranch_scc0 .LBB0_2796
	s_add_u32 s36, s59, 0xffffff00
	s_addc_u32 s37, s81, -1
	s_andn2_b64 vcc, exec, s[42:43]
	s_cbranch_vccnz .LBB0_2799
	v_mov_b32_e32 v2, 0
	s_mov_b32 s12, s26
	s_mov_b32 s80, s28
	s_mov_b64 s[24:25], s[34:35]
	s_mov_b32 s68, s58
	v_mov_b32_e32 v3, v2
	v_mov_b32_e32 v4, v2
	v_mov_b32_e32 v5, v2
	v_mov_b32_e32 v6, v2
	v_mov_b32_e32 v7, v2
	v_mov_b32_e32 v8, v2
	v_mov_b32_e32 v9, v2
	v_mov_b32_e32 v18, v2
	v_mov_b32_e32 v19, v2
	v_mov_b32_e32 v20, v2
	v_mov_b32_e32 v21, v2
	v_mov_b32_e32 v22, v2
	v_mov_b32_e32 v23, v2
	v_mov_b32_e32 v24, v2
	v_mov_b32_e32 v25, v2
	v_mov_b32_e32 v34, v2
	v_mov_b32_e32 v35, v2
	v_mov_b32_e32 v36, v2
	v_mov_b32_e32 v37, v2
	v_mov_b32_e32 v38, v2
	v_mov_b32_e32 v39, v2
	v_mov_b32_e32 v40, v2
	v_mov_b32_e32 v41, v2
	v_mov_b32_e32 v50, v2
	v_mov_b32_e32 v51, v2
	v_mov_b32_e32 v52, v2
	v_mov_b32_e32 v53, v2
	v_mov_b32_e32 v54, v2
	v_mov_b32_e32 v55, v2
	v_mov_b32_e32 v56, v2
	v_mov_b32_e32 v57, v2
	v_mov_b32_e32 v10, v2
	v_mov_b32_e32 v11, v2
	v_mov_b32_e32 v12, v2
	v_mov_b32_e32 v13, v2
	v_mov_b32_e32 v14, v2
	v_mov_b32_e32 v15, v2
	v_mov_b32_e32 v16, v2
	v_mov_b32_e32 v17, v2
	v_mov_b32_e32 v26, v2
	v_mov_b32_e32 v27, v2
	v_mov_b32_e32 v28, v2
	v_mov_b32_e32 v29, v2
	v_mov_b32_e32 v30, v2
	v_mov_b32_e32 v31, v2
	v_mov_b32_e32 v32, v2
	v_mov_b32_e32 v33, v2
	v_mov_b32_e32 v42, v2
	v_mov_b32_e32 v43, v2
	v_mov_b32_e32 v44, v2
	v_mov_b32_e32 v45, v2
	v_mov_b32_e32 v46, v2
	v_mov_b32_e32 v47, v2
	v_mov_b32_e32 v48, v2
	v_mov_b32_e32 v49, v2
	v_mov_b32_e32 v58, v2
	v_mov_b32_e32 v59, v2
	v_mov_b32_e32 v60, v2
	v_mov_b32_e32 v61, v2
	v_mov_b32_e32 v62, v2
	v_mov_b32_e32 v63, v2
	v_mov_b32_e32 v64, v2
	v_mov_b32_e32 v65, v2
	v_mov_b32_e32 v66, v2
	v_mov_b32_e32 v67, v2
	v_mov_b32_e32 v68, v2
	v_mov_b32_e32 v69, v2
	v_mov_b32_e32 v70, v2
	v_mov_b32_e32 v71, v2
	v_mov_b32_e32 v72, v2
	v_mov_b32_e32 v73, v2
	v_mov_b32_e32 v82, v2
	v_mov_b32_e32 v83, v2
	v_mov_b32_e32 v84, v2
	v_mov_b32_e32 v85, v2
	v_mov_b32_e32 v86, v2
	v_mov_b32_e32 v87, v2
	v_mov_b32_e32 v88, v2
	v_mov_b32_e32 v89, v2
	v_mov_b32_e32 v98, v2
	v_mov_b32_e32 v99, v2
	v_mov_b32_e32 v100, v2
	v_mov_b32_e32 v101, v2
	v_mov_b32_e32 v102, v2
	v_mov_b32_e32 v103, v2
	v_mov_b32_e32 v104, v2
	v_mov_b32_e32 v105, v2
	v_mov_b32_e32 v114, v2
	v_mov_b32_e32 v115, v2
	v_mov_b32_e32 v116, v2
	v_mov_b32_e32 v117, v2
	v_mov_b32_e32 v122, v2
	v_mov_b32_e32 v123, v2
	v_mov_b32_e32 v124, v2
	v_mov_b32_e32 v125, v2
	v_mov_b32_e32 v74, v2
	v_mov_b32_e32 v75, v2
	v_mov_b32_e32 v76, v2
	v_mov_b32_e32 v77, v2
	v_mov_b32_e32 v78, v2
	v_mov_b32_e32 v79, v2
	v_mov_b32_e32 v80, v2
	v_mov_b32_e32 v81, v2
	v_mov_b32_e32 v90, v2
	v_mov_b32_e32 v91, v2
	v_mov_b32_e32 v92, v2
	v_mov_b32_e32 v93, v2
	v_mov_b32_e32 v94, v2
	v_mov_b32_e32 v95, v2
	v_mov_b32_e32 v96, v2
	v_mov_b32_e32 v97, v2
	v_mov_b32_e32 v106, v2
	v_mov_b32_e32 v107, v2
	v_mov_b32_e32 v108, v2
	v_mov_b32_e32 v109, v2
	v_mov_b32_e32 v110, v2
	v_mov_b32_e32 v111, v2
	v_mov_b32_e32 v112, v2
	v_mov_b32_e32 v113, v2
	v_mov_b32_e32 v130, v2
	v_mov_b32_e32 v131, v2
	v_mov_b32_e32 v132, v2
	v_mov_b32_e32 v133, v2
	v_mov_b32_e32 v134, v2
	v_mov_b32_e32 v135, v2
	v_mov_b32_e32 v136, v2
	v_mov_b32_e32 v137, v2
	s_movk_i32 s92, 0x2b20
	s_andn2_b64 vcc, exec, s[40:41]
	s_cbranch_vccnz .LBB0_2800
	s_branch .LBB0_2801

.LBB0_2891:
	s_add_u32 s44, s24, s36
	s_addc_u32 s45, s25, s37
	s_add_u32 s44, s44, 0x100
	s_addc_u32 s45, s45, 0
	s_add_u32 s50, s59, s36
	s_addc_u32 s64, s81, s37
	s_add_i32 s65, 0, 0x10000
	s_cmpk_eq_i32 s36, 0x1f00
	s_cselect_b32 s47, s29, s45
	s_cselect_b32 s46, s82, s44
	s_cselect_b32 s45, s27, s64
	s_cselect_b32 s44, s83, s50
	s_add_i32 s50, 0, 0x14000
	v_add_u32_e32 v160, s65, v146
	v_add_u32_e32 v164, s50, v146
	ds_read_b128 v[148:151], v160
	ds_read_b128 v[152:155], v160 offset:1024
	ds_read_b128 v[156:159], v160 offset:2048
	ds_read_b128 v[160:163], v160 offset:3072
	ds_read_b128 v[168:171], v164
	ds_read_b128 v[172:175], v164 offset:1024
	ds_read_b128 v[176:179], v164 offset:2048
	ds_read_b128 v[180:183], v164 offset:3072
	v_lshl_add_u64 v[164:165], v[144:145], 0, s[36:37]
	s_add_i32 m0, s4, 0xc000
	ds_read_b128 v[184:187], v147
	ds_read_b128 v[188:191], v147 offset:1024
	ds_read_b128 v[192:195], v147 offset:2048
	ds_read_b128 v[196:199], v147 offset:3072
	ds_read_b128 v[200:203], v147 offset:4096
	ds_read_b128 v[204:207], v147 offset:5120
	ds_read_b128 v[216:219], v147 offset:6144
	ds_read_b128 v[220:223], v147 offset:7168
	global_load_lds_dwordx4 v[164:165], off
	s_add_i32 m0, s4, 0xe000
	v_lshl_add_u64 v[164:165], v[142:143], 0, s[36:37]
	global_load_lds_dwordx4 v[164:165], off
	s_waitcnt vmcnt(8) lgkmcnt(0)
	s_barrier
	s_setprio 1
	v_mfma_f32_16x16x32_bf16 v[134:137], v[148:151], v[184:187], v[134:137]
	v_mfma_f32_16x16x32_bf16 v[130:133], v[156:159], v[184:187], v[130:133]
	v_mfma_f32_16x16x32_bf16 v[110:113], v[148:151], v[192:195], v[110:113]
	v_mfma_f32_16x16x32_bf16 v[106:109], v[156:159], v[192:195], v[106:109]
	v_mfma_f32_16x16x32_bf16 v[94:97], v[148:151], v[200:203], v[94:97]
	v_mfma_f32_16x16x32_bf16 v[90:93], v[156:159], v[200:203], v[90:93]
	v_mfma_f32_16x16x32_bf16 v[78:81], v[148:151], v[216:219], v[78:81]
	v_mfma_f32_16x16x32_bf16 v[74:77], v[156:159], v[216:219], v[74:77]
	v_mfma_f32_16x16x32_bf16 v[134:137], v[152:155], v[188:191], v[134:137]
	v_mfma_f32_16x16x32_bf16 v[130:133], v[160:163], v[188:191], v[130:133]
	v_mfma_f32_16x16x32_bf16 v[110:113], v[152:155], v[196:199], v[110:113]
	v_mfma_f32_16x16x32_bf16 v[106:109], v[160:163], v[196:199], v[106:109]
	v_mfma_f32_16x16x32_bf16 v[94:97], v[152:155], v[204:207], v[94:97]
	v_mfma_f32_16x16x32_bf16 v[90:93], v[160:163], v[204:207], v[90:93]
	v_mfma_f32_16x16x32_bf16 v[78:81], v[152:155], v[220:223], v[78:81]
	v_mfma_f32_16x16x32_bf16 v[74:77], v[160:163], v[220:223], v[74:77]
	s_setprio 0
	s_setprio 1
	v_mfma_f32_16x16x32_bf16 v[118:121], v[168:171], v[184:187], v[118:121]
	v_mfma_f32_16x16x32_bf16 v[114:117], v[176:179], v[184:187], v[114:117]
	v_mfma_f32_16x16x32_bf16 v[102:105], v[168:171], v[192:195], v[102:105]
	v_mfma_f32_16x16x32_bf16 v[98:101], v[176:179], v[192:195], v[98:101]
	v_mfma_f32_16x16x32_bf16 v[86:89], v[168:171], v[200:203], v[86:89]
	v_mfma_f32_16x16x32_bf16 v[82:85], v[176:179], v[200:203], v[82:85]
	v_mfma_f32_16x16x32_bf16 v[70:73], v[168:171], v[216:219], v[70:73]
	v_mfma_f32_16x16x32_bf16 v[66:69], v[176:179], v[216:219], v[66:69]
	v_mfma_f32_16x16x32_bf16 v[118:121], v[172:175], v[188:191], v[118:121]
	v_mfma_f32_16x16x32_bf16 v[114:117], v[180:183], v[188:191], v[114:117]
	v_mfma_f32_16x16x32_bf16 v[102:105], v[172:175], v[196:199], v[102:105]
	v_mfma_f32_16x16x32_bf16 v[98:101], v[180:183], v[196:199], v[98:101]
	v_mfma_f32_16x16x32_bf16 v[86:89], v[172:175], v[204:207], v[86:89]
	v_mfma_f32_16x16x32_bf16 v[82:85], v[180:183], v[204:207], v[82:85]
	v_mfma_f32_16x16x32_bf16 v[70:73], v[172:175], v[220:223], v[70:73]
	v_mfma_f32_16x16x32_bf16 v[66:69], v[180:183], v[220:223], v[66:69]
	s_setprio 0
	s_barrier
	s_add_i32 s64, s65, s76
	v_lshl_add_u64 v[164:165], s[44:45], 0, v[126:127]
	s_mov_b32 m0, s64
	ds_read_b128 v[184:187], v147 offset:16384
	ds_read_b128 v[188:191], v147 offset:17408
	ds_read_b128 v[192:195], v147 offset:18432
	ds_read_b128 v[196:199], v147 offset:19456
	ds_read_b128 v[200:203], v147 offset:20480
	ds_read_b128 v[204:207], v147 offset:21504
	ds_read_b128 v[216:219], v147 offset:22528
	ds_read_b128 v[220:223], v147 offset:23552
	global_load_lds_dwordx4 v[164:165], off
	s_add_i32 m0, s64, 0x2000
	s_add_u32 s92, s44, 0x100000
	v_lshl_add_u64 v[208:209], s[44:45], 0, v[122:123]
	s_addc_u32 s93, s45, 0
	s_add_i32 s50, s50, s76
	global_load_lds_dwordx4 v[208:209], off
	v_lshl_add_u64 v[240:241], s[92:93], 0, v[126:127]
	s_mov_b32 m0, s50
	v_lshl_add_u64 v[242:243], s[46:47], 0, v[124:125]
	global_load_lds_dwordx4 v[240:241], off
	s_add_i32 m0, s50, 0x2000
	v_lshl_add_u64 v[240:241], s[92:93], 0, v[122:123]
	global_load_lds_dwordx4 v[240:241], off
	s_mov_b32 m0, s4
	v_lshl_add_u64 v[240:241], s[46:47], 0, v[128:129]
	global_load_lds_dwordx4 v[240:241], off
	s_mov_b32 m0, s33
	s_nop 0
	global_load_lds_dwordx4 v[242:243], off
	s_waitcnt vmcnt(8) lgkmcnt(0)
	s_barrier
	s_setprio 1
	v_mfma_f32_16x16x32_bf16 v[62:65], v[148:151], v[184:187], v[62:65]
	v_mfma_f32_16x16x32_bf16 v[58:61], v[156:159], v[184:187], v[58:61]
	v_mfma_f32_16x16x32_bf16 v[46:49], v[148:151], v[192:195], v[46:49]
	v_mfma_f32_16x16x32_bf16 v[42:45], v[156:159], v[192:195], v[42:45]
	v_mfma_f32_16x16x32_bf16 v[30:33], v[148:151], v[200:203], v[30:33]
	v_mfma_f32_16x16x32_bf16 v[26:29], v[156:159], v[200:203], v[26:29]
	v_mfma_f32_16x16x32_bf16 v[14:17], v[148:151], v[216:219], v[14:17]
	v_mfma_f32_16x16x32_bf16 v[10:13], v[156:159], v[216:219], v[10:13]
	v_mfma_f32_16x16x32_bf16 v[62:65], v[152:155], v[188:191], v[62:65]
	v_mfma_f32_16x16x32_bf16 v[58:61], v[160:163], v[188:191], v[58:61]
	v_mfma_f32_16x16x32_bf16 v[46:49], v[152:155], v[196:199], v[46:49]
	v_mfma_f32_16x16x32_bf16 v[42:45], v[160:163], v[196:199], v[42:45]
	v_mfma_f32_16x16x32_bf16 v[30:33], v[152:155], v[204:207], v[30:33]
	v_mfma_f32_16x16x32_bf16 v[26:29], v[160:163], v[204:207], v[26:29]
	v_mfma_f32_16x16x32_bf16 v[14:17], v[152:155], v[220:223], v[14:17]
	v_mfma_f32_16x16x32_bf16 v[10:13], v[160:163], v[220:223], v[10:13]
	s_setprio 0
	s_setprio 1
	v_mfma_f32_16x16x32_bf16 v[54:57], v[168:171], v[184:187], v[54:57]
	v_mfma_f32_16x16x32_bf16 v[50:53], v[176:179], v[184:187], v[50:53]
	v_mfma_f32_16x16x32_bf16 v[38:41], v[168:171], v[192:195], v[38:41]
	v_mfma_f32_16x16x32_bf16 v[34:37], v[176:179], v[192:195], v[34:37]
	v_mfma_f32_16x16x32_bf16 v[22:25], v[168:171], v[200:203], v[22:25]
	v_mfma_f32_16x16x32_bf16 v[18:21], v[176:179], v[200:203], v[18:21]
	v_mfma_f32_16x16x32_bf16 v[6:9], v[168:171], v[216:219], v[6:9]
	v_mfma_f32_16x16x32_bf16 v[2:5], v[176:179], v[216:219], v[2:5]
	v_mfma_f32_16x16x32_bf16 v[54:57], v[172:175], v[188:191], v[54:57]
	v_mfma_f32_16x16x32_bf16 v[50:53], v[180:183], v[188:191], v[50:53]
	v_mfma_f32_16x16x32_bf16 v[38:41], v[172:175], v[196:199], v[38:41]
	v_mfma_f32_16x16x32_bf16 v[34:37], v[180:183], v[196:199], v[34:37]
	v_mfma_f32_16x16x32_bf16 v[22:25], v[172:175], v[204:207], v[22:25]
	v_mfma_f32_16x16x32_bf16 v[18:21], v[180:183], v[204:207], v[18:21]
	v_mfma_f32_16x16x32_bf16 v[6:9], v[172:175], v[220:223], v[6:9]
	v_mfma_f32_16x16x32_bf16 v[2:5], v[180:183], v[220:223], v[2:5]
	s_setprio 0
	s_barrier
	s_add_i32 s50, 0, 0x18000
	s_add_i32 s64, 0, 0x1c000
	v_add_u32_e32 v160, s50, v146
	v_add_u32_e32 v167, s64, v146
	ds_read_b128 v[148:151], v160
	ds_read_b128 v[152:155], v160 offset:1024
	ds_read_b128 v[156:159], v160 offset:2048
	ds_read_b128 v[160:163], v160 offset:3072
	ds_read_b128 v[168:171], v167
	ds_read_b128 v[172:175], v167 offset:1024
	ds_read_b128 v[176:179], v167 offset:2048
	ds_read_b128 v[180:183], v167 offset:3072
	s_add_u32 s46, s46, 0x100000
	s_addc_u32 s47, s47, 0
	s_mov_b32 m0, s77
	v_lshl_add_u64 v[244:245], s[46:47], 0, v[128:129]
	ds_read_b128 v[184:187], v147 offset:32768
	ds_read_b128 v[188:191], v147 offset:33792
	ds_read_b128 v[192:195], v147 offset:34816
	ds_read_b128 v[196:199], v147 offset:35840
	ds_read_b128 v[200:203], v147 offset:36864
	ds_read_b128 v[204:207], v147 offset:37888
	ds_read_b128 v[216:219], v147 offset:38912
	ds_read_b128 v[220:223], v147 offset:39936
	global_load_lds_dwordx4 v[244:245], off
	s_mov_b32 m0, s78
	v_lshl_add_u64 v[244:245], s[46:47], 0, v[124:125]
	global_load_lds_dwordx4 v[244:245], off
	s_waitcnt vmcnt(8) lgkmcnt(0)
	s_barrier
	s_setprio 1
	v_mfma_f32_16x16x32_bf16 v[134:137], v[148:151], v[184:187], v[134:137]
	v_mfma_f32_16x16x32_bf16 v[130:133], v[156:159], v[184:187], v[130:133]
	v_mfma_f32_16x16x32_bf16 v[110:113], v[148:151], v[192:195], v[110:113]
	v_mfma_f32_16x16x32_bf16 v[106:109], v[156:159], v[192:195], v[106:109]
	v_mfma_f32_16x16x32_bf16 v[94:97], v[148:151], v[200:203], v[94:97]
	v_mfma_f32_16x16x32_bf16 v[90:93], v[156:159], v[200:203], v[90:93]
	v_mfma_f32_16x16x32_bf16 v[78:81], v[148:151], v[216:219], v[78:81]
	v_mfma_f32_16x16x32_bf16 v[74:77], v[156:159], v[216:219], v[74:77]
	v_mfma_f32_16x16x32_bf16 v[134:137], v[152:155], v[188:191], v[134:137]
	v_mfma_f32_16x16x32_bf16 v[130:133], v[160:163], v[188:191], v[130:133]
	v_mfma_f32_16x16x32_bf16 v[110:113], v[152:155], v[196:199], v[110:113]
	v_mfma_f32_16x16x32_bf16 v[106:109], v[160:163], v[196:199], v[106:109]
	v_mfma_f32_16x16x32_bf16 v[94:97], v[152:155], v[204:207], v[94:97]
	v_mfma_f32_16x16x32_bf16 v[90:93], v[160:163], v[204:207], v[90:93]
	v_mfma_f32_16x16x32_bf16 v[78:81], v[152:155], v[220:223], v[78:81]
	v_mfma_f32_16x16x32_bf16 v[74:77], v[160:163], v[220:223], v[74:77]
	s_setprio 0
	s_setprio 1
	v_mfma_f32_16x16x32_bf16 v[118:121], v[168:171], v[184:187], v[118:121]
	v_mfma_f32_16x16x32_bf16 v[114:117], v[176:179], v[184:187], v[114:117]
	v_mfma_f32_16x16x32_bf16 v[102:105], v[168:171], v[192:195], v[102:105]
	v_mfma_f32_16x16x32_bf16 v[98:101], v[176:179], v[192:195], v[98:101]
	v_mfma_f32_16x16x32_bf16 v[86:89], v[168:171], v[200:203], v[86:89]
	v_mfma_f32_16x16x32_bf16 v[82:85], v[176:179], v[200:203], v[82:85]
	v_mfma_f32_16x16x32_bf16 v[70:73], v[168:171], v[216:219], v[70:73]
	v_mfma_f32_16x16x32_bf16 v[66:69], v[176:179], v[216:219], v[66:69]
	v_mfma_f32_16x16x32_bf16 v[118:121], v[172:175], v[188:191], v[118:121]
	v_mfma_f32_16x16x32_bf16 v[114:117], v[180:183], v[188:191], v[114:117]
	v_mfma_f32_16x16x32_bf16 v[102:105], v[172:175], v[196:199], v[102:105]
	v_mfma_f32_16x16x32_bf16 v[98:101], v[180:183], v[196:199], v[98:101]
	v_mfma_f32_16x16x32_bf16 v[86:89], v[172:175], v[204:207], v[86:89]
	v_mfma_f32_16x16x32_bf16 v[82:85], v[180:183], v[204:207], v[82:85]
	v_mfma_f32_16x16x32_bf16 v[70:73], v[172:175], v[220:223], v[70:73]
	v_mfma_f32_16x16x32_bf16 v[66:69], v[180:183], v[220:223], v[66:69]
	s_setprio 0
	s_barrier
	s_add_i32 s46, s50, s76
	v_lshl_add_u64 v[164:165], v[164:165], 0, s[56:57]
	s_mov_b32 m0, s46
	ds_read_b128 v[184:187], v147 offset:49152
	ds_read_b128 v[188:191], v147 offset:50176
	ds_read_b128 v[192:195], v147 offset:51200
	ds_read_b128 v[196:199], v147 offset:52224
	ds_read_b128 v[200:203], v147 offset:53248
	ds_read_b128 v[204:207], v147 offset:54272
	ds_read_b128 v[216:219], v147 offset:55296
	ds_read_b128 v[220:223], v147 offset:56320
	global_load_lds_dwordx4 v[164:165], off
	s_add_i32 m0, s46, 0x2000
	s_add_u32 s44, s44, 0x100080
	v_lshl_add_u64 v[164:165], v[208:209], 0, s[56:57]
	s_addc_u32 s45, s45, 0
	s_add_i32 s46, s64, s76
	global_load_lds_dwordx4 v[164:165], off
	s_mov_b32 m0, s46
	v_lshl_add_u64 v[164:165], s[44:45], 0, v[126:127]
	global_load_lds_dwordx4 v[164:165], off
	s_add_i32 m0, s46, 0x2000
	v_lshl_add_u64 v[164:165], s[44:45], 0, v[122:123]
	global_load_lds_dwordx4 v[164:165], off
	s_mov_b32 m0, s79
	v_lshl_add_u64 v[164:165], v[240:241], 0, s[56:57]
	global_load_lds_dwordx4 v[164:165], off
	s_mov_b32 m0, s80
	v_lshl_add_u64 v[164:165], v[242:243], 0, s[56:57]
	global_load_lds_dwordx4 v[164:165], off
	s_waitcnt vmcnt(8) lgkmcnt(0)
	s_barrier
	s_setprio 1
	v_mfma_f32_16x16x32_bf16 v[62:65], v[148:151], v[184:187], v[62:65]
	v_mfma_f32_16x16x32_bf16 v[58:61], v[156:159], v[184:187], v[58:61]
	v_mfma_f32_16x16x32_bf16 v[46:49], v[148:151], v[192:195], v[46:49]
	v_mfma_f32_16x16x32_bf16 v[42:45], v[156:159], v[192:195], v[42:45]
	v_mfma_f32_16x16x32_bf16 v[30:33], v[148:151], v[200:203], v[30:33]
	v_mfma_f32_16x16x32_bf16 v[26:29], v[156:159], v[200:203], v[26:29]
	v_mfma_f32_16x16x32_bf16 v[14:17], v[148:151], v[216:219], v[14:17]
	v_mfma_f32_16x16x32_bf16 v[10:13], v[156:159], v[216:219], v[10:13]
	v_mfma_f32_16x16x32_bf16 v[62:65], v[152:155], v[188:191], v[62:65]
	v_mfma_f32_16x16x32_bf16 v[58:61], v[160:163], v[188:191], v[58:61]
	v_mfma_f32_16x16x32_bf16 v[46:49], v[152:155], v[196:199], v[46:49]
	v_mfma_f32_16x16x32_bf16 v[42:45], v[160:163], v[196:199], v[42:45]
	v_mfma_f32_16x16x32_bf16 v[30:33], v[152:155], v[204:207], v[30:33]
	v_mfma_f32_16x16x32_bf16 v[26:29], v[160:163], v[204:207], v[26:29]
	v_mfma_f32_16x16x32_bf16 v[14:17], v[152:155], v[220:223], v[14:17]
	v_mfma_f32_16x16x32_bf16 v[10:13], v[160:163], v[220:223], v[10:13]
	s_setprio 0
	s_setprio 1
	v_mfma_f32_16x16x32_bf16 v[54:57], v[168:171], v[184:187], v[54:57]
	v_mfma_f32_16x16x32_bf16 v[50:53], v[176:179], v[184:187], v[50:53]
	v_mfma_f32_16x16x32_bf16 v[38:41], v[168:171], v[192:195], v[38:41]
	v_mfma_f32_16x16x32_bf16 v[34:37], v[176:179], v[192:195], v[34:37]
	v_mfma_f32_16x16x32_bf16 v[22:25], v[168:171], v[200:203], v[22:25]
	v_mfma_f32_16x16x32_bf16 v[18:21], v[176:179], v[200:203], v[18:21]
	v_mfma_f32_16x16x32_bf16 v[6:9], v[168:171], v[216:219], v[6:9]
	v_mfma_f32_16x16x32_bf16 v[2:5], v[176:179], v[216:219], v[2:5]
	v_mfma_f32_16x16x32_bf16 v[54:57], v[172:175], v[188:191], v[54:57]
	v_mfma_f32_16x16x32_bf16 v[50:53], v[180:183], v[188:191], v[50:53]
	v_mfma_f32_16x16x32_bf16 v[38:41], v[172:175], v[196:199], v[38:41]
	v_mfma_f32_16x16x32_bf16 v[34:37], v[180:183], v[196:199], v[34:37]
	v_mfma_f32_16x16x32_bf16 v[22:25], v[172:175], v[204:207], v[22:25]
	v_mfma_f32_16x16x32_bf16 v[18:21], v[180:183], v[204:207], v[18:21]
	v_mfma_f32_16x16x32_bf16 v[6:9], v[172:175], v[220:223], v[6:9]
	v_mfma_f32_16x16x32_bf16 v[2:5], v[180:183], v[220:223], v[2:5]
	s_setprio 0
	s_barrier
	s_add_i32 s84, s84, 2
	s_add_u32 s36, s36, 0x100
	s_addc_u32 s37, s37, 0
	s_cmp_gt_u32 s84, 61
	s_cbranch_scc0 .LBB0_2891
	s_add_u32 s36, s59, 0xffffff00
	s_addc_u32 s37, s81, -1
	s_andn2_b64 vcc, exec, s[42:43]
	s_cbranch_vccnz .LBB0_2894
	v_mov_b32_e32 v2, 0
	s_mov_b32 s20, s26
	s_mov_b32 s52, s28
	s_mov_b64 s[24:25], s[34:35]
	s_mov_b32 s68, s58
	v_mov_b32_e32 v3, v2
	v_mov_b32_e32 v4, v2
	v_mov_b32_e32 v5, v2
	v_mov_b32_e32 v6, v2
	v_mov_b32_e32 v7, v2
	v_mov_b32_e32 v8, v2
	v_mov_b32_e32 v9, v2
	v_mov_b32_e32 v18, v2
	v_mov_b32_e32 v19, v2
	v_mov_b32_e32 v20, v2
	v_mov_b32_e32 v21, v2
	v_mov_b32_e32 v22, v2
	v_mov_b32_e32 v23, v2
	v_mov_b32_e32 v24, v2
	v_mov_b32_e32 v25, v2
	v_mov_b32_e32 v34, v2
	v_mov_b32_e32 v35, v2
	v_mov_b32_e32 v36, v2
	v_mov_b32_e32 v37, v2
	v_mov_b32_e32 v38, v2
	v_mov_b32_e32 v39, v2
	v_mov_b32_e32 v40, v2
	v_mov_b32_e32 v41, v2
	v_mov_b32_e32 v50, v2
	v_mov_b32_e32 v51, v2
	v_mov_b32_e32 v52, v2
	v_mov_b32_e32 v53, v2
	v_mov_b32_e32 v54, v2
	v_mov_b32_e32 v55, v2
	v_mov_b32_e32 v56, v2
	v_mov_b32_e32 v57, v2
	v_mov_b32_e32 v10, v2
	v_mov_b32_e32 v11, v2
	v_mov_b32_e32 v12, v2
	v_mov_b32_e32 v13, v2
	v_mov_b32_e32 v14, v2
	v_mov_b32_e32 v15, v2
	v_mov_b32_e32 v16, v2
	v_mov_b32_e32 v17, v2
	v_mov_b32_e32 v26, v2
	v_mov_b32_e32 v27, v2
	v_mov_b32_e32 v28, v2
	v_mov_b32_e32 v29, v2
	v_mov_b32_e32 v30, v2
	v_mov_b32_e32 v31, v2
	v_mov_b32_e32 v32, v2
	v_mov_b32_e32 v33, v2
	v_mov_b32_e32 v42, v2
	v_mov_b32_e32 v43, v2
	v_mov_b32_e32 v44, v2
	v_mov_b32_e32 v45, v2
	v_mov_b32_e32 v46, v2
	v_mov_b32_e32 v47, v2
	v_mov_b32_e32 v48, v2
	v_mov_b32_e32 v49, v2
	v_mov_b32_e32 v58, v2
	v_mov_b32_e32 v59, v2
	v_mov_b32_e32 v60, v2
	v_mov_b32_e32 v61, v2
	v_mov_b32_e32 v62, v2
	v_mov_b32_e32 v63, v2
	v_mov_b32_e32 v64, v2
	v_mov_b32_e32 v65, v2
	v_mov_b32_e32 v66, v2
	v_mov_b32_e32 v67, v2
	v_mov_b32_e32 v68, v2
	v_mov_b32_e32 v69, v2
	v_mov_b32_e32 v70, v2
	v_mov_b32_e32 v71, v2
	v_mov_b32_e32 v72, v2
	v_mov_b32_e32 v73, v2
	v_mov_b32_e32 v82, v2
	v_mov_b32_e32 v83, v2
	v_mov_b32_e32 v84, v2
	v_mov_b32_e32 v85, v2
	v_mov_b32_e32 v86, v2
	v_mov_b32_e32 v87, v2
	v_mov_b32_e32 v88, v2
	v_mov_b32_e32 v89, v2
	v_mov_b32_e32 v98, v2
	v_mov_b32_e32 v99, v2
	v_mov_b32_e32 v100, v2
	v_mov_b32_e32 v101, v2
	v_mov_b32_e32 v102, v2
	v_mov_b32_e32 v103, v2
	v_mov_b32_e32 v104, v2
	v_mov_b32_e32 v105, v2
	v_mov_b32_e32 v114, v2
	v_mov_b32_e32 v115, v2
	v_mov_b32_e32 v116, v2
	v_mov_b32_e32 v117, v2
	v_mov_b32_e32 v118, v2
	v_mov_b32_e32 v119, v2
	v_mov_b32_e32 v120, v2
	v_mov_b32_e32 v121, v2
	v_mov_b32_e32 v74, v2
	v_mov_b32_e32 v75, v2
	v_mov_b32_e32 v76, v2
	v_mov_b32_e32 v77, v2
	v_mov_b32_e32 v78, v2
	v_mov_b32_e32 v79, v2
	v_mov_b32_e32 v80, v2
	v_mov_b32_e32 v81, v2
	v_mov_b32_e32 v90, v2
	v_mov_b32_e32 v91, v2
	v_mov_b32_e32 v92, v2
	v_mov_b32_e32 v93, v2
	v_mov_b32_e32 v94, v2
	v_mov_b32_e32 v95, v2
	v_mov_b32_e32 v96, v2
	v_mov_b32_e32 v97, v2
	v_mov_b32_e32 v106, v2
	v_mov_b32_e32 v107, v2
	v_mov_b32_e32 v108, v2
	v_mov_b32_e32 v109, v2
	v_mov_b32_e32 v110, v2
	v_mov_b32_e32 v111, v2
	v_mov_b32_e32 v112, v2
	v_mov_b32_e32 v113, v2
	v_mov_b32_e32 v130, v2
	v_mov_b32_e32 v131, v2
	v_mov_b32_e32 v132, v2
	v_mov_b32_e32 v133, v2
	v_mov_b32_e32 v134, v2
	v_mov_b32_e32 v135, v2
	v_mov_b32_e32 v136, v2
	v_mov_b32_e32 v137, v2
	s_movk_i32 s92, 0x2b20
	s_andn2_b64 vcc, exec, s[40:41]
	s_cbranch_vccnz .LBB0_2895
	s_branch .LBB0_2896

.LBB0_2982:
	s_add_u32 s42, s24, s36
	s_addc_u32 s43, s25, s37
	s_add_u32 s42, s42, 0x100
	s_addc_u32 s43, s43, 0
	s_add_u32 s50, s59, s36
	s_addc_u32 s64, s79, s37
	s_add_i32 s65, 0, 0x10000
	s_cmpk_eq_i32 s36, 0x1f00
	s_cselect_b32 s45, s29, s43
	s_cselect_b32 s44, s80, s42
	s_cselect_b32 s43, s27, s64
	s_cselect_b32 s42, s81, s50
	s_add_i32 s50, 0, 0x14000
	v_add_u32_e32 v160, s65, v146
	v_add_u32_e32 v176, s50, v146
	ds_read_b128 v[148:151], v160
	ds_read_b128 v[152:155], v160 offset:1024
	ds_read_b128 v[156:159], v160 offset:2048
	ds_read_b128 v[160:163], v160 offset:3072
	ds_read_b128 v[164:167], v176
	ds_read_b128 v[168:171], v176 offset:1024
	ds_read_b128 v[172:175], v176 offset:2048
	ds_read_b128 v[176:179], v176 offset:3072
	v_lshl_add_u64 v[208:209], v[144:145], 0, s[36:37]
	s_add_i32 m0, s4, 0xc000
	ds_read_b128 v[180:183], v147
	ds_read_b128 v[184:187], v147 offset:1024
	ds_read_b128 v[188:191], v147 offset:2048
	ds_read_b128 v[192:195], v147 offset:3072
	ds_read_b128 v[196:199], v147 offset:4096
	ds_read_b128 v[200:203], v147 offset:5120
	ds_read_b128 v[204:207], v147 offset:6144
	ds_read_b128 v[216:219], v147 offset:7168
	global_load_lds_dwordx4 v[208:209], off
	s_add_i32 m0, s4, 0xe000
	v_lshl_add_u64 v[208:209], v[142:143], 0, s[36:37]
	global_load_lds_dwordx4 v[208:209], off
	s_waitcnt vmcnt(8) lgkmcnt(0)
	s_barrier
	s_setprio 1
	v_mfma_f32_16x16x32_bf16 v[134:137], v[148:151], v[180:183], v[134:137]
	v_mfma_f32_16x16x32_bf16 v[130:133], v[156:159], v[180:183], v[130:133]
	v_mfma_f32_16x16x32_bf16 v[110:113], v[148:151], v[188:191], v[110:113]
	v_mfma_f32_16x16x32_bf16 v[106:109], v[156:159], v[188:191], v[106:109]
	v_mfma_f32_16x16x32_bf16 v[94:97], v[148:151], v[196:199], v[94:97]
	v_mfma_f32_16x16x32_bf16 v[90:93], v[156:159], v[196:199], v[90:93]
	v_mfma_f32_16x16x32_bf16 v[78:81], v[148:151], v[204:207], v[78:81]
	v_mfma_f32_16x16x32_bf16 v[74:77], v[156:159], v[204:207], v[74:77]
	v_mfma_f32_16x16x32_bf16 v[134:137], v[152:155], v[184:187], v[134:137]
	v_mfma_f32_16x16x32_bf16 v[130:133], v[160:163], v[184:187], v[130:133]
	v_mfma_f32_16x16x32_bf16 v[110:113], v[152:155], v[192:195], v[110:113]
	v_mfma_f32_16x16x32_bf16 v[106:109], v[160:163], v[192:195], v[106:109]
	v_mfma_f32_16x16x32_bf16 v[94:97], v[152:155], v[200:203], v[94:97]
	v_mfma_f32_16x16x32_bf16 v[90:93], v[160:163], v[200:203], v[90:93]
	v_mfma_f32_16x16x32_bf16 v[78:81], v[152:155], v[216:219], v[78:81]
	v_mfma_f32_16x16x32_bf16 v[74:77], v[160:163], v[216:219], v[74:77]
	s_setprio 0
	s_setprio 1
	v_mfma_f32_16x16x32_bf16 v[118:121], v[164:167], v[180:183], v[118:121]
	v_mfma_f32_16x16x32_bf16 v[114:117], v[172:175], v[180:183], v[114:117]
	v_mfma_f32_16x16x32_bf16 v[102:105], v[164:167], v[188:191], v[102:105]
	v_mfma_f32_16x16x32_bf16 v[98:101], v[172:175], v[188:191], v[98:101]
	v_mfma_f32_16x16x32_bf16 v[86:89], v[164:167], v[196:199], v[86:89]
	v_mfma_f32_16x16x32_bf16 v[82:85], v[172:175], v[196:199], v[82:85]
	v_mfma_f32_16x16x32_bf16 v[70:73], v[164:167], v[204:207], v[70:73]
	v_mfma_f32_16x16x32_bf16 v[66:69], v[172:175], v[204:207], v[66:69]
	v_mfma_f32_16x16x32_bf16 v[118:121], v[168:171], v[184:187], v[118:121]
	v_mfma_f32_16x16x32_bf16 v[114:117], v[176:179], v[184:187], v[114:117]
	v_mfma_f32_16x16x32_bf16 v[102:105], v[168:171], v[192:195], v[102:105]
	v_mfma_f32_16x16x32_bf16 v[98:101], v[176:179], v[192:195], v[98:101]
	v_mfma_f32_16x16x32_bf16 v[86:89], v[168:171], v[200:203], v[86:89]
	v_mfma_f32_16x16x32_bf16 v[82:85], v[176:179], v[200:203], v[82:85]
	v_mfma_f32_16x16x32_bf16 v[70:73], v[168:171], v[216:219], v[70:73]
	v_mfma_f32_16x16x32_bf16 v[66:69], v[176:179], v[216:219], v[66:69]
	s_setprio 0
	s_barrier
	s_add_i32 s64, s65, s63
	v_lshl_add_u64 v[208:209], s[42:43], 0, v[126:127]
	s_mov_b32 m0, s64
	ds_read_b128 v[180:183], v147 offset:16384
	ds_read_b128 v[184:187], v147 offset:17408
	ds_read_b128 v[188:191], v147 offset:18432
	ds_read_b128 v[192:195], v147 offset:19456
	ds_read_b128 v[196:199], v147 offset:20480
	ds_read_b128 v[200:203], v147 offset:21504
	ds_read_b128 v[204:207], v147 offset:22528
	ds_read_b128 v[216:219], v147 offset:23552
	global_load_lds_dwordx4 v[208:209], off
	s_add_i32 m0, s64, 0x2000
	s_add_u32 s84, s42, 0x100000
	v_lshl_add_u64 v[220:221], s[42:43], 0, v[122:123]
	s_addc_u32 s85, s43, 0
	s_add_i32 s50, s50, s63
	global_load_lds_dwordx4 v[220:221], off
	v_lshl_add_u64 v[222:223], s[84:85], 0, v[126:127]
	s_mov_b32 m0, s50
	v_lshl_add_u64 v[240:241], s[44:45], 0, v[124:125]
	global_load_lds_dwordx4 v[222:223], off
	s_add_i32 m0, s50, 0x2000
	v_lshl_add_u64 v[222:223], s[84:85], 0, v[122:123]
	global_load_lds_dwordx4 v[222:223], off
	s_mov_b32 m0, s4
	v_lshl_add_u64 v[222:223], s[44:45], 0, v[128:129]
	global_load_lds_dwordx4 v[222:223], off
	s_mov_b32 m0, s33
	s_nop 0
	global_load_lds_dwordx4 v[240:241], off
	s_waitcnt vmcnt(8) lgkmcnt(0)
	s_barrier
	s_setprio 1
	v_mfma_f32_16x16x32_bf16 v[62:65], v[148:151], v[180:183], v[62:65]
	v_mfma_f32_16x16x32_bf16 v[58:61], v[156:159], v[180:183], v[58:61]
	v_mfma_f32_16x16x32_bf16 v[46:49], v[148:151], v[188:191], v[46:49]
	v_mfma_f32_16x16x32_bf16 v[42:45], v[156:159], v[188:191], v[42:45]
	v_mfma_f32_16x16x32_bf16 v[30:33], v[148:151], v[196:199], v[30:33]
	v_mfma_f32_16x16x32_bf16 v[26:29], v[156:159], v[196:199], v[26:29]
	v_mfma_f32_16x16x32_bf16 v[14:17], v[148:151], v[204:207], v[14:17]
	v_mfma_f32_16x16x32_bf16 v[10:13], v[156:159], v[204:207], v[10:13]
	v_mfma_f32_16x16x32_bf16 v[62:65], v[152:155], v[184:187], v[62:65]
	v_mfma_f32_16x16x32_bf16 v[58:61], v[160:163], v[184:187], v[58:61]
	v_mfma_f32_16x16x32_bf16 v[46:49], v[152:155], v[192:195], v[46:49]
	v_mfma_f32_16x16x32_bf16 v[42:45], v[160:163], v[192:195], v[42:45]
	v_mfma_f32_16x16x32_bf16 v[30:33], v[152:155], v[200:203], v[30:33]
	v_mfma_f32_16x16x32_bf16 v[26:29], v[160:163], v[200:203], v[26:29]
	v_mfma_f32_16x16x32_bf16 v[14:17], v[152:155], v[216:219], v[14:17]
	v_mfma_f32_16x16x32_bf16 v[10:13], v[160:163], v[216:219], v[10:13]
	s_setprio 0
	s_setprio 1
	v_mfma_f32_16x16x32_bf16 v[54:57], v[164:167], v[180:183], v[54:57]
	v_mfma_f32_16x16x32_bf16 v[50:53], v[172:175], v[180:183], v[50:53]
	v_mfma_f32_16x16x32_bf16 v[38:41], v[164:167], v[188:191], v[38:41]
	v_mfma_f32_16x16x32_bf16 v[34:37], v[172:175], v[188:191], v[34:37]
	v_mfma_f32_16x16x32_bf16 v[22:25], v[164:167], v[196:199], v[22:25]
	v_mfma_f32_16x16x32_bf16 v[18:21], v[172:175], v[196:199], v[18:21]
	v_mfma_f32_16x16x32_bf16 v[6:9], v[164:167], v[204:207], v[6:9]
	v_mfma_f32_16x16x32_bf16 v[2:5], v[172:175], v[204:207], v[2:5]
	v_mfma_f32_16x16x32_bf16 v[54:57], v[168:171], v[184:187], v[54:57]
	v_mfma_f32_16x16x32_bf16 v[50:53], v[176:179], v[184:187], v[50:53]
	v_mfma_f32_16x16x32_bf16 v[38:41], v[168:171], v[192:195], v[38:41]
	v_mfma_f32_16x16x32_bf16 v[34:37], v[176:179], v[192:195], v[34:37]
	v_mfma_f32_16x16x32_bf16 v[22:25], v[168:171], v[200:203], v[22:25]
	v_mfma_f32_16x16x32_bf16 v[18:21], v[176:179], v[200:203], v[18:21]
	v_mfma_f32_16x16x32_bf16 v[6:9], v[168:171], v[216:219], v[6:9]
	v_mfma_f32_16x16x32_bf16 v[2:5], v[176:179], v[216:219], v[2:5]
	s_setprio 0
	s_barrier
	s_add_i32 s50, 0, 0x18000
	s_add_i32 s64, 0, 0x1c000
	v_add_u32_e32 v160, s50, v146
	v_add_u32_e32 v176, s64, v146
	ds_read_b128 v[148:151], v160
	ds_read_b128 v[152:155], v160 offset:1024
	ds_read_b128 v[156:159], v160 offset:2048
	ds_read_b128 v[160:163], v160 offset:3072
	ds_read_b128 v[164:167], v176
	ds_read_b128 v[168:171], v176 offset:1024
	ds_read_b128 v[172:175], v176 offset:2048
	ds_read_b128 v[176:179], v176 offset:3072
	s_add_u32 s44, s44, 0x100000
	s_addc_u32 s45, s45, 0
	s_mov_b32 m0, s70
	v_lshl_add_u64 v[242:243], s[44:45], 0, v[128:129]
	ds_read_b128 v[180:183], v147 offset:32768
	ds_read_b128 v[184:187], v147 offset:33792
	ds_read_b128 v[188:191], v147 offset:34816
	ds_read_b128 v[192:195], v147 offset:35840
	ds_read_b128 v[196:199], v147 offset:36864
	ds_read_b128 v[200:203], v147 offset:37888
	ds_read_b128 v[204:207], v147 offset:38912
	ds_read_b128 v[216:219], v147 offset:39936
	global_load_lds_dwordx4 v[242:243], off
	s_mov_b32 m0, s71
	v_lshl_add_u64 v[242:243], s[44:45], 0, v[124:125]
	global_load_lds_dwordx4 v[242:243], off
	s_waitcnt vmcnt(8) lgkmcnt(0)
	s_barrier
	s_setprio 1
	v_mfma_f32_16x16x32_bf16 v[134:137], v[148:151], v[180:183], v[134:137]
	v_mfma_f32_16x16x32_bf16 v[130:133], v[156:159], v[180:183], v[130:133]
	v_mfma_f32_16x16x32_bf16 v[110:113], v[148:151], v[188:191], v[110:113]
	v_mfma_f32_16x16x32_bf16 v[106:109], v[156:159], v[188:191], v[106:109]
	v_mfma_f32_16x16x32_bf16 v[94:97], v[148:151], v[196:199], v[94:97]
	v_mfma_f32_16x16x32_bf16 v[90:93], v[156:159], v[196:199], v[90:93]
	v_mfma_f32_16x16x32_bf16 v[78:81], v[148:151], v[204:207], v[78:81]
	v_mfma_f32_16x16x32_bf16 v[74:77], v[156:159], v[204:207], v[74:77]
	v_mfma_f32_16x16x32_bf16 v[134:137], v[152:155], v[184:187], v[134:137]
	v_mfma_f32_16x16x32_bf16 v[130:133], v[160:163], v[184:187], v[130:133]
	v_mfma_f32_16x16x32_bf16 v[110:113], v[152:155], v[192:195], v[110:113]
	v_mfma_f32_16x16x32_bf16 v[106:109], v[160:163], v[192:195], v[106:109]
	v_mfma_f32_16x16x32_bf16 v[94:97], v[152:155], v[200:203], v[94:97]
	v_mfma_f32_16x16x32_bf16 v[90:93], v[160:163], v[200:203], v[90:93]
	v_mfma_f32_16x16x32_bf16 v[78:81], v[152:155], v[216:219], v[78:81]
	v_mfma_f32_16x16x32_bf16 v[74:77], v[160:163], v[216:219], v[74:77]
	s_setprio 0
	s_setprio 1
	v_mfma_f32_16x16x32_bf16 v[118:121], v[164:167], v[180:183], v[118:121]
	v_mfma_f32_16x16x32_bf16 v[114:117], v[172:175], v[180:183], v[114:117]
	v_mfma_f32_16x16x32_bf16 v[102:105], v[164:167], v[188:191], v[102:105]
	v_mfma_f32_16x16x32_bf16 v[98:101], v[172:175], v[188:191], v[98:101]
	v_mfma_f32_16x16x32_bf16 v[86:89], v[164:167], v[196:199], v[86:89]
	v_mfma_f32_16x16x32_bf16 v[82:85], v[172:175], v[196:199], v[82:85]
	v_mfma_f32_16x16x32_bf16 v[70:73], v[164:167], v[204:207], v[70:73]
	v_mfma_f32_16x16x32_bf16 v[66:69], v[172:175], v[204:207], v[66:69]
	v_mfma_f32_16x16x32_bf16 v[118:121], v[168:171], v[184:187], v[118:121]
	v_mfma_f32_16x16x32_bf16 v[114:117], v[176:179], v[184:187], v[114:117]
	v_mfma_f32_16x16x32_bf16 v[102:105], v[168:171], v[192:195], v[102:105]
	v_mfma_f32_16x16x32_bf16 v[98:101], v[176:179], v[192:195], v[98:101]
	v_mfma_f32_16x16x32_bf16 v[86:89], v[168:171], v[200:203], v[86:89]
	v_mfma_f32_16x16x32_bf16 v[82:85], v[176:179], v[200:203], v[82:85]
	v_mfma_f32_16x16x32_bf16 v[70:73], v[168:171], v[216:219], v[70:73]
	v_mfma_f32_16x16x32_bf16 v[66:69], v[176:179], v[216:219], v[66:69]
	s_setprio 0
	s_barrier
	s_add_i32 s44, s50, s63
	v_lshl_add_u64 v[208:209], v[208:209], 0, s[56:57]
	s_mov_b32 m0, s44
	ds_read_b128 v[180:183], v147 offset:49152
	ds_read_b128 v[184:187], v147 offset:50176
	ds_read_b128 v[188:191], v147 offset:51200
	ds_read_b128 v[192:195], v147 offset:52224
	ds_read_b128 v[196:199], v147 offset:53248
	ds_read_b128 v[200:203], v147 offset:54272
	ds_read_b128 v[204:207], v147 offset:55296
	ds_read_b128 v[216:219], v147 offset:56320
	global_load_lds_dwordx4 v[208:209], off
	s_add_i32 m0, s44, 0x2000
	s_add_u32 s42, s42, 0x100080
	v_lshl_add_u64 v[208:209], v[220:221], 0, s[56:57]
	s_addc_u32 s43, s43, 0
	s_add_i32 s44, s64, s63
	global_load_lds_dwordx4 v[208:209], off
	s_mov_b32 m0, s44
	v_lshl_add_u64 v[208:209], s[42:43], 0, v[126:127]
	global_load_lds_dwordx4 v[208:209], off
	s_add_i32 m0, s44, 0x2000
	v_lshl_add_u64 v[208:209], s[42:43], 0, v[122:123]
	global_load_lds_dwordx4 v[208:209], off
	s_mov_b32 m0, s76
	v_lshl_add_u64 v[208:209], v[222:223], 0, s[56:57]
	global_load_lds_dwordx4 v[208:209], off
	s_mov_b32 m0, s77
	v_lshl_add_u64 v[208:209], v[240:241], 0, s[56:57]
	global_load_lds_dwordx4 v[208:209], off
	s_waitcnt vmcnt(8) lgkmcnt(0)
	s_barrier
	s_setprio 1
	v_mfma_f32_16x16x32_bf16 v[62:65], v[148:151], v[180:183], v[62:65]
	v_mfma_f32_16x16x32_bf16 v[58:61], v[156:159], v[180:183], v[58:61]
	v_mfma_f32_16x16x32_bf16 v[46:49], v[148:151], v[188:191], v[46:49]
	v_mfma_f32_16x16x32_bf16 v[42:45], v[156:159], v[188:191], v[42:45]
	v_mfma_f32_16x16x32_bf16 v[30:33], v[148:151], v[196:199], v[30:33]
	v_mfma_f32_16x16x32_bf16 v[26:29], v[156:159], v[196:199], v[26:29]
	v_mfma_f32_16x16x32_bf16 v[14:17], v[148:151], v[204:207], v[14:17]
	v_mfma_f32_16x16x32_bf16 v[10:13], v[156:159], v[204:207], v[10:13]
	v_mfma_f32_16x16x32_bf16 v[62:65], v[152:155], v[184:187], v[62:65]
	v_mfma_f32_16x16x32_bf16 v[58:61], v[160:163], v[184:187], v[58:61]
	v_mfma_f32_16x16x32_bf16 v[46:49], v[152:155], v[192:195], v[46:49]
	v_mfma_f32_16x16x32_bf16 v[42:45], v[160:163], v[192:195], v[42:45]
	v_mfma_f32_16x16x32_bf16 v[30:33], v[152:155], v[200:203], v[30:33]
	v_mfma_f32_16x16x32_bf16 v[26:29], v[160:163], v[200:203], v[26:29]
	v_mfma_f32_16x16x32_bf16 v[14:17], v[152:155], v[216:219], v[14:17]
	v_mfma_f32_16x16x32_bf16 v[10:13], v[160:163], v[216:219], v[10:13]
	s_setprio 0
	s_setprio 1
	v_mfma_f32_16x16x32_bf16 v[54:57], v[164:167], v[180:183], v[54:57]
	v_mfma_f32_16x16x32_bf16 v[50:53], v[172:175], v[180:183], v[50:53]
	v_mfma_f32_16x16x32_bf16 v[38:41], v[164:167], v[188:191], v[38:41]
	v_mfma_f32_16x16x32_bf16 v[34:37], v[172:175], v[188:191], v[34:37]
	v_mfma_f32_16x16x32_bf16 v[22:25], v[164:167], v[196:199], v[22:25]
	v_mfma_f32_16x16x32_bf16 v[18:21], v[172:175], v[196:199], v[18:21]
	v_mfma_f32_16x16x32_bf16 v[6:9], v[164:167], v[204:207], v[6:9]
	v_mfma_f32_16x16x32_bf16 v[2:5], v[172:175], v[204:207], v[2:5]
	v_mfma_f32_16x16x32_bf16 v[54:57], v[168:171], v[184:187], v[54:57]
	v_mfma_f32_16x16x32_bf16 v[50:53], v[176:179], v[184:187], v[50:53]
	v_mfma_f32_16x16x32_bf16 v[38:41], v[168:171], v[192:195], v[38:41]
	v_mfma_f32_16x16x32_bf16 v[34:37], v[176:179], v[192:195], v[34:37]
	v_mfma_f32_16x16x32_bf16 v[22:25], v[168:171], v[200:203], v[22:25]
	v_mfma_f32_16x16x32_bf16 v[18:21], v[176:179], v[200:203], v[18:21]
	v_mfma_f32_16x16x32_bf16 v[6:9], v[168:171], v[216:219], v[6:9]
	v_mfma_f32_16x16x32_bf16 v[2:5], v[176:179], v[216:219], v[2:5]
	s_setprio 0
	s_barrier
	s_add_i32 s82, s82, 2
	s_add_u32 s36, s36, 0x100
	s_addc_u32 s37, s37, 0
	s_cmp_gt_u32 s82, 61
	s_cbranch_scc0 .LBB0_2982
	s_add_u32 s36, s59, 0xffffff00
	s_addc_u32 s37, s79, -1
	s_andn2_b64 vcc, exec, s[40:41]
	s_cbranch_vccnz .LBB0_2985
	v_mov_b32_e32 v2, 0
	s_mov_b32 s20, s26
	s_mov_b32 s78, s28
	s_mov_b64 s[24:25], s[34:35]
	s_mov_b32 s68, s58
	v_mov_b32_e32 v3, v2
	v_mov_b32_e32 v4, v2
	v_mov_b32_e32 v5, v2
	v_mov_b32_e32 v6, v2
	v_mov_b32_e32 v7, v2
	v_mov_b32_e32 v8, v2
	v_mov_b32_e32 v9, v2
	v_mov_b32_e32 v18, v2
	v_mov_b32_e32 v19, v2
	v_mov_b32_e32 v20, v2
	v_mov_b32_e32 v21, v2
	v_mov_b32_e32 v22, v2
	v_mov_b32_e32 v23, v2
	v_mov_b32_e32 v24, v2
	v_mov_b32_e32 v25, v2
	v_mov_b32_e32 v34, v2
	v_mov_b32_e32 v35, v2
	v_mov_b32_e32 v36, v2
	v_mov_b32_e32 v37, v2
	v_mov_b32_e32 v38, v2
	v_mov_b32_e32 v39, v2
	v_mov_b32_e32 v40, v2
	v_mov_b32_e32 v41, v2
	v_mov_b32_e32 v50, v2
	v_mov_b32_e32 v51, v2
	v_mov_b32_e32 v52, v2
	v_mov_b32_e32 v53, v2
	v_mov_b32_e32 v54, v2
	v_mov_b32_e32 v55, v2
	v_mov_b32_e32 v56, v2
	v_mov_b32_e32 v57, v2
	v_mov_b32_e32 v10, v2
	v_mov_b32_e32 v11, v2
	v_mov_b32_e32 v12, v2
	v_mov_b32_e32 v13, v2
	v_mov_b32_e32 v14, v2
	v_mov_b32_e32 v15, v2
	v_mov_b32_e32 v16, v2
	v_mov_b32_e32 v17, v2
	v_mov_b32_e32 v26, v2
	v_mov_b32_e32 v27, v2
	v_mov_b32_e32 v28, v2
	v_mov_b32_e32 v29, v2
	v_mov_b32_e32 v30, v2
	v_mov_b32_e32 v31, v2
	v_mov_b32_e32 v32, v2
	v_mov_b32_e32 v33, v2
	v_mov_b32_e32 v42, v2
	v_mov_b32_e32 v43, v2
	v_mov_b32_e32 v44, v2
	v_mov_b32_e32 v45, v2
	v_mov_b32_e32 v46, v2
	v_mov_b32_e32 v47, v2
	v_mov_b32_e32 v48, v2
	v_mov_b32_e32 v49, v2
	v_mov_b32_e32 v58, v2
	v_mov_b32_e32 v59, v2
	v_mov_b32_e32 v60, v2
	v_mov_b32_e32 v61, v2
	v_mov_b32_e32 v62, v2
	v_mov_b32_e32 v63, v2
	v_mov_b32_e32 v64, v2
	v_mov_b32_e32 v65, v2
	v_mov_b32_e32 v66, v2
	v_mov_b32_e32 v67, v2
	v_mov_b32_e32 v68, v2
	v_mov_b32_e32 v69, v2
	v_mov_b32_e32 v70, v2
	v_mov_b32_e32 v71, v2
	v_mov_b32_e32 v72, v2
	v_mov_b32_e32 v73, v2
	v_mov_b32_e32 v82, v2
	v_mov_b32_e32 v83, v2
	v_mov_b32_e32 v84, v2
	v_mov_b32_e32 v85, v2
	v_mov_b32_e32 v86, v2
	v_mov_b32_e32 v87, v2
	v_mov_b32_e32 v88, v2
	v_mov_b32_e32 v89, v2
	v_mov_b32_e32 v98, v2
	v_mov_b32_e32 v99, v2
	v_mov_b32_e32 v100, v2
	v_mov_b32_e32 v101, v2
	v_mov_b32_e32 v102, v2
	v_mov_b32_e32 v103, v2
	v_mov_b32_e32 v104, v2
	v_mov_b32_e32 v105, v2
	v_mov_b32_e32 v114, v2
	v_mov_b32_e32 v115, v2
	v_mov_b32_e32 v116, v2
	v_mov_b32_e32 v117, v2
	v_mov_b32_e32 v118, v2
	v_mov_b32_e32 v119, v2
	v_mov_b32_e32 v120, v2
	v_mov_b32_e32 v121, v2
	v_mov_b32_e32 v74, v2
	v_mov_b32_e32 v75, v2
	v_mov_b32_e32 v76, v2
	v_mov_b32_e32 v77, v2
	v_mov_b32_e32 v78, v2
	v_mov_b32_e32 v79, v2
	v_mov_b32_e32 v80, v2
	v_mov_b32_e32 v81, v2
	v_mov_b32_e32 v90, v2
	v_mov_b32_e32 v91, v2
	v_mov_b32_e32 v92, v2
	v_mov_b32_e32 v93, v2
	v_mov_b32_e32 v94, v2
	v_mov_b32_e32 v95, v2
	v_mov_b32_e32 v96, v2
	v_mov_b32_e32 v97, v2
	v_mov_b32_e32 v106, v2
	v_mov_b32_e32 v107, v2
	v_mov_b32_e32 v108, v2
	v_mov_b32_e32 v109, v2
	v_mov_b32_e32 v110, v2
	v_mov_b32_e32 v111, v2
	v_mov_b32_e32 v112, v2
	v_mov_b32_e32 v113, v2
	v_mov_b32_e32 v130, v2
	v_mov_b32_e32 v131, v2
	v_mov_b32_e32 v132, v2
	v_mov_b32_e32 v133, v2
	v_mov_b32_e32 v134, v2
	v_mov_b32_e32 v135, v2
	v_mov_b32_e32 v136, v2
	v_mov_b32_e32 v137, v2
	s_andn2_b64 vcc, exec, s[38:39]
	s_cbranch_vccnz .LBB0_2986
	s_branch .LBB0_2987
